# static s_setprio 1 for waves 4-7 set once at kernel start; all per-segment s_setprio flips removed
# baseline (speedup 1.0000x reference)
; #define LAS __attribute__((address_space(3)))
; __device__ __forceinline__ int lane_id_v() { int l; asm volatile("v_mbcnt_lo_u32_b32 %0, -1, 0\n\tv_mbcnt_hi_u32_b32 %0, -1, %0" : "=v"(l)); return l; }
; __global__ void __launch_bounds__(NTHR, 2) mega_fwd(Args args) {
;     ...
;     F.wave = __builtin_amdgcn_readfirstlane((int)threadIdx.x >> 6); F.lane = lane_id_v(); F.tid = F.wave * 64 + F.lane;
;     F.G = gridDim.x; { const int bx = blockIdx.x; const int vcu = (F.G % 8 == 0) ? (bx % 8) * (F.G / 8) + bx / 8 : bx; F.gw = vcu * NWAVES + F.wave; F.NGW = F.G * NWAVES; }
;     const int gw0 = F.gw;
;     F.ws = args.ws; F.ctl = (gu32*)(args.ws + WS_CTL); F.out = args.out;
;     F.in = args.in;
;     for (int u = F.tid; u < (LDS_BYTES - MISC_OFF) / 4; u += NTHR) ((LAS unsigned*)(F.lds + MISC_OFF))[u] = 0u;
.LBB0_2:
	s_lshr_b32 s0, s3, 6
	v_writelane_b32 v251, s0, 2
	s_cmp_lt_u32 s0, 4
	s_cbranch_scc1 .Lprio_skip
	s_setprio 1
.Lprio_skip:
	s_load_dwordx2 s[0:1], s[92:93], 0xe0
	s_and_b32 s87, s3, 0xffffffc0
	v_add_u32_e32 v1, s87, v64
	s_movk_i32 s4, 0x1000
	v_cmp_gt_i32_e32 vcc, s4, v1
	s_and_saveexec_b64 s[4:5], vcc
	s_cbranch_execz .LBB0_5
	v_readlane_b32 s6, v251, 2
	s_lshl_b32 s6, s6, 8
	s_add_i32 s6, s6, 0
	v_lshl_add_u32 v2, v64, 2, s6
	v_add_u32_e32 v1, 0xfffffe00, v1
	v_add_u32_e32 v2, 0x20000, v2
	s_mov_b64 s[6:7], 0
	v_mov_b32_e32 v3, 0
	s_movk_i32 s8, 0xdff

; #define PG8_STAGE(bufoff, gbase, voff) do { _Pragma("unroll") for (int _i = 0; _i < 2; ++_i) \
;         __builtin_amdgcn_global_load_lds((const unsigned*)((const char*)(gbase) + (voff)[_i]), (LAS unsigned*)(lds + (bufoff) + ldsw + _i * 8192), 16, 0, 0); } while (0)
; #define PG8_STAGE_A(bufoff, h, kp, nx) do { if constexpr (GATHER) { const unsigned _p = (nx) ? ng[h] : cg[h]; unsigned _v[2]; _v[0] = (_p & 0xffffu) * lda + CA2[0]; _v[1] = (_p >> 16) * lda + CA2[1]; PG8_STAGE(bufoff, kp, _v); } \
;         else { PG8_STAGE(bufoff, (kp) + (h) * hstepA, voffA); } } while (0)
; #define PG8_LDA(dst, b, h) do { _Pragma("unroll") for (int m = 0; m < 4; ++m) _Pragma("unroll") for (int k = 0; k < 2; ++k) dst[m][k] = *(const LAS bf16x8*)(lds + PG8_SA(b, h) + aoff + m * 2048 + k * 1024); } while (0)
; #define PG8_LDB(dst, b, h) do { _Pragma("unroll") for (int n = 0; n < 2; ++n) _Pragma("unroll") for (int k = 0; k < 2; ++k) dst[n][k] = *(const LAS bf16x8*)(lds + PG8_SB(b, h) + boff + n * 2048 + k * 1024); } while (0)
; #define PG8_MMA(ai, bj, At, Bt) do { __builtin_amdgcn_s_setprio(1); _Pragma("unroll") for (int m = 0; m < 4; ++m) _Pragma("unroll") for (int n = 0; n < 2; ++n) _Pragma("unroll") for (int k = 0; k < 2; ++k) \
;         acc[ai][bj][m][n] = __builtin_amdgcn_mfma_f32_16x16x32_bf16(Bt[n][k], At[m][k], acc[ai][bj][m][n], 0, 0, 0); __builtin_amdgcn_s_setprio(0); } while (0)
; #define PG8_WAIT_V(n) asm volatile("s_waitcnt vmcnt(" #n ")" ::: "memory")
; #define PG8_WAIT_L(n) asm volatile("s_waitcnt lgkmcnt(" #n ")" ::: "memory")
; #define PG8_BAR __builtin_amdgcn_s_barrier()
; #define PG8_SCHED __builtin_amdgcn_sched_barrier(0)
;     ...
;             PG8_LDB(B0, 0, 0); PG8_LDB(B1, 0, 1); PG8_SCHED; PG8_LDA(At, 0, 0); PG8_STAGE_A(PG8_SA(1, 1), 1, a1, false);
;             PG8_WAIT_V(8); PG8_WAIT_L(0); PG8_BAR; if (cur.amask & 1) { PG8_MMA(0, 0, At, B0); PG8_MMA(0, 1, At, B1); } PG8_BAR; PG8_SCHED;
;             PG8_LDA(At, 0, 1); PG8_STAGE(PG8_SB(0, 0), b2, voffB); PG8_STAGE(PG8_SB(0, 1), b2 + hstepB, voffB); PG8_STAGE_A(PG8_SA(0, 0), 0, a2, last);
;             PG8_WAIT_V(8); PG8_WAIT_L(0); PG8_BAR; if (cur.amask & 2) { PG8_MMA(1, 0, At, B0); PG8_MMA(1, 1, At, B1); } PG8_BAR; PG8_SCHED;
.LBB0_544:
	s_add_i32 s34, s31, 2
	s_add_u32 s54, s76, 0xfff80080
	s_addc_u32 s55, s77, -1
	s_add_i32 s82, 0, 0x10000
	s_cmp_eq_u32 s28, s31
	s_cselect_b32 s87, s24, s55
	s_cselect_b32 s86, s25, s54
	v_add_u32_e32 v142, s82, v146
	s_cselect_b32 s81, s26, s30
	s_cselect_b32 s80, s27, s29
	s_add_i32 s31, 0, 0x14000
	ds_read_b128 v[150:153], v142
	ds_read_b128 v[154:157], v142 offset:1024
	ds_read_b128 v[158:161], v142 offset:2048
	ds_read_b128 v[162:165], v142 offset:3072
	v_add_u32_e32 v142, s31, v146
	ds_read_b128 v[166:169], v142
	ds_read_b128 v[170:173], v142 offset:1024
	ds_read_b128 v[174:177], v142 offset:2048
	ds_read_b128 v[178:181], v142 offset:3072
	v_lshl_add_u64 v[142:143], s[76:77], 0, v[138:139]
	s_add_i32 m0, s7, 0xc000
	ds_read_b128 v[182:185], v147
	ds_read_b128 v[186:189], v147 offset:1024
	ds_read_b128 v[190:193], v147 offset:2048
	ds_read_b128 v[194:197], v147 offset:3072
	ds_read_b128 v[198:201], v147 offset:4096
	ds_read_b128 v[202:205], v147 offset:5120
	ds_read_b128 v[206:209], v147 offset:6144
	ds_read_b128 v[210:213], v147 offset:7168
	global_load_lds_dwordx4 v[142:143], off
	v_lshl_add_u64 v[142:143], s[76:77], 0, v[140:141]
	s_add_i32 m0, s7, 0xe000
	s_nop 0
	global_load_lds_dwordx4 v[142:143], off
	s_waitcnt vmcnt(8)
	s_waitcnt lgkmcnt(0)
	s_barrier
	s_waitcnt lgkmcnt(0)
	v_mfma_f32_16x16x32_bf16 v[114:117], v[150:153], v[182:185], v[114:117]
	v_mfma_f32_16x16x32_bf16 v[118:121], v[158:161], v[182:185], v[118:121]
	v_mfma_f32_16x16x32_bf16 v[98:101], v[150:153], v[190:193], v[98:101]
	v_mfma_f32_16x16x32_bf16 v[102:105], v[158:161], v[190:193], v[102:105]
	v_mfma_f32_16x16x32_bf16 v[82:85], v[150:153], v[198:201], v[82:85]
	v_mfma_f32_16x16x32_bf16 v[86:89], v[158:161], v[198:201], v[86:89]
	v_mfma_f32_16x16x32_bf16 v[66:69], v[150:153], v[206:209], v[66:69]
	v_mfma_f32_16x16x32_bf16 v[70:73], v[158:161], v[206:209], v[70:73]
	v_mfma_f32_16x16x32_bf16 v[114:117], v[154:157], v[186:189], v[114:117]
	v_mfma_f32_16x16x32_bf16 v[118:121], v[162:165], v[186:189], v[118:121]
	v_mfma_f32_16x16x32_bf16 v[98:101], v[154:157], v[194:197], v[98:101]
	v_mfma_f32_16x16x32_bf16 v[102:105], v[162:165], v[194:197], v[102:105]
	v_mfma_f32_16x16x32_bf16 v[82:85], v[154:157], v[202:205], v[82:85]
	v_mfma_f32_16x16x32_bf16 v[86:89], v[162:165], v[202:205], v[86:89]
	v_mfma_f32_16x16x32_bf16 v[66:69], v[154:157], v[210:213], v[66:69]
	v_mfma_f32_16x16x32_bf16 v[70:73], v[162:165], v[210:213], v[70:73]
	v_mfma_f32_16x16x32_bf16 v[122:125], v[166:169], v[182:185], v[122:125]
	v_mfma_f32_16x16x32_bf16 v[126:129], v[174:177], v[182:185], v[126:129]
	v_mfma_f32_16x16x32_bf16 v[106:109], v[166:169], v[190:193], v[106:109]
	v_mfma_f32_16x16x32_bf16 v[110:113], v[174:177], v[190:193], v[110:113]
	v_mfma_f32_16x16x32_bf16 v[90:93], v[166:169], v[198:201], v[90:93]
	v_mfma_f32_16x16x32_bf16 v[94:97], v[174:177], v[198:201], v[94:97]
	v_mfma_f32_16x16x32_bf16 v[74:77], v[166:169], v[206:209], v[74:77]
	v_mfma_f32_16x16x32_bf16 v[78:81], v[174:177], v[206:209], v[78:81]
	v_mfma_f32_16x16x32_bf16 v[122:125], v[170:173], v[186:189], v[122:125]
	v_mfma_f32_16x16x32_bf16 v[126:129], v[178:181], v[186:189], v[126:129]
	v_mfma_f32_16x16x32_bf16 v[106:109], v[170:173], v[194:197], v[106:109]
	v_mfma_f32_16x16x32_bf16 v[110:113], v[178:181], v[194:197], v[110:113]
	v_mfma_f32_16x16x32_bf16 v[90:93], v[170:173], v[202:205], v[90:93]
	v_mfma_f32_16x16x32_bf16 v[94:97], v[178:181], v[202:205], v[94:97]
	v_mfma_f32_16x16x32_bf16 v[74:77], v[170:173], v[210:213], v[74:77]
	v_mfma_f32_16x16x32_bf16 v[78:81], v[178:181], v[210:213], v[78:81]
	s_barrier
	s_add_i32 s54, s82, s43
	v_lshl_add_u64 v[142:143], s[80:81], 0, v[0:1]
	s_mov_b32 m0, s54
	ds_read_b128 v[182:185], v147 offset:16384
	ds_read_b128 v[186:189], v147 offset:17408
	ds_read_b128 v[190:193], v147 offset:18432
	ds_read_b128 v[194:197], v147 offset:19456
	ds_read_b128 v[198:201], v147 offset:20480
	ds_read_b128 v[202:205], v147 offset:21504
	ds_read_b128 v[206:209], v147 offset:22528
	ds_read_b128 v[210:213], v147 offset:23552
	global_load_lds_dwordx4 v[142:143], off
	s_add_i32 m0, s54, 0x2000
	s_add_u32 s54, s80, 0x80000
	v_lshl_add_u64 v[214:215], s[80:81], 0, v[134:135]
	s_addc_u32 s55, s81, 0
	s_add_i32 s31, s31, s43
	global_load_lds_dwordx4 v[214:215], off
	v_lshl_add_u64 v[224:225], s[54:55], 0, v[0:1]
	s_mov_b32 m0, s31
	v_lshl_add_u64 v[226:227], s[86:87], 0, v[132:133]
	global_load_lds_dwordx4 v[224:225], off
	v_lshl_add_u64 v[224:225], s[54:55], 0, v[134:135]
	s_add_i32 m0, s31, 0x2000
	s_nop 0
	global_load_lds_dwordx4 v[224:225], off
	v_lshl_add_u64 v[224:225], s[86:87], 0, v[130:131]
	s_mov_b32 m0, s7
	s_nop 0
	global_load_lds_dwordx4 v[224:225], off
	s_mov_b32 m0, s8
	s_nop 0
	global_load_lds_dwordx4 v[226:227], off
	s_waitcnt vmcnt(8)
	s_waitcnt lgkmcnt(0)
	s_barrier
; #define PG8_STAGE_A(bufoff, h, kp, nx) do { if constexpr (GATHER) { const unsigned _p = (nx) ? ng[h] : cg[h]; unsigned _v[2]; _v[0] = (_p & 0xffffu) * lda + CA2[0]; _v[1] = (_p >> 16) * lda + CA2[1]; PG8_STAGE(bufoff, kp, _v); } \
;         else { PG8_STAGE(bufoff, (kp) + (h) * hstepA, voffA); } } while (0)
; #define PG8_LDA(dst, b, h) do { _Pragma("unroll") for (int m = 0; m < 4; ++m) _Pragma("unroll") for (int k = 0; k < 2; ++k) dst[m][k] = *(const LAS bf16x8*)(lds + PG8_SA(b, h) + aoff + m * 2048 + k * 1024); } while (0)
; #define PG8_LDB(dst, b, h) do { _Pragma("unroll") for (int n = 0; n < 2; ++n) _Pragma("unroll") for (int k = 0; k < 2; ++k) dst[n][k] = *(const LAS bf16x8*)(lds + PG8_SB(b, h) + boff + n * 2048 + k * 1024); } while (0)
; #define PG8_MMA(ai, bj, At, Bt) do { __builtin_amdgcn_s_setprio(1); _Pragma("unroll") for (int m = 0; m < 4; ++m) _Pragma("unroll") for (int n = 0; n < 2; ++n) _Pragma("unroll") for (int k = 0; k < 2; ++k) \
;         acc[ai][bj][m][n] = __builtin_amdgcn_mfma_f32_16x16x32_bf16(Bt[n][k], At[m][k], acc[ai][bj][m][n], 0, 0, 0); __builtin_amdgcn_s_setprio(0); } while (0)
; #define PG8_WAIT_V(n) asm volatile("s_waitcnt vmcnt(" #n ")" ::: "memory")
; #define PG8_WAIT_L(n) asm volatile("s_waitcnt lgkmcnt(" #n ")" ::: "memory")
; #define PG8_BAR __builtin_amdgcn_s_barrier()
; #define PG8_SCHED __builtin_amdgcn_sched_barrier(0)
;     ...
;             PG8_WAIT_V(8); PG8_WAIT_L(0); PG8_BAR; if (cur.amask & 2) { PG8_MMA(1, 0, At, B0); PG8_MMA(1, 1, At, B1); } PG8_BAR; PG8_SCHED;
;             PG8_LDB(B0, 1, 0); PG8_LDB(B1, 1, 1); PG8_SCHED; PG8_LDA(At, 1, 0); PG8_STAGE_A(PG8_SA(0, 1), 1, a2, last);
;             PG8_WAIT_V(8); PG8_WAIT_L(0); PG8_BAR; if (cur.amask & 1) { PG8_MMA(0, 0, At, B0); PG8_MMA(0, 1, At, B1); } PG8_BAR; PG8_SCHED;
	s_waitcnt lgkmcnt(0)
	v_mfma_f32_16x16x32_bf16 v[50:53], v[150:153], v[182:185], v[50:53]
	v_mfma_f32_16x16x32_bf16 v[54:57], v[158:161], v[182:185], v[54:57]
	v_mfma_f32_16x16x32_bf16 v[34:37], v[150:153], v[190:193], v[34:37]
	v_mfma_f32_16x16x32_bf16 v[38:41], v[158:161], v[190:193], v[38:41]
	v_mfma_f32_16x16x32_bf16 v[18:21], v[150:153], v[198:201], v[18:21]
	v_mfma_f32_16x16x32_bf16 v[22:25], v[158:161], v[198:201], v[22:25]
	v_mfma_f32_16x16x32_bf16 v[2:5], v[150:153], v[206:209], v[2:5]
	v_mfma_f32_16x16x32_bf16 v[6:9], v[158:161], v[206:209], v[6:9]
	v_mfma_f32_16x16x32_bf16 v[50:53], v[154:157], v[186:189], v[50:53]
	v_mfma_f32_16x16x32_bf16 v[54:57], v[162:165], v[186:189], v[54:57]
	v_mfma_f32_16x16x32_bf16 v[34:37], v[154:157], v[194:197], v[34:37]
	v_mfma_f32_16x16x32_bf16 v[38:41], v[162:165], v[194:197], v[38:41]
	v_mfma_f32_16x16x32_bf16 v[18:21], v[154:157], v[202:205], v[18:21]
	v_mfma_f32_16x16x32_bf16 v[22:25], v[162:165], v[202:205], v[22:25]
	v_mfma_f32_16x16x32_bf16 v[2:5], v[154:157], v[210:213], v[2:5]
	v_mfma_f32_16x16x32_bf16 v[6:9], v[162:165], v[210:213], v[6:9]
	v_mfma_f32_16x16x32_bf16 v[58:61], v[166:169], v[182:185], v[58:61]
	v_mfma_f32_16x16x32_bf16 v[62:65], v[174:177], v[182:185], v[62:65]
	v_mfma_f32_16x16x32_bf16 v[42:45], v[166:169], v[190:193], v[42:45]
	v_mfma_f32_16x16x32_bf16 v[46:49], v[174:177], v[190:193], v[46:49]
	v_mfma_f32_16x16x32_bf16 v[26:29], v[166:169], v[198:201], v[26:29]
	v_mfma_f32_16x16x32_bf16 v[30:33], v[174:177], v[198:201], v[30:33]
	v_mfma_f32_16x16x32_bf16 v[10:13], v[166:169], v[206:209], v[10:13]
	v_mfma_f32_16x16x32_bf16 v[14:17], v[174:177], v[206:209], v[14:17]
	v_mfma_f32_16x16x32_bf16 v[58:61], v[170:173], v[186:189], v[58:61]
	v_mfma_f32_16x16x32_bf16 v[62:65], v[178:181], v[186:189], v[62:65]
	v_mfma_f32_16x16x32_bf16 v[42:45], v[170:173], v[194:197], v[42:45]
	v_mfma_f32_16x16x32_bf16 v[46:49], v[178:181], v[194:197], v[46:49]
	v_mfma_f32_16x16x32_bf16 v[26:29], v[170:173], v[202:205], v[26:29]
	v_mfma_f32_16x16x32_bf16 v[30:33], v[178:181], v[202:205], v[30:33]
	v_mfma_f32_16x16x32_bf16 v[10:13], v[170:173], v[210:213], v[10:13]
	v_mfma_f32_16x16x32_bf16 v[14:17], v[178:181], v[210:213], v[14:17]
	s_barrier
	s_add_i32 s31, 0, 0x18000
	v_add_u32_e32 v148, s31, v146
	s_add_i32 s82, 0, 0x1c000
	ds_read_b128 v[150:153], v148
	ds_read_b128 v[154:157], v148 offset:1024
	ds_read_b128 v[158:161], v148 offset:2048
	ds_read_b128 v[162:165], v148 offset:3072
	v_add_u32_e32 v148, s82, v146
	ds_read_b128 v[166:169], v148
	ds_read_b128 v[170:173], v148 offset:1024
	ds_read_b128 v[174:177], v148 offset:2048
	ds_read_b128 v[178:181], v148 offset:3072
	s_add_u32 s54, s86, 0x80000
	s_addc_u32 s55, s87, 0
	s_mov_b32 m0, s9
	v_lshl_add_u64 v[228:229], s[54:55], 0, v[130:131]
	ds_read_b128 v[182:185], v147 offset:32768
	ds_read_b128 v[186:189], v147 offset:33792
	ds_read_b128 v[190:193], v147 offset:34816
	ds_read_b128 v[194:197], v147 offset:35840
	ds_read_b128 v[198:201], v147 offset:36864
	ds_read_b128 v[202:205], v147 offset:37888
	ds_read_b128 v[206:209], v147 offset:38912
	ds_read_b128 v[210:213], v147 offset:39936
	global_load_lds_dwordx4 v[228:229], off
	v_lshl_add_u64 v[228:229], s[54:55], 0, v[132:133]
	s_mov_b32 m0, s10
	s_nop 0
	global_load_lds_dwordx4 v[228:229], off
	s_waitcnt vmcnt(8)
	s_waitcnt lgkmcnt(0)
	s_barrier
	s_waitcnt lgkmcnt(0)
	v_mfma_f32_16x16x32_bf16 v[114:117], v[150:153], v[182:185], v[114:117]
	v_mfma_f32_16x16x32_bf16 v[118:121], v[158:161], v[182:185], v[118:121]
	v_mfma_f32_16x16x32_bf16 v[98:101], v[150:153], v[190:193], v[98:101]
	v_mfma_f32_16x16x32_bf16 v[102:105], v[158:161], v[190:193], v[102:105]
	v_mfma_f32_16x16x32_bf16 v[82:85], v[150:153], v[198:201], v[82:85]
	v_mfma_f32_16x16x32_bf16 v[86:89], v[158:161], v[198:201], v[86:89]
	v_mfma_f32_16x16x32_bf16 v[66:69], v[150:153], v[206:209], v[66:69]
	v_mfma_f32_16x16x32_bf16 v[70:73], v[158:161], v[206:209], v[70:73]
	v_mfma_f32_16x16x32_bf16 v[114:117], v[154:157], v[186:189], v[114:117]
	v_mfma_f32_16x16x32_bf16 v[118:121], v[162:165], v[186:189], v[118:121]
	v_mfma_f32_16x16x32_bf16 v[98:101], v[154:157], v[194:197], v[98:101]
	v_mfma_f32_16x16x32_bf16 v[102:105], v[162:165], v[194:197], v[102:105]
	v_mfma_f32_16x16x32_bf16 v[82:85], v[154:157], v[202:205], v[82:85]
	v_mfma_f32_16x16x32_bf16 v[86:89], v[162:165], v[202:205], v[86:89]
	v_mfma_f32_16x16x32_bf16 v[66:69], v[154:157], v[210:213], v[66:69]
	v_mfma_f32_16x16x32_bf16 v[70:73], v[162:165], v[210:213], v[70:73]
	v_mfma_f32_16x16x32_bf16 v[122:125], v[166:169], v[182:185], v[122:125]
	v_mfma_f32_16x16x32_bf16 v[126:129], v[174:177], v[182:185], v[126:129]
	v_mfma_f32_16x16x32_bf16 v[106:109], v[166:169], v[190:193], v[106:109]
	v_mfma_f32_16x16x32_bf16 v[110:113], v[174:177], v[190:193], v[110:113]
	v_mfma_f32_16x16x32_bf16 v[90:93], v[166:169], v[198:201], v[90:93]
	v_mfma_f32_16x16x32_bf16 v[94:97], v[174:177], v[198:201], v[94:97]
	v_mfma_f32_16x16x32_bf16 v[74:77], v[166:169], v[206:209], v[74:77]
	v_mfma_f32_16x16x32_bf16 v[78:81], v[174:177], v[206:209], v[78:81]
	v_mfma_f32_16x16x32_bf16 v[122:125], v[170:173], v[186:189], v[122:125]
	v_mfma_f32_16x16x32_bf16 v[126:129], v[178:181], v[186:189], v[126:129]
	v_mfma_f32_16x16x32_bf16 v[106:109], v[170:173], v[194:197], v[106:109]
	v_mfma_f32_16x16x32_bf16 v[110:113], v[178:181], v[194:197], v[110:113]
	v_mfma_f32_16x16x32_bf16 v[90:93], v[170:173], v[202:205], v[90:93]
	v_mfma_f32_16x16x32_bf16 v[94:97], v[178:181], v[202:205], v[94:97]
	v_mfma_f32_16x16x32_bf16 v[74:77], v[170:173], v[210:213], v[74:77]
	v_mfma_f32_16x16x32_bf16 v[78:81], v[178:181], v[210:213], v[78:81]
	s_barrier
; #define PG8_STAGE(bufoff, gbase, voff) do { _Pragma("unroll") for (int _i = 0; _i < 2; ++_i) \
;         __builtin_amdgcn_global_load_lds((const unsigned*)((const char*)(gbase) + (voff)[_i]), (LAS unsigned*)(lds + (bufoff) + ldsw + _i * 8192), 16, 0, 0); } while (0)
; #define PG8_STAGE_A(bufoff, h, kp, nx) do { if constexpr (GATHER) { const unsigned _p = (nx) ? ng[h] : cg[h]; unsigned _v[2]; _v[0] = (_p & 0xffffu) * lda + CA2[0]; _v[1] = (_p >> 16) * lda + CA2[1]; PG8_STAGE(bufoff, kp, _v); } \
;         else { PG8_STAGE(bufoff, (kp) + (h) * hstepA, voffA); } } while (0)
; #define PG8_LDA(dst, b, h) do { _Pragma("unroll") for (int m = 0; m < 4; ++m) _Pragma("unroll") for (int k = 0; k < 2; ++k) dst[m][k] = *(const LAS bf16x8*)(lds + PG8_SA(b, h) + aoff + m * 2048 + k * 1024); } while (0)
; #define PG8_MMA(ai, bj, At, Bt) do { __builtin_amdgcn_s_setprio(1); _Pragma("unroll") for (int m = 0; m < 4; ++m) _Pragma("unroll") for (int n = 0; n < 2; ++n) _Pragma("unroll") for (int k = 0; k < 2; ++k) \
;         acc[ai][bj][m][n] = __builtin_amdgcn_mfma_f32_16x16x32_bf16(Bt[n][k], At[m][k], acc[ai][bj][m][n], 0, 0, 0); __builtin_amdgcn_s_setprio(0); } while (0)
; #define PG8_WAIT_V(n) asm volatile("s_waitcnt vmcnt(" #n ")" ::: "memory")
; #define PG8_WAIT_L(n) asm volatile("s_waitcnt lgkmcnt(" #n ")" ::: "memory")
; #define PG8_BAR __builtin_amdgcn_s_barrier()
; #define PG8_SCHED __builtin_amdgcn_sched_barrier(0)
;     ...
;             PG8_LDA(At, 1, 1); PG8_STAGE(PG8_SB(1, 0), b3, voffB); PG8_STAGE(PG8_SB(1, 1), b3 + hstepB, voffB); PG8_STAGE_A(PG8_SA(1, 0), 0, a3, last);
;             PG8_WAIT_V(8); PG8_WAIT_L(0); PG8_BAR; if (cur.amask & 2) { PG8_MMA(1, 0, At, B0); PG8_MMA(1, 1, At, B1); } PG8_BAR; PG8_SCHED;
;         }
	s_add_i32 s31, s31, s43
	v_lshl_add_u64 v[142:143], v[142:143], 0, s[92:93]
	s_mov_b32 m0, s31
	ds_read_b128 v[182:185], v147 offset:49152
	ds_read_b128 v[186:189], v147 offset:50176
	ds_read_b128 v[190:193], v147 offset:51200
	ds_read_b128 v[194:197], v147 offset:52224
	ds_read_b128 v[198:201], v147 offset:53248
	ds_read_b128 v[202:205], v147 offset:54272
	ds_read_b128 v[206:209], v147 offset:55296
	ds_read_b128 v[210:213], v147 offset:56320
	global_load_lds_dwordx4 v[142:143], off
	s_add_i32 m0, s31, 0x2000
	s_add_u32 s54, s80, 0x80080
	v_lshl_add_u64 v[142:143], v[214:215], 0, s[92:93]
	s_addc_u32 s55, s81, 0
	s_add_i32 s31, s82, s43
	global_load_lds_dwordx4 v[142:143], off
	v_lshl_add_u64 v[142:143], s[54:55], 0, v[0:1]
	s_mov_b32 m0, s31
	s_nop 0
	global_load_lds_dwordx4 v[142:143], off
	v_lshl_add_u64 v[142:143], s[54:55], 0, v[134:135]
	s_add_i32 m0, s31, 0x2000
	s_nop 0
	global_load_lds_dwordx4 v[142:143], off
	v_lshl_add_u64 v[142:143], v[224:225], 0, s[92:93]
	s_mov_b32 m0, s16
	s_nop 0
	global_load_lds_dwordx4 v[142:143], off
	v_lshl_add_u64 v[142:143], v[226:227], 0, s[92:93]
	s_mov_b32 m0, s17
	s_nop 0
	global_load_lds_dwordx4 v[142:143], off
	s_waitcnt vmcnt(8)
	s_waitcnt lgkmcnt(0)
	s_barrier
	s_waitcnt lgkmcnt(0)
	v_mfma_f32_16x16x32_bf16 v[50:53], v[150:153], v[182:185], v[50:53]
	v_mfma_f32_16x16x32_bf16 v[54:57], v[158:161], v[182:185], v[54:57]
	v_mfma_f32_16x16x32_bf16 v[34:37], v[150:153], v[190:193], v[34:37]
	v_mfma_f32_16x16x32_bf16 v[38:41], v[158:161], v[190:193], v[38:41]
	v_mfma_f32_16x16x32_bf16 v[18:21], v[150:153], v[198:201], v[18:21]
	v_mfma_f32_16x16x32_bf16 v[22:25], v[158:161], v[198:201], v[22:25]
	v_mfma_f32_16x16x32_bf16 v[2:5], v[150:153], v[206:209], v[2:5]
	v_mfma_f32_16x16x32_bf16 v[6:9], v[158:161], v[206:209], v[6:9]
	v_mfma_f32_16x16x32_bf16 v[50:53], v[154:157], v[186:189], v[50:53]
	v_mfma_f32_16x16x32_bf16 v[54:57], v[162:165], v[186:189], v[54:57]
	v_mfma_f32_16x16x32_bf16 v[34:37], v[154:157], v[194:197], v[34:37]
	v_mfma_f32_16x16x32_bf16 v[38:41], v[162:165], v[194:197], v[38:41]
	v_mfma_f32_16x16x32_bf16 v[18:21], v[154:157], v[202:205], v[18:21]
	v_mfma_f32_16x16x32_bf16 v[22:25], v[162:165], v[202:205], v[22:25]
	v_mfma_f32_16x16x32_bf16 v[2:5], v[154:157], v[210:213], v[2:5]
	v_mfma_f32_16x16x32_bf16 v[6:9], v[162:165], v[210:213], v[6:9]
	v_mfma_f32_16x16x32_bf16 v[58:61], v[166:169], v[182:185], v[58:61]
	v_mfma_f32_16x16x32_bf16 v[62:65], v[174:177], v[182:185], v[62:65]
	v_mfma_f32_16x16x32_bf16 v[42:45], v[166:169], v[190:193], v[42:45]
	v_mfma_f32_16x16x32_bf16 v[46:49], v[174:177], v[190:193], v[46:49]
	v_mfma_f32_16x16x32_bf16 v[26:29], v[166:169], v[198:201], v[26:29]
	v_mfma_f32_16x16x32_bf16 v[30:33], v[174:177], v[198:201], v[30:33]
	v_mfma_f32_16x16x32_bf16 v[10:13], v[166:169], v[206:209], v[10:13]
	v_mfma_f32_16x16x32_bf16 v[14:17], v[174:177], v[206:209], v[14:17]
	v_mfma_f32_16x16x32_bf16 v[58:61], v[170:173], v[186:189], v[58:61]
	v_mfma_f32_16x16x32_bf16 v[62:65], v[178:181], v[186:189], v[62:65]
	v_mfma_f32_16x16x32_bf16 v[42:45], v[170:173], v[194:197], v[42:45]
	v_mfma_f32_16x16x32_bf16 v[46:49], v[178:181], v[194:197], v[46:49]
	v_mfma_f32_16x16x32_bf16 v[26:29], v[170:173], v[202:205], v[26:29]
	v_mfma_f32_16x16x32_bf16 v[30:33], v[178:181], v[202:205], v[30:33]
	v_mfma_f32_16x16x32_bf16 v[10:13], v[170:173], v[210:213], v[10:13]
	v_mfma_f32_16x16x32_bf16 v[14:17], v[178:181], v[210:213], v[14:17]
	s_barrier
	s_add_u32 s76, s76, 0x100
	s_addc_u32 s77, s77, 0
	s_add_u32 s29, s29, 0x100
	s_addc_u32 s30, s30, 0
	s_cmp_ge_u32 s34, s22
	s_mov_b32 s31, s34
	s_cbranch_scc0 .LBB0_544
	v_readlane_b32 s24, v252, 14
	v_readlane_b32 s25, v252, 15
	s_and_b64 vcc, exec, s[24:25]
	s_cbranch_vccz .LBB0_547
	s_barrier

; #define PG8_STAGE(bufoff, gbase, voff) do { _Pragma("unroll") for (int _i = 0; _i < 2; ++_i) \
;         __builtin_amdgcn_global_load_lds((const unsigned*)((const char*)(gbase) + (voff)[_i]), (LAS unsigned*)(lds + (bufoff) + ldsw + _i * 8192), 16, 0, 0); } while (0)
; #define PG8_STAGE_A(bufoff, h, kp, nx) do { if constexpr (GATHER) { const unsigned _p = (nx) ? ng[h] : cg[h]; unsigned _v[2]; _v[0] = (_p & 0xffffu) * lda + CA2[0]; _v[1] = (_p >> 16) * lda + CA2[1]; PG8_STAGE(bufoff, kp, _v); } \
;         else { PG8_STAGE(bufoff, (kp) + (h) * hstepA, voffA); } } while (0)
; #define PG8_LDA(dst, b, h) do { _Pragma("unroll") for (int m = 0; m < 4; ++m) _Pragma("unroll") for (int k = 0; k < 2; ++k) dst[m][k] = *(const LAS bf16x8*)(lds + PG8_SA(b, h) + aoff + m * 2048 + k * 1024); } while (0)
; #define PG8_LDB(dst, b, h) do { _Pragma("unroll") for (int n = 0; n < 2; ++n) _Pragma("unroll") for (int k = 0; k < 2; ++k) dst[n][k] = *(const LAS bf16x8*)(lds + PG8_SB(b, h) + boff + n * 2048 + k * 1024); } while (0)
; #define PG8_MMA(ai, bj, At, Bt) do { __builtin_amdgcn_s_setprio(1); _Pragma("unroll") for (int m = 0; m < 4; ++m) _Pragma("unroll") for (int n = 0; n < 2; ++n) _Pragma("unroll") for (int k = 0; k < 2; ++k) \
;         acc[ai][bj][m][n] = __builtin_amdgcn_mfma_f32_16x16x32_bf16(Bt[n][k], At[m][k], acc[ai][bj][m][n], 0, 0, 0); __builtin_amdgcn_s_setprio(0); } while (0)
; #define PG8_WAIT_V(n) asm volatile("s_waitcnt vmcnt(" #n ")" ::: "memory")
;     ...
;         for (int t = 0; t < nt; t += 2) {
;             const bool last = (t == nt - 2);
;             const char* a1 = cA + (size_t)(t + 1) * kstep;
;             const char* a2 = last ? nA : cA + (size_t)(t + 2) * kstep; const char* b2 = last ? nB : cB + (size_t)(t + 2) * kstep;
;             const char* a3 = a2 + kstep; const char* b3 = b2 + kstep;
;             PG8_LDB(B0, 0, 0); PG8_LDB(B1, 0, 1); PG8_SCHED; PG8_LDA(At, 0, 0); PG8_STAGE_A(PG8_SA(1, 1), 1, a1, false);
;             PG8_WAIT_V(8); PG8_WAIT_L(0); PG8_BAR; if (cur.amask & 1) { PG8_MMA(0, 0, At, B0); PG8_MMA(0, 1, At, B1); } PG8_BAR; PG8_SCHED;
;             PG8_LDA(At, 0, 1); PG8_STAGE(PG8_SB(0, 0), b2, voffB); PG8_STAGE(PG8_SB(0, 1), b2 + hstepB, voffB); PG8_STAGE_A(PG8_SA(0, 0), 0, a2, last);
;             PG8_WAIT_V(8); PG8_WAIT_L(0); PG8_BAR; if (cur.amask & 2) { PG8_MMA(1, 0, At, B0); PG8_MMA(1, 1, At, B1); } PG8_BAR; PG8_SCHED;
.LBB0_1085:
	s_add_u32 s16, s48, 0xfff80080
	s_addc_u32 s17, s49, -1
	s_add_i32 s18, 0, 0x10000
	s_cmp_eq_u32 s15, 28
	s_cselect_b32 s53, s39, s17
	s_cselect_b32 s52, s38, s16
	v_add_u32_e32 v148, s18, v151
	s_cselect_b32 s51, s41, s14
	s_cselect_b32 s50, s40, s13
	s_add_i32 s19, 0, 0x14000
	ds_read_b128 v[144:147], v148
	ds_read_b128 v[154:157], v148 offset:1024
	ds_read_b128 v[158:161], v148 offset:2048
	ds_read_b128 v[162:165], v148 offset:3072
	v_add_u32_e32 v148, s19, v151
	ds_read_b128 v[166:169], v148
	ds_read_b128 v[170:173], v148 offset:1024
	ds_read_b128 v[174:177], v148 offset:2048
	ds_read_b128 v[178:181], v148 offset:3072
	v_lshl_add_u64 v[148:149], s[48:49], 0, v[140:141]
	s_add_i32 m0, s6, 0xc000
	ds_read_b128 v[182:185], v152
	ds_read_b128 v[186:189], v152 offset:1024
	ds_read_b128 v[190:193], v152 offset:2048
	ds_read_b128 v[194:197], v152 offset:3072
	ds_read_b128 v[198:201], v152 offset:4096
	ds_read_b128 v[202:205], v152 offset:5120
	ds_read_b128 v[206:209], v152 offset:6144
	ds_read_b128 v[210:213], v152 offset:7168
	global_load_lds_dwordx4 v[148:149], off
	v_lshl_add_u64 v[148:149], s[48:49], 0, v[142:143]
	s_add_i32 m0, s6, 0xe000
	s_nop 0
	global_load_lds_dwordx4 v[148:149], off
	s_waitcnt vmcnt(8)
	s_waitcnt lgkmcnt(0)
	s_barrier
	s_waitcnt lgkmcnt(0)
	v_mfma_f32_16x16x32_bf16 v[126:129], v[144:147], v[182:185], v[126:129]
	v_mfma_f32_16x16x32_bf16 v[122:125], v[158:161], v[182:185], v[122:125]
	v_mfma_f32_16x16x32_bf16 v[110:113], v[144:147], v[190:193], v[110:113]
	v_mfma_f32_16x16x32_bf16 v[106:109], v[158:161], v[190:193], v[106:109]
	v_mfma_f32_16x16x32_bf16 v[94:97], v[144:147], v[198:201], v[94:97]
	v_mfma_f32_16x16x32_bf16 v[90:93], v[158:161], v[198:201], v[90:93]
	v_mfma_f32_16x16x32_bf16 v[78:81], v[144:147], v[206:209], v[78:81]
	v_mfma_f32_16x16x32_bf16 v[74:77], v[158:161], v[206:209], v[74:77]
	v_mfma_f32_16x16x32_bf16 v[126:129], v[154:157], v[186:189], v[126:129]
	v_mfma_f32_16x16x32_bf16 v[122:125], v[162:165], v[186:189], v[122:125]
	v_mfma_f32_16x16x32_bf16 v[110:113], v[154:157], v[194:197], v[110:113]
	v_mfma_f32_16x16x32_bf16 v[106:109], v[162:165], v[194:197], v[106:109]
	v_mfma_f32_16x16x32_bf16 v[94:97], v[154:157], v[202:205], v[94:97]
	v_mfma_f32_16x16x32_bf16 v[90:93], v[162:165], v[202:205], v[90:93]
	v_mfma_f32_16x16x32_bf16 v[78:81], v[154:157], v[210:213], v[78:81]
	v_mfma_f32_16x16x32_bf16 v[74:77], v[162:165], v[210:213], v[74:77]
	v_mfma_f32_16x16x32_bf16 v[118:121], v[166:169], v[182:185], v[118:121]
	v_mfma_f32_16x16x32_bf16 v[114:117], v[174:177], v[182:185], v[114:117]
	v_mfma_f32_16x16x32_bf16 v[102:105], v[166:169], v[190:193], v[102:105]
	v_mfma_f32_16x16x32_bf16 v[98:101], v[174:177], v[190:193], v[98:101]
	v_mfma_f32_16x16x32_bf16 v[86:89], v[166:169], v[198:201], v[86:89]
	v_mfma_f32_16x16x32_bf16 v[82:85], v[174:177], v[198:201], v[82:85]
	v_mfma_f32_16x16x32_bf16 v[70:73], v[166:169], v[206:209], v[70:73]
	v_mfma_f32_16x16x32_bf16 v[66:69], v[174:177], v[206:209], v[66:69]
	v_mfma_f32_16x16x32_bf16 v[118:121], v[170:173], v[186:189], v[118:121]
	v_mfma_f32_16x16x32_bf16 v[114:117], v[178:181], v[186:189], v[114:117]
	v_mfma_f32_16x16x32_bf16 v[102:105], v[170:173], v[194:197], v[102:105]
	v_mfma_f32_16x16x32_bf16 v[98:101], v[178:181], v[194:197], v[98:101]
	v_mfma_f32_16x16x32_bf16 v[86:89], v[170:173], v[202:205], v[86:89]
	v_mfma_f32_16x16x32_bf16 v[82:85], v[178:181], v[202:205], v[82:85]
	v_mfma_f32_16x16x32_bf16 v[70:73], v[170:173], v[210:213], v[70:73]
	v_mfma_f32_16x16x32_bf16 v[66:69], v[178:181], v[210:213], v[66:69]
	s_barrier
	s_add_i32 s16, s18, s43
	v_lshl_add_u64 v[148:149], s[50:51], 0, v[0:1]
	s_mov_b32 m0, s16
	ds_read_b128 v[182:185], v152 offset:16384
	ds_read_b128 v[186:189], v152 offset:17408
	ds_read_b128 v[190:193], v152 offset:18432
	ds_read_b128 v[194:197], v152 offset:19456
	ds_read_b128 v[198:201], v152 offset:20480
	ds_read_b128 v[202:205], v152 offset:21504
	ds_read_b128 v[206:209], v152 offset:22528
	ds_read_b128 v[210:213], v152 offset:23552
	global_load_lds_dwordx4 v[148:149], off
	s_add_i32 m0, s16, 0x2000
	s_add_u32 s16, s50, 0x80000
	v_lshl_add_u64 v[214:215], s[50:51], 0, v[134:135]
	s_addc_u32 s17, s51, 0
	s_add_i32 s18, s19, s43
	global_load_lds_dwordx4 v[214:215], off
	v_lshl_add_u64 v[224:225], s[16:17], 0, v[0:1]
	s_mov_b32 m0, s18
	v_lshl_add_u64 v[226:227], s[52:53], 0, v[132:133]
	global_load_lds_dwordx4 v[224:225], off
	v_lshl_add_u64 v[224:225], s[16:17], 0, v[134:135]
	s_add_i32 m0, s18, 0x2000
	s_nop 0
	global_load_lds_dwordx4 v[224:225], off
	v_lshl_add_u64 v[224:225], s[52:53], 0, v[130:131]
	s_mov_b32 m0, s6
	s_nop 0
	global_load_lds_dwordx4 v[224:225], off
	s_mov_b32 m0, s7
	s_nop 0
	global_load_lds_dwordx4 v[226:227], off
	s_waitcnt vmcnt(8)
	s_waitcnt lgkmcnt(0)
	s_barrier
; #define PG8_STAGE(bufoff, gbase, voff) do { _Pragma("unroll") for (int _i = 0; _i < 2; ++_i) \
;         __builtin_amdgcn_global_load_lds((const unsigned*)((const char*)(gbase) + (voff)[_i]), (LAS unsigned*)(lds + (bufoff) + ldsw + _i * 8192), 16, 0, 0); } while (0)
; #define PG8_STAGE_A(bufoff, h, kp, nx) do { if constexpr (GATHER) { const unsigned _p = (nx) ? ng[h] : cg[h]; unsigned _v[2]; _v[0] = (_p & 0xffffu) * lda + CA2[0]; _v[1] = (_p >> 16) * lda + CA2[1]; PG8_STAGE(bufoff, kp, _v); } \
;         else { PG8_STAGE(bufoff, (kp) + (h) * hstepA, voffA); } } while (0)
; #define PG8_LDA(dst, b, h) do { _Pragma("unroll") for (int m = 0; m < 4; ++m) _Pragma("unroll") for (int k = 0; k < 2; ++k) dst[m][k] = *(const LAS bf16x8*)(lds + PG8_SA(b, h) + aoff + m * 2048 + k * 1024); } while (0)
; #define PG8_LDB(dst, b, h) do { _Pragma("unroll") for (int n = 0; n < 2; ++n) _Pragma("unroll") for (int k = 0; k < 2; ++k) dst[n][k] = *(const LAS bf16x8*)(lds + PG8_SB(b, h) + boff + n * 2048 + k * 1024); } while (0)
; #define PG8_MMA(ai, bj, At, Bt) do { __builtin_amdgcn_s_setprio(1); _Pragma("unroll") for (int m = 0; m < 4; ++m) _Pragma("unroll") for (int n = 0; n < 2; ++n) _Pragma("unroll") for (int k = 0; k < 2; ++k) \
;         acc[ai][bj][m][n] = __builtin_amdgcn_mfma_f32_16x16x32_bf16(Bt[n][k], At[m][k], acc[ai][bj][m][n], 0, 0, 0); __builtin_amdgcn_s_setprio(0); } while (0)
; #define PG8_WAIT_V(n) asm volatile("s_waitcnt vmcnt(" #n ")" ::: "memory")
; #define PG8_WAIT_L(n) asm volatile("s_waitcnt lgkmcnt(" #n ")" ::: "memory")
; #define PG8_BAR __builtin_amdgcn_s_barrier()
; #define PG8_SCHED __builtin_amdgcn_sched_barrier(0)
;     ...
;             PG8_WAIT_V(8); PG8_WAIT_L(0); PG8_BAR; if (cur.amask & 2) { PG8_MMA(1, 0, At, B0); PG8_MMA(1, 1, At, B1); } PG8_BAR; PG8_SCHED;
;             PG8_LDB(B0, 1, 0); PG8_LDB(B1, 1, 1); PG8_SCHED; PG8_LDA(At, 1, 0); PG8_STAGE_A(PG8_SA(0, 1), 1, a2, last);
;             PG8_WAIT_V(8); PG8_WAIT_L(0); PG8_BAR; if (cur.amask & 1) { PG8_MMA(0, 0, At, B0); PG8_MMA(0, 1, At, B1); } PG8_BAR; PG8_SCHED;
;             PG8_LDA(At, 1, 1); PG8_STAGE(PG8_SB(1, 0), b3, voffB); PG8_STAGE(PG8_SB(1, 1), b3 + hstepB, voffB); PG8_STAGE_A(PG8_SA(1, 0), 0, a3, last);
;             PG8_WAIT_V(8); PG8_WAIT_L(0); PG8_BAR; if (cur.amask & 2) { PG8_MMA(1, 0, At, B0); PG8_MMA(1, 1, At, B1); } PG8_BAR; PG8_SCHED;
	s_waitcnt lgkmcnt(0)
	v_mfma_f32_16x16x32_bf16 v[62:65], v[144:147], v[182:185], v[62:65]
	v_mfma_f32_16x16x32_bf16 v[58:61], v[158:161], v[182:185], v[58:61]
	v_mfma_f32_16x16x32_bf16 v[46:49], v[144:147], v[190:193], v[46:49]
	v_mfma_f32_16x16x32_bf16 v[42:45], v[158:161], v[190:193], v[42:45]
	v_mfma_f32_16x16x32_bf16 v[30:33], v[144:147], v[198:201], v[30:33]
	v_mfma_f32_16x16x32_bf16 v[26:29], v[158:161], v[198:201], v[26:29]
	v_mfma_f32_16x16x32_bf16 v[14:17], v[144:147], v[206:209], v[14:17]
	v_mfma_f32_16x16x32_bf16 v[10:13], v[158:161], v[206:209], v[10:13]
	v_mfma_f32_16x16x32_bf16 v[62:65], v[154:157], v[186:189], v[62:65]
	v_mfma_f32_16x16x32_bf16 v[58:61], v[162:165], v[186:189], v[58:61]
	v_mfma_f32_16x16x32_bf16 v[46:49], v[154:157], v[194:197], v[46:49]
	v_mfma_f32_16x16x32_bf16 v[42:45], v[162:165], v[194:197], v[42:45]
	v_mfma_f32_16x16x32_bf16 v[30:33], v[154:157], v[202:205], v[30:33]
	v_mfma_f32_16x16x32_bf16 v[26:29], v[162:165], v[202:205], v[26:29]
	v_mfma_f32_16x16x32_bf16 v[14:17], v[154:157], v[210:213], v[14:17]
	v_mfma_f32_16x16x32_bf16 v[10:13], v[162:165], v[210:213], v[10:13]
	v_mfma_f32_16x16x32_bf16 v[54:57], v[166:169], v[182:185], v[54:57]
	v_mfma_f32_16x16x32_bf16 v[50:53], v[174:177], v[182:185], v[50:53]
	v_mfma_f32_16x16x32_bf16 v[38:41], v[166:169], v[190:193], v[38:41]
	v_mfma_f32_16x16x32_bf16 v[34:37], v[174:177], v[190:193], v[34:37]
	v_mfma_f32_16x16x32_bf16 v[22:25], v[166:169], v[198:201], v[22:25]
	v_mfma_f32_16x16x32_bf16 v[18:21], v[174:177], v[198:201], v[18:21]
	v_mfma_f32_16x16x32_bf16 v[6:9], v[166:169], v[206:209], v[6:9]
	v_mfma_f32_16x16x32_bf16 v[2:5], v[174:177], v[206:209], v[2:5]
	v_mfma_f32_16x16x32_bf16 v[54:57], v[170:173], v[186:189], v[54:57]
	v_mfma_f32_16x16x32_bf16 v[50:53], v[178:181], v[186:189], v[50:53]
	v_mfma_f32_16x16x32_bf16 v[38:41], v[170:173], v[194:197], v[38:41]
	v_mfma_f32_16x16x32_bf16 v[34:37], v[178:181], v[194:197], v[34:37]
	v_mfma_f32_16x16x32_bf16 v[22:25], v[170:173], v[202:205], v[22:25]
	v_mfma_f32_16x16x32_bf16 v[18:21], v[178:181], v[202:205], v[18:21]
	v_mfma_f32_16x16x32_bf16 v[6:9], v[170:173], v[210:213], v[6:9]
	v_mfma_f32_16x16x32_bf16 v[2:5], v[178:181], v[210:213], v[2:5]
	s_barrier
	s_add_i32 s18, 0, 0x18000
	v_add_u32_e32 v153, s18, v151
	s_add_i32 s19, 0, 0x1c000
	ds_read_b128 v[144:147], v153
	ds_read_b128 v[154:157], v153 offset:1024
	ds_read_b128 v[158:161], v153 offset:2048
	ds_read_b128 v[162:165], v153 offset:3072
	v_add_u32_e32 v153, s19, v151
	ds_read_b128 v[166:169], v153
	ds_read_b128 v[170:173], v153 offset:1024
	ds_read_b128 v[174:177], v153 offset:2048
	ds_read_b128 v[178:181], v153 offset:3072
	s_add_u32 s16, s52, 0x80000
	s_addc_u32 s17, s53, 0
	s_mov_b32 m0, s8
	v_lshl_add_u64 v[228:229], s[16:17], 0, v[130:131]
	ds_read_b128 v[182:185], v152 offset:32768
	ds_read_b128 v[186:189], v152 offset:33792
	ds_read_b128 v[190:193], v152 offset:34816
	ds_read_b128 v[194:197], v152 offset:35840
	ds_read_b128 v[198:201], v152 offset:36864
	ds_read_b128 v[202:205], v152 offset:37888
	ds_read_b128 v[206:209], v152 offset:38912
	ds_read_b128 v[210:213], v152 offset:39936
	global_load_lds_dwordx4 v[228:229], off
	v_lshl_add_u64 v[228:229], s[16:17], 0, v[132:133]
	s_mov_b32 m0, s9
	s_nop 0
	global_load_lds_dwordx4 v[228:229], off
	s_waitcnt vmcnt(8)
	s_waitcnt lgkmcnt(0)
	s_barrier
	s_waitcnt lgkmcnt(0)
	v_mfma_f32_16x16x32_bf16 v[126:129], v[144:147], v[182:185], v[126:129]
	v_mfma_f32_16x16x32_bf16 v[122:125], v[158:161], v[182:185], v[122:125]
	v_mfma_f32_16x16x32_bf16 v[110:113], v[144:147], v[190:193], v[110:113]
	v_mfma_f32_16x16x32_bf16 v[106:109], v[158:161], v[190:193], v[106:109]
	v_mfma_f32_16x16x32_bf16 v[94:97], v[144:147], v[198:201], v[94:97]
	v_mfma_f32_16x16x32_bf16 v[90:93], v[158:161], v[198:201], v[90:93]
	v_mfma_f32_16x16x32_bf16 v[78:81], v[144:147], v[206:209], v[78:81]
	v_mfma_f32_16x16x32_bf16 v[74:77], v[158:161], v[206:209], v[74:77]
	v_mfma_f32_16x16x32_bf16 v[126:129], v[154:157], v[186:189], v[126:129]
	v_mfma_f32_16x16x32_bf16 v[122:125], v[162:165], v[186:189], v[122:125]
	v_mfma_f32_16x16x32_bf16 v[110:113], v[154:157], v[194:197], v[110:113]
	v_mfma_f32_16x16x32_bf16 v[106:109], v[162:165], v[194:197], v[106:109]
	v_mfma_f32_16x16x32_bf16 v[94:97], v[154:157], v[202:205], v[94:97]
	v_mfma_f32_16x16x32_bf16 v[90:93], v[162:165], v[202:205], v[90:93]
	v_mfma_f32_16x16x32_bf16 v[78:81], v[154:157], v[210:213], v[78:81]
	v_mfma_f32_16x16x32_bf16 v[74:77], v[162:165], v[210:213], v[74:77]
	v_mfma_f32_16x16x32_bf16 v[118:121], v[166:169], v[182:185], v[118:121]
	v_mfma_f32_16x16x32_bf16 v[114:117], v[174:177], v[182:185], v[114:117]
	v_mfma_f32_16x16x32_bf16 v[102:105], v[166:169], v[190:193], v[102:105]
	v_mfma_f32_16x16x32_bf16 v[98:101], v[174:177], v[190:193], v[98:101]
	v_mfma_f32_16x16x32_bf16 v[86:89], v[166:169], v[198:201], v[86:89]
	v_mfma_f32_16x16x32_bf16 v[82:85], v[174:177], v[198:201], v[82:85]
	v_mfma_f32_16x16x32_bf16 v[70:73], v[166:169], v[206:209], v[70:73]
	v_mfma_f32_16x16x32_bf16 v[66:69], v[174:177], v[206:209], v[66:69]
	v_mfma_f32_16x16x32_bf16 v[118:121], v[170:173], v[186:189], v[118:121]
	v_mfma_f32_16x16x32_bf16 v[114:117], v[178:181], v[186:189], v[114:117]
	v_mfma_f32_16x16x32_bf16 v[102:105], v[170:173], v[194:197], v[102:105]
	v_mfma_f32_16x16x32_bf16 v[98:101], v[178:181], v[194:197], v[98:101]
	v_mfma_f32_16x16x32_bf16 v[86:89], v[170:173], v[202:205], v[86:89]
	v_mfma_f32_16x16x32_bf16 v[82:85], v[178:181], v[202:205], v[82:85]
	v_mfma_f32_16x16x32_bf16 v[70:73], v[170:173], v[210:213], v[70:73]
	v_mfma_f32_16x16x32_bf16 v[66:69], v[178:181], v[210:213], v[66:69]
	s_barrier
; #define PG8_STAGE(bufoff, gbase, voff) do { _Pragma("unroll") for (int _i = 0; _i < 2; ++_i) \
;         __builtin_amdgcn_global_load_lds((const unsigned*)((const char*)(gbase) + (voff)[_i]), (LAS unsigned*)(lds + (bufoff) + ldsw + _i * 8192), 16, 0, 0); } while (0)
; #define PG8_STAGE_A(bufoff, h, kp, nx) do { if constexpr (GATHER) { const unsigned _p = (nx) ? ng[h] : cg[h]; unsigned _v[2]; _v[0] = (_p & 0xffffu) * lda + CA2[0]; _v[1] = (_p >> 16) * lda + CA2[1]; PG8_STAGE(bufoff, kp, _v); } \
;         else { PG8_STAGE(bufoff, (kp) + (h) * hstepA, voffA); } } while (0)
; #define PG8_LDA(dst, b, h) do { _Pragma("unroll") for (int m = 0; m < 4; ++m) _Pragma("unroll") for (int k = 0; k < 2; ++k) dst[m][k] = *(const LAS bf16x8*)(lds + PG8_SA(b, h) + aoff + m * 2048 + k * 1024); } while (0)
; #define PG8_MMA(ai, bj, At, Bt) do { __builtin_amdgcn_s_setprio(1); _Pragma("unroll") for (int m = 0; m < 4; ++m) _Pragma("unroll") for (int n = 0; n < 2; ++n) _Pragma("unroll") for (int k = 0; k < 2; ++k) \
;         acc[ai][bj][m][n] = __builtin_amdgcn_mfma_f32_16x16x32_bf16(Bt[n][k], At[m][k], acc[ai][bj][m][n], 0, 0, 0); __builtin_amdgcn_s_setprio(0); } while (0)
; #define PG8_WAIT_V(n) asm volatile("s_waitcnt vmcnt(" #n ")" ::: "memory")
; #define PG8_WAIT_L(n) asm volatile("s_waitcnt lgkmcnt(" #n ")" ::: "memory")
; #define PG8_BAR __builtin_amdgcn_s_barrier()
; #define PG8_SCHED __builtin_amdgcn_sched_barrier(0)
;     ...
;             PG8_LDA(At, 1, 1); PG8_STAGE(PG8_SB(1, 0), b3, voffB); PG8_STAGE(PG8_SB(1, 1), b3 + hstepB, voffB); PG8_STAGE_A(PG8_SA(1, 0), 0, a3, last);
;             PG8_WAIT_V(8); PG8_WAIT_L(0); PG8_BAR; if (cur.amask & 2) { PG8_MMA(1, 0, At, B0); PG8_MMA(1, 1, At, B1); } PG8_BAR; PG8_SCHED;
;         }
	s_add_i32 s16, s18, s43
	v_lshl_add_u64 v[148:149], v[148:149], 0, s[92:93]
	s_mov_b32 m0, s16
	ds_read_b128 v[182:185], v152 offset:49152
	ds_read_b128 v[186:189], v152 offset:50176
	ds_read_b128 v[190:193], v152 offset:51200
	ds_read_b128 v[194:197], v152 offset:52224
	ds_read_b128 v[198:201], v152 offset:53248
	ds_read_b128 v[202:205], v152 offset:54272
	ds_read_b128 v[206:209], v152 offset:55296
	ds_read_b128 v[210:213], v152 offset:56320
	global_load_lds_dwordx4 v[148:149], off
	s_add_i32 m0, s16, 0x2000
	s_add_u32 s16, s50, 0x80080
	v_lshl_add_u64 v[148:149], v[214:215], 0, s[92:93]
	s_addc_u32 s17, s51, 0
	s_add_i32 s18, s19, s43
	global_load_lds_dwordx4 v[148:149], off
	v_lshl_add_u64 v[148:149], s[16:17], 0, v[0:1]
	s_mov_b32 m0, s18
	s_nop 0
	global_load_lds_dwordx4 v[148:149], off
	v_lshl_add_u64 v[148:149], s[16:17], 0, v[134:135]
	s_add_i32 m0, s18, 0x2000
	s_nop 0
	global_load_lds_dwordx4 v[148:149], off
	v_lshl_add_u64 v[148:149], v[224:225], 0, s[92:93]
	s_mov_b32 m0, s10
	s_nop 0
	global_load_lds_dwordx4 v[148:149], off
	v_lshl_add_u64 v[148:149], v[226:227], 0, s[92:93]
	s_mov_b32 m0, s11
	s_nop 0
	global_load_lds_dwordx4 v[148:149], off
	s_waitcnt vmcnt(8)
	s_waitcnt lgkmcnt(0)
	s_barrier
	s_waitcnt lgkmcnt(0)
	v_mfma_f32_16x16x32_bf16 v[62:65], v[144:147], v[182:185], v[62:65]
	v_mfma_f32_16x16x32_bf16 v[58:61], v[158:161], v[182:185], v[58:61]
	v_mfma_f32_16x16x32_bf16 v[46:49], v[144:147], v[190:193], v[46:49]
	v_mfma_f32_16x16x32_bf16 v[42:45], v[158:161], v[190:193], v[42:45]
	v_mfma_f32_16x16x32_bf16 v[30:33], v[144:147], v[198:201], v[30:33]
	v_mfma_f32_16x16x32_bf16 v[26:29], v[158:161], v[198:201], v[26:29]
	v_mfma_f32_16x16x32_bf16 v[14:17], v[144:147], v[206:209], v[14:17]
	v_mfma_f32_16x16x32_bf16 v[10:13], v[158:161], v[206:209], v[10:13]
	v_mfma_f32_16x16x32_bf16 v[62:65], v[154:157], v[186:189], v[62:65]
	v_mfma_f32_16x16x32_bf16 v[58:61], v[162:165], v[186:189], v[58:61]
	v_mfma_f32_16x16x32_bf16 v[46:49], v[154:157], v[194:197], v[46:49]
	v_mfma_f32_16x16x32_bf16 v[42:45], v[162:165], v[194:197], v[42:45]
	v_mfma_f32_16x16x32_bf16 v[30:33], v[154:157], v[202:205], v[30:33]
	v_mfma_f32_16x16x32_bf16 v[26:29], v[162:165], v[202:205], v[26:29]
	v_mfma_f32_16x16x32_bf16 v[14:17], v[154:157], v[210:213], v[14:17]
	v_mfma_f32_16x16x32_bf16 v[10:13], v[162:165], v[210:213], v[10:13]
	v_mfma_f32_16x16x32_bf16 v[54:57], v[166:169], v[182:185], v[54:57]
	v_mfma_f32_16x16x32_bf16 v[50:53], v[174:177], v[182:185], v[50:53]
	v_mfma_f32_16x16x32_bf16 v[38:41], v[166:169], v[190:193], v[38:41]
	v_mfma_f32_16x16x32_bf16 v[34:37], v[174:177], v[190:193], v[34:37]
	v_mfma_f32_16x16x32_bf16 v[22:25], v[166:169], v[198:201], v[22:25]
	v_mfma_f32_16x16x32_bf16 v[18:21], v[174:177], v[198:201], v[18:21]
	v_mfma_f32_16x16x32_bf16 v[6:9], v[166:169], v[206:209], v[6:9]
	v_mfma_f32_16x16x32_bf16 v[2:5], v[174:177], v[206:209], v[2:5]
	v_mfma_f32_16x16x32_bf16 v[54:57], v[170:173], v[186:189], v[54:57]
	v_mfma_f32_16x16x32_bf16 v[50:53], v[178:181], v[186:189], v[50:53]
	v_mfma_f32_16x16x32_bf16 v[38:41], v[170:173], v[194:197], v[38:41]
	v_mfma_f32_16x16x32_bf16 v[34:37], v[178:181], v[194:197], v[34:37]
	v_mfma_f32_16x16x32_bf16 v[22:25], v[170:173], v[202:205], v[22:25]
	v_mfma_f32_16x16x32_bf16 v[18:21], v[178:181], v[202:205], v[18:21]
	v_mfma_f32_16x16x32_bf16 v[6:9], v[170:173], v[210:213], v[6:9]
	v_mfma_f32_16x16x32_bf16 v[2:5], v[178:181], v[210:213], v[2:5]
	s_barrier
	s_add_i32 s15, s15, 2
	s_add_u32 s48, s48, 0x100
	s_addc_u32 s49, s49, 0
	s_add_u32 s13, s13, 0x100
	s_addc_u32 s14, s14, 0
	s_cmp_gt_u32 s15, 29
	s_cbranch_scc0 .LBB0_1085
	v_readlane_b32 s14, v252, 14
	v_readlane_b32 s15, v252, 15
	s_and_b64 vcc, exec, s[14:15]
	s_cbranch_vccz .LBB0_1088
	s_barrier

; #define PG8_STAGE(bufoff, gbase, voff) do { _Pragma("unroll") for (int _i = 0; _i < 2; ++_i) \
;         __builtin_amdgcn_global_load_lds((const unsigned*)((const char*)(gbase) + (voff)[_i]), (LAS unsigned*)(lds + (bufoff) + ldsw + _i * 8192), 16, 0, 0); } while (0)
; #define PG8_STAGE_A(bufoff, h, kp, nx) do { if constexpr (GATHER) { const unsigned _p = (nx) ? ng[h] : cg[h]; unsigned _v[2]; _v[0] = (_p & 0xffffu) * lda + CA2[0]; _v[1] = (_p >> 16) * lda + CA2[1]; PG8_STAGE(bufoff, kp, _v); } \
;         else { PG8_STAGE(bufoff, (kp) + (h) * hstepA, voffA); } } while (0)
; #define PG8_LDA(dst, b, h) do { _Pragma("unroll") for (int m = 0; m < 4; ++m) _Pragma("unroll") for (int k = 0; k < 2; ++k) dst[m][k] = *(const LAS bf16x8*)(lds + PG8_SA(b, h) + aoff + m * 2048 + k * 1024); } while (0)
; #define PG8_LDB(dst, b, h) do { _Pragma("unroll") for (int n = 0; n < 2; ++n) _Pragma("unroll") for (int k = 0; k < 2; ++k) dst[n][k] = *(const LAS bf16x8*)(lds + PG8_SB(b, h) + boff + n * 2048 + k * 1024); } while (0)
; #define PG8_MMA(ai, bj, At, Bt) do { __builtin_amdgcn_s_setprio(1); _Pragma("unroll") for (int m = 0; m < 4; ++m) _Pragma("unroll") for (int n = 0; n < 2; ++n) _Pragma("unroll") for (int k = 0; k < 2; ++k) \
;         acc[ai][bj][m][n] = __builtin_amdgcn_mfma_f32_16x16x32_bf16(Bt[n][k], At[m][k], acc[ai][bj][m][n], 0, 0, 0); __builtin_amdgcn_s_setprio(0); } while (0)
; #define PG8_WAIT_V(n) asm volatile("s_waitcnt vmcnt(" #n ")" ::: "memory")
;     ...
;         for (int t = 0; t < nt; t += 2) {
;             const bool last = (t == nt - 2);
;             const char* a1 = cA + (size_t)(t + 1) * kstep;
;             const char* a2 = last ? nA : cA + (size_t)(t + 2) * kstep; const char* b2 = last ? nB : cB + (size_t)(t + 2) * kstep;
;             const char* a3 = a2 + kstep; const char* b3 = b2 + kstep;
;             PG8_LDB(B0, 0, 0); PG8_LDB(B1, 0, 1); PG8_SCHED; PG8_LDA(At, 0, 0); PG8_STAGE_A(PG8_SA(1, 1), 1, a1, false);
;             PG8_WAIT_V(8); PG8_WAIT_L(0); PG8_BAR; if (cur.amask & 1) { PG8_MMA(0, 0, At, B0); PG8_MMA(0, 1, At, B1); } PG8_BAR; PG8_SCHED;
;             PG8_LDA(At, 0, 1); PG8_STAGE(PG8_SB(0, 0), b2, voffB); PG8_STAGE(PG8_SB(0, 1), b2 + hstepB, voffB); PG8_STAGE_A(PG8_SA(0, 0), 0, a2, last);
;             PG8_WAIT_V(8); PG8_WAIT_L(0); PG8_BAR; if (cur.amask & 2) { PG8_MMA(1, 0, At, B0); PG8_MMA(1, 1, At, B1); } PG8_BAR; PG8_SCHED;
.LBB0_1117:
	s_add_u32 s16, s48, 0xfff80080
	s_addc_u32 s17, s49, -1
	s_add_i32 s18, 0, 0x10000
	s_cmp_eq_u32 s15, 28
	s_cselect_b32 s53, s39, s17
	s_cselect_b32 s52, s38, s16
	v_add_u32_e32 v148, s18, v151
	s_cselect_b32 s51, s41, s14
	s_cselect_b32 s50, s40, s13
	s_add_i32 s19, 0, 0x14000
	ds_read_b128 v[144:147], v148
	ds_read_b128 v[154:157], v148 offset:1024
	ds_read_b128 v[158:161], v148 offset:2048
	ds_read_b128 v[162:165], v148 offset:3072
	v_add_u32_e32 v148, s19, v151
	ds_read_b128 v[166:169], v148
	ds_read_b128 v[170:173], v148 offset:1024
	ds_read_b128 v[174:177], v148 offset:2048
	ds_read_b128 v[178:181], v148 offset:3072
	v_lshl_add_u64 v[148:149], s[48:49], 0, v[140:141]
	s_add_i32 m0, s6, 0xc000
	ds_read_b128 v[182:185], v152
	ds_read_b128 v[186:189], v152 offset:1024
	ds_read_b128 v[190:193], v152 offset:2048
	ds_read_b128 v[194:197], v152 offset:3072
	ds_read_b128 v[198:201], v152 offset:4096
	ds_read_b128 v[202:205], v152 offset:5120
	ds_read_b128 v[206:209], v152 offset:6144
	ds_read_b128 v[210:213], v152 offset:7168
	global_load_lds_dwordx4 v[148:149], off
	v_lshl_add_u64 v[148:149], s[48:49], 0, v[142:143]
	s_add_i32 m0, s6, 0xe000
	s_nop 0
	global_load_lds_dwordx4 v[148:149], off
	s_waitcnt vmcnt(8)
	s_waitcnt lgkmcnt(0)
	s_barrier
	s_waitcnt lgkmcnt(0)
	v_mfma_f32_16x16x32_bf16 v[126:129], v[144:147], v[182:185], v[126:129]
	v_mfma_f32_16x16x32_bf16 v[122:125], v[158:161], v[182:185], v[122:125]
	v_mfma_f32_16x16x32_bf16 v[114:117], v[144:147], v[190:193], v[114:117]
	v_mfma_f32_16x16x32_bf16 v[106:109], v[158:161], v[190:193], v[106:109]
	v_mfma_f32_16x16x32_bf16 v[94:97], v[144:147], v[198:201], v[94:97]
	v_mfma_f32_16x16x32_bf16 v[90:93], v[158:161], v[198:201], v[90:93]
	v_mfma_f32_16x16x32_bf16 v[82:85], v[144:147], v[206:209], v[82:85]
	v_mfma_f32_16x16x32_bf16 v[74:77], v[158:161], v[206:209], v[74:77]
	v_mfma_f32_16x16x32_bf16 v[126:129], v[154:157], v[186:189], v[126:129]
	v_mfma_f32_16x16x32_bf16 v[122:125], v[162:165], v[186:189], v[122:125]
	v_mfma_f32_16x16x32_bf16 v[114:117], v[154:157], v[194:197], v[114:117]
	v_mfma_f32_16x16x32_bf16 v[106:109], v[162:165], v[194:197], v[106:109]
	v_mfma_f32_16x16x32_bf16 v[94:97], v[154:157], v[202:205], v[94:97]
	v_mfma_f32_16x16x32_bf16 v[90:93], v[162:165], v[202:205], v[90:93]
	v_mfma_f32_16x16x32_bf16 v[82:85], v[154:157], v[210:213], v[82:85]
	v_mfma_f32_16x16x32_bf16 v[74:77], v[162:165], v[210:213], v[74:77]
	v_mfma_f32_16x16x32_bf16 v[118:121], v[166:169], v[182:185], v[118:121]
	v_mfma_f32_16x16x32_bf16 v[110:113], v[174:177], v[182:185], v[110:113]
	v_mfma_f32_16x16x32_bf16 v[102:105], v[166:169], v[190:193], v[102:105]
	v_mfma_f32_16x16x32_bf16 v[98:101], v[174:177], v[190:193], v[98:101]
	v_mfma_f32_16x16x32_bf16 v[86:89], v[166:169], v[198:201], v[86:89]
	v_mfma_f32_16x16x32_bf16 v[78:81], v[174:177], v[198:201], v[78:81]
	v_mfma_f32_16x16x32_bf16 v[70:73], v[166:169], v[206:209], v[70:73]
	v_mfma_f32_16x16x32_bf16 v[66:69], v[174:177], v[206:209], v[66:69]
	v_mfma_f32_16x16x32_bf16 v[118:121], v[170:173], v[186:189], v[118:121]
	v_mfma_f32_16x16x32_bf16 v[110:113], v[178:181], v[186:189], v[110:113]
	v_mfma_f32_16x16x32_bf16 v[102:105], v[170:173], v[194:197], v[102:105]
	v_mfma_f32_16x16x32_bf16 v[98:101], v[178:181], v[194:197], v[98:101]
	v_mfma_f32_16x16x32_bf16 v[86:89], v[170:173], v[202:205], v[86:89]
	v_mfma_f32_16x16x32_bf16 v[78:81], v[178:181], v[202:205], v[78:81]
	v_mfma_f32_16x16x32_bf16 v[70:73], v[170:173], v[210:213], v[70:73]
	v_mfma_f32_16x16x32_bf16 v[66:69], v[178:181], v[210:213], v[66:69]
	s_barrier
	s_add_i32 s16, s18, s43
	v_lshl_add_u64 v[148:149], s[50:51], 0, v[0:1]
	s_mov_b32 m0, s16
	ds_read_b128 v[182:185], v152 offset:16384
	ds_read_b128 v[186:189], v152 offset:17408
	ds_read_b128 v[190:193], v152 offset:18432
	ds_read_b128 v[194:197], v152 offset:19456
	ds_read_b128 v[198:201], v152 offset:20480
	ds_read_b128 v[202:205], v152 offset:21504
	ds_read_b128 v[206:209], v152 offset:22528
	ds_read_b128 v[210:213], v152 offset:23552
	global_load_lds_dwordx4 v[148:149], off
	s_add_i32 m0, s16, 0x2000
	s_add_u32 s16, s50, 0x80000
	v_lshl_add_u64 v[214:215], s[50:51], 0, v[134:135]
	s_addc_u32 s17, s51, 0
	s_add_i32 s18, s19, s43
	global_load_lds_dwordx4 v[214:215], off
	v_lshl_add_u64 v[224:225], s[16:17], 0, v[0:1]
	s_mov_b32 m0, s18
	v_lshl_add_u64 v[226:227], s[52:53], 0, v[132:133]
	global_load_lds_dwordx4 v[224:225], off
	v_lshl_add_u64 v[224:225], s[16:17], 0, v[134:135]
	s_add_i32 m0, s18, 0x2000
	s_nop 0
	global_load_lds_dwordx4 v[224:225], off
	v_lshl_add_u64 v[224:225], s[52:53], 0, v[130:131]
	s_mov_b32 m0, s6
	s_nop 0
	global_load_lds_dwordx4 v[224:225], off
	s_mov_b32 m0, s7
	s_nop 0
	global_load_lds_dwordx4 v[226:227], off
	s_waitcnt vmcnt(8)
	s_waitcnt lgkmcnt(0)
	s_barrier
; #define PG8_STAGE(bufoff, gbase, voff) do { _Pragma("unroll") for (int _i = 0; _i < 2; ++_i) \
;         __builtin_amdgcn_global_load_lds((const unsigned*)((const char*)(gbase) + (voff)[_i]), (LAS unsigned*)(lds + (bufoff) + ldsw + _i * 8192), 16, 0, 0); } while (0)
; #define PG8_STAGE_A(bufoff, h, kp, nx) do { if constexpr (GATHER) { const unsigned _p = (nx) ? ng[h] : cg[h]; unsigned _v[2]; _v[0] = (_p & 0xffffu) * lda + CA2[0]; _v[1] = (_p >> 16) * lda + CA2[1]; PG8_STAGE(bufoff, kp, _v); } \
;         else { PG8_STAGE(bufoff, (kp) + (h) * hstepA, voffA); } } while (0)
; #define PG8_LDA(dst, b, h) do { _Pragma("unroll") for (int m = 0; m < 4; ++m) _Pragma("unroll") for (int k = 0; k < 2; ++k) dst[m][k] = *(const LAS bf16x8*)(lds + PG8_SA(b, h) + aoff + m * 2048 + k * 1024); } while (0)
; #define PG8_LDB(dst, b, h) do { _Pragma("unroll") for (int n = 0; n < 2; ++n) _Pragma("unroll") for (int k = 0; k < 2; ++k) dst[n][k] = *(const LAS bf16x8*)(lds + PG8_SB(b, h) + boff + n * 2048 + k * 1024); } while (0)
; #define PG8_MMA(ai, bj, At, Bt) do { __builtin_amdgcn_s_setprio(1); _Pragma("unroll") for (int m = 0; m < 4; ++m) _Pragma("unroll") for (int n = 0; n < 2; ++n) _Pragma("unroll") for (int k = 0; k < 2; ++k) \
;         acc[ai][bj][m][n] = __builtin_amdgcn_mfma_f32_16x16x32_bf16(Bt[n][k], At[m][k], acc[ai][bj][m][n], 0, 0, 0); __builtin_amdgcn_s_setprio(0); } while (0)
; #define PG8_WAIT_V(n) asm volatile("s_waitcnt vmcnt(" #n ")" ::: "memory")
; #define PG8_WAIT_L(n) asm volatile("s_waitcnt lgkmcnt(" #n ")" ::: "memory")
; #define PG8_BAR __builtin_amdgcn_s_barrier()
; #define PG8_SCHED __builtin_amdgcn_sched_barrier(0)
;     ...
;             PG8_WAIT_V(8); PG8_WAIT_L(0); PG8_BAR; if (cur.amask & 2) { PG8_MMA(1, 0, At, B0); PG8_MMA(1, 1, At, B1); } PG8_BAR; PG8_SCHED;
;             PG8_LDB(B0, 1, 0); PG8_LDB(B1, 1, 1); PG8_SCHED; PG8_LDA(At, 1, 0); PG8_STAGE_A(PG8_SA(0, 1), 1, a2, last);
;             PG8_WAIT_V(8); PG8_WAIT_L(0); PG8_BAR; if (cur.amask & 1) { PG8_MMA(0, 0, At, B0); PG8_MMA(0, 1, At, B1); } PG8_BAR; PG8_SCHED;
;             PG8_LDA(At, 1, 1); PG8_STAGE(PG8_SB(1, 0), b3, voffB); PG8_STAGE(PG8_SB(1, 1), b3 + hstepB, voffB); PG8_STAGE_A(PG8_SA(1, 0), 0, a3, last);
;             PG8_WAIT_V(8); PG8_WAIT_L(0); PG8_BAR; if (cur.amask & 2) { PG8_MMA(1, 0, At, B0); PG8_MMA(1, 1, At, B1); } PG8_BAR; PG8_SCHED;
	s_waitcnt lgkmcnt(0)
	v_mfma_f32_16x16x32_bf16 v[62:65], v[144:147], v[182:185], v[62:65]
	v_mfma_f32_16x16x32_bf16 v[58:61], v[158:161], v[182:185], v[58:61]
	v_mfma_f32_16x16x32_bf16 v[50:53], v[144:147], v[190:193], v[50:53]
	v_mfma_f32_16x16x32_bf16 v[42:45], v[158:161], v[190:193], v[42:45]
	v_mfma_f32_16x16x32_bf16 v[30:33], v[144:147], v[198:201], v[30:33]
	v_mfma_f32_16x16x32_bf16 v[26:29], v[158:161], v[198:201], v[26:29]
	v_mfma_f32_16x16x32_bf16 v[18:21], v[144:147], v[206:209], v[18:21]
	v_mfma_f32_16x16x32_bf16 v[10:13], v[158:161], v[206:209], v[10:13]
	v_mfma_f32_16x16x32_bf16 v[62:65], v[154:157], v[186:189], v[62:65]
	v_mfma_f32_16x16x32_bf16 v[58:61], v[162:165], v[186:189], v[58:61]
	v_mfma_f32_16x16x32_bf16 v[50:53], v[154:157], v[194:197], v[50:53]
	v_mfma_f32_16x16x32_bf16 v[42:45], v[162:165], v[194:197], v[42:45]
	v_mfma_f32_16x16x32_bf16 v[30:33], v[154:157], v[202:205], v[30:33]
	v_mfma_f32_16x16x32_bf16 v[26:29], v[162:165], v[202:205], v[26:29]
	v_mfma_f32_16x16x32_bf16 v[18:21], v[154:157], v[210:213], v[18:21]
	v_mfma_f32_16x16x32_bf16 v[10:13], v[162:165], v[210:213], v[10:13]
	v_mfma_f32_16x16x32_bf16 v[54:57], v[166:169], v[182:185], v[54:57]
	v_mfma_f32_16x16x32_bf16 v[46:49], v[174:177], v[182:185], v[46:49]
	v_mfma_f32_16x16x32_bf16 v[38:41], v[166:169], v[190:193], v[38:41]
	v_mfma_f32_16x16x32_bf16 v[34:37], v[174:177], v[190:193], v[34:37]
	v_mfma_f32_16x16x32_bf16 v[22:25], v[166:169], v[198:201], v[22:25]
	v_mfma_f32_16x16x32_bf16 v[14:17], v[174:177], v[198:201], v[14:17]
	v_mfma_f32_16x16x32_bf16 v[6:9], v[166:169], v[206:209], v[6:9]
	v_mfma_f32_16x16x32_bf16 v[2:5], v[174:177], v[206:209], v[2:5]
	v_mfma_f32_16x16x32_bf16 v[54:57], v[170:173], v[186:189], v[54:57]
	v_mfma_f32_16x16x32_bf16 v[46:49], v[178:181], v[186:189], v[46:49]
	v_mfma_f32_16x16x32_bf16 v[38:41], v[170:173], v[194:197], v[38:41]
	v_mfma_f32_16x16x32_bf16 v[34:37], v[178:181], v[194:197], v[34:37]
	v_mfma_f32_16x16x32_bf16 v[22:25], v[170:173], v[202:205], v[22:25]
	v_mfma_f32_16x16x32_bf16 v[14:17], v[178:181], v[202:205], v[14:17]
	v_mfma_f32_16x16x32_bf16 v[6:9], v[170:173], v[210:213], v[6:9]
	v_mfma_f32_16x16x32_bf16 v[2:5], v[178:181], v[210:213], v[2:5]
	s_barrier
	s_add_i32 s18, 0, 0x18000
	v_add_u32_e32 v153, s18, v151
	s_add_i32 s19, 0, 0x1c000
	ds_read_b128 v[144:147], v153
	ds_read_b128 v[154:157], v153 offset:1024
	ds_read_b128 v[158:161], v153 offset:2048
	ds_read_b128 v[162:165], v153 offset:3072
	v_add_u32_e32 v153, s19, v151
	ds_read_b128 v[166:169], v153
	ds_read_b128 v[170:173], v153 offset:1024
	ds_read_b128 v[174:177], v153 offset:2048
	ds_read_b128 v[178:181], v153 offset:3072
	s_add_u32 s16, s52, 0x80000
	s_addc_u32 s17, s53, 0
	s_mov_b32 m0, s8
	v_lshl_add_u64 v[228:229], s[16:17], 0, v[130:131]
	ds_read_b128 v[182:185], v152 offset:32768
	ds_read_b128 v[186:189], v152 offset:33792
	ds_read_b128 v[190:193], v152 offset:34816
	ds_read_b128 v[194:197], v152 offset:35840
	ds_read_b128 v[198:201], v152 offset:36864
	ds_read_b128 v[202:205], v152 offset:37888
	ds_read_b128 v[206:209], v152 offset:38912
	ds_read_b128 v[210:213], v152 offset:39936
	global_load_lds_dwordx4 v[228:229], off
	v_lshl_add_u64 v[228:229], s[16:17], 0, v[132:133]
	s_mov_b32 m0, s9
	s_nop 0
	global_load_lds_dwordx4 v[228:229], off
	s_waitcnt vmcnt(8)
	s_waitcnt lgkmcnt(0)
	s_barrier
	s_waitcnt lgkmcnt(0)
	v_mfma_f32_16x16x32_bf16 v[126:129], v[144:147], v[182:185], v[126:129]
	v_mfma_f32_16x16x32_bf16 v[122:125], v[158:161], v[182:185], v[122:125]
	v_mfma_f32_16x16x32_bf16 v[114:117], v[144:147], v[190:193], v[114:117]
	v_mfma_f32_16x16x32_bf16 v[106:109], v[158:161], v[190:193], v[106:109]
	v_mfma_f32_16x16x32_bf16 v[94:97], v[144:147], v[198:201], v[94:97]
	v_mfma_f32_16x16x32_bf16 v[90:93], v[158:161], v[198:201], v[90:93]
	v_mfma_f32_16x16x32_bf16 v[82:85], v[144:147], v[206:209], v[82:85]
	v_mfma_f32_16x16x32_bf16 v[74:77], v[158:161], v[206:209], v[74:77]
	v_mfma_f32_16x16x32_bf16 v[126:129], v[154:157], v[186:189], v[126:129]
	v_mfma_f32_16x16x32_bf16 v[122:125], v[162:165], v[186:189], v[122:125]
	v_mfma_f32_16x16x32_bf16 v[114:117], v[154:157], v[194:197], v[114:117]
	v_mfma_f32_16x16x32_bf16 v[106:109], v[162:165], v[194:197], v[106:109]
	v_mfma_f32_16x16x32_bf16 v[94:97], v[154:157], v[202:205], v[94:97]
	v_mfma_f32_16x16x32_bf16 v[90:93], v[162:165], v[202:205], v[90:93]
	v_mfma_f32_16x16x32_bf16 v[82:85], v[154:157], v[210:213], v[82:85]
	v_mfma_f32_16x16x32_bf16 v[74:77], v[162:165], v[210:213], v[74:77]
	v_mfma_f32_16x16x32_bf16 v[118:121], v[166:169], v[182:185], v[118:121]
	v_mfma_f32_16x16x32_bf16 v[110:113], v[174:177], v[182:185], v[110:113]
	v_mfma_f32_16x16x32_bf16 v[102:105], v[166:169], v[190:193], v[102:105]
	v_mfma_f32_16x16x32_bf16 v[98:101], v[174:177], v[190:193], v[98:101]
	v_mfma_f32_16x16x32_bf16 v[86:89], v[166:169], v[198:201], v[86:89]
	v_mfma_f32_16x16x32_bf16 v[78:81], v[174:177], v[198:201], v[78:81]
	v_mfma_f32_16x16x32_bf16 v[70:73], v[166:169], v[206:209], v[70:73]
	v_mfma_f32_16x16x32_bf16 v[66:69], v[174:177], v[206:209], v[66:69]
	v_mfma_f32_16x16x32_bf16 v[118:121], v[170:173], v[186:189], v[118:121]
	v_mfma_f32_16x16x32_bf16 v[110:113], v[178:181], v[186:189], v[110:113]
	v_mfma_f32_16x16x32_bf16 v[102:105], v[170:173], v[194:197], v[102:105]
	v_mfma_f32_16x16x32_bf16 v[98:101], v[178:181], v[194:197], v[98:101]
	v_mfma_f32_16x16x32_bf16 v[86:89], v[170:173], v[202:205], v[86:89]
	v_mfma_f32_16x16x32_bf16 v[78:81], v[178:181], v[202:205], v[78:81]
	v_mfma_f32_16x16x32_bf16 v[70:73], v[170:173], v[210:213], v[70:73]
	v_mfma_f32_16x16x32_bf16 v[66:69], v[178:181], v[210:213], v[66:69]
	s_barrier
; #define PG8_STAGE(bufoff, gbase, voff) do { _Pragma("unroll") for (int _i = 0; _i < 2; ++_i) \
;         __builtin_amdgcn_global_load_lds((const unsigned*)((const char*)(gbase) + (voff)[_i]), (LAS unsigned*)(lds + (bufoff) + ldsw + _i * 8192), 16, 0, 0); } while (0)
; #define PG8_STAGE_A(bufoff, h, kp, nx) do { if constexpr (GATHER) { const unsigned _p = (nx) ? ng[h] : cg[h]; unsigned _v[2]; _v[0] = (_p & 0xffffu) * lda + CA2[0]; _v[1] = (_p >> 16) * lda + CA2[1]; PG8_STAGE(bufoff, kp, _v); } \
;         else { PG8_STAGE(bufoff, (kp) + (h) * hstepA, voffA); } } while (0)
; #define PG8_LDA(dst, b, h) do { _Pragma("unroll") for (int m = 0; m < 4; ++m) _Pragma("unroll") for (int k = 0; k < 2; ++k) dst[m][k] = *(const LAS bf16x8*)(lds + PG8_SA(b, h) + aoff + m * 2048 + k * 1024); } while (0)
; #define PG8_MMA(ai, bj, At, Bt) do { __builtin_amdgcn_s_setprio(1); _Pragma("unroll") for (int m = 0; m < 4; ++m) _Pragma("unroll") for (int n = 0; n < 2; ++n) _Pragma("unroll") for (int k = 0; k < 2; ++k) \
;         acc[ai][bj][m][n] = __builtin_amdgcn_mfma_f32_16x16x32_bf16(Bt[n][k], At[m][k], acc[ai][bj][m][n], 0, 0, 0); __builtin_amdgcn_s_setprio(0); } while (0)
; #define PG8_WAIT_V(n) asm volatile("s_waitcnt vmcnt(" #n ")" ::: "memory")
; #define PG8_WAIT_L(n) asm volatile("s_waitcnt lgkmcnt(" #n ")" ::: "memory")
; #define PG8_BAR __builtin_amdgcn_s_barrier()
; #define PG8_SCHED __builtin_amdgcn_sched_barrier(0)
;     ...
;             PG8_LDA(At, 1, 1); PG8_STAGE(PG8_SB(1, 0), b3, voffB); PG8_STAGE(PG8_SB(1, 1), b3 + hstepB, voffB); PG8_STAGE_A(PG8_SA(1, 0), 0, a3, last);
;             PG8_WAIT_V(8); PG8_WAIT_L(0); PG8_BAR; if (cur.amask & 2) { PG8_MMA(1, 0, At, B0); PG8_MMA(1, 1, At, B1); } PG8_BAR; PG8_SCHED;
;         }
	s_add_i32 s16, s18, s43
	v_lshl_add_u64 v[148:149], v[148:149], 0, s[92:93]
	s_mov_b32 m0, s16
	ds_read_b128 v[182:185], v152 offset:49152
	ds_read_b128 v[186:189], v152 offset:50176
	ds_read_b128 v[190:193], v152 offset:51200
	ds_read_b128 v[194:197], v152 offset:52224
	ds_read_b128 v[198:201], v152 offset:53248
	ds_read_b128 v[202:205], v152 offset:54272
	ds_read_b128 v[206:209], v152 offset:55296
	ds_read_b128 v[210:213], v152 offset:56320
	global_load_lds_dwordx4 v[148:149], off
	s_add_i32 m0, s16, 0x2000
	s_add_u32 s16, s50, 0x80080
	v_lshl_add_u64 v[148:149], v[214:215], 0, s[92:93]
	s_addc_u32 s17, s51, 0
	s_add_i32 s18, s19, s43
	global_load_lds_dwordx4 v[148:149], off
	v_lshl_add_u64 v[148:149], s[16:17], 0, v[0:1]
	s_mov_b32 m0, s18
	s_nop 0
	global_load_lds_dwordx4 v[148:149], off
	v_lshl_add_u64 v[148:149], s[16:17], 0, v[134:135]
	s_add_i32 m0, s18, 0x2000
	s_nop 0
	global_load_lds_dwordx4 v[148:149], off
	v_lshl_add_u64 v[148:149], v[224:225], 0, s[92:93]
	s_mov_b32 m0, s10
	s_nop 0
	global_load_lds_dwordx4 v[148:149], off
	v_lshl_add_u64 v[148:149], v[226:227], 0, s[92:93]
	s_mov_b32 m0, s11
	s_nop 0
	global_load_lds_dwordx4 v[148:149], off
	s_waitcnt vmcnt(8)
	s_waitcnt lgkmcnt(0)
	s_barrier
	s_waitcnt lgkmcnt(0)
	v_mfma_f32_16x16x32_bf16 v[62:65], v[144:147], v[182:185], v[62:65]
	v_mfma_f32_16x16x32_bf16 v[58:61], v[158:161], v[182:185], v[58:61]
	v_mfma_f32_16x16x32_bf16 v[50:53], v[144:147], v[190:193], v[50:53]
	v_mfma_f32_16x16x32_bf16 v[42:45], v[158:161], v[190:193], v[42:45]
	v_mfma_f32_16x16x32_bf16 v[30:33], v[144:147], v[198:201], v[30:33]
	v_mfma_f32_16x16x32_bf16 v[26:29], v[158:161], v[198:201], v[26:29]
	v_mfma_f32_16x16x32_bf16 v[18:21], v[144:147], v[206:209], v[18:21]
	v_mfma_f32_16x16x32_bf16 v[10:13], v[158:161], v[206:209], v[10:13]
	v_mfma_f32_16x16x32_bf16 v[62:65], v[154:157], v[186:189], v[62:65]
	v_mfma_f32_16x16x32_bf16 v[58:61], v[162:165], v[186:189], v[58:61]
	v_mfma_f32_16x16x32_bf16 v[50:53], v[154:157], v[194:197], v[50:53]
	v_mfma_f32_16x16x32_bf16 v[42:45], v[162:165], v[194:197], v[42:45]
	v_mfma_f32_16x16x32_bf16 v[30:33], v[154:157], v[202:205], v[30:33]
	v_mfma_f32_16x16x32_bf16 v[26:29], v[162:165], v[202:205], v[26:29]
	v_mfma_f32_16x16x32_bf16 v[18:21], v[154:157], v[210:213], v[18:21]
	v_mfma_f32_16x16x32_bf16 v[10:13], v[162:165], v[210:213], v[10:13]
	v_mfma_f32_16x16x32_bf16 v[54:57], v[166:169], v[182:185], v[54:57]
	v_mfma_f32_16x16x32_bf16 v[46:49], v[174:177], v[182:185], v[46:49]
	v_mfma_f32_16x16x32_bf16 v[38:41], v[166:169], v[190:193], v[38:41]
	v_mfma_f32_16x16x32_bf16 v[34:37], v[174:177], v[190:193], v[34:37]
	v_mfma_f32_16x16x32_bf16 v[22:25], v[166:169], v[198:201], v[22:25]
	v_mfma_f32_16x16x32_bf16 v[14:17], v[174:177], v[198:201], v[14:17]
	v_mfma_f32_16x16x32_bf16 v[6:9], v[166:169], v[206:209], v[6:9]
	v_mfma_f32_16x16x32_bf16 v[2:5], v[174:177], v[206:209], v[2:5]
	v_mfma_f32_16x16x32_bf16 v[54:57], v[170:173], v[186:189], v[54:57]
	v_mfma_f32_16x16x32_bf16 v[46:49], v[178:181], v[186:189], v[46:49]
	v_mfma_f32_16x16x32_bf16 v[38:41], v[170:173], v[194:197], v[38:41]
	v_mfma_f32_16x16x32_bf16 v[34:37], v[178:181], v[194:197], v[34:37]
	v_mfma_f32_16x16x32_bf16 v[22:25], v[170:173], v[202:205], v[22:25]
	v_mfma_f32_16x16x32_bf16 v[14:17], v[178:181], v[202:205], v[14:17]
	v_mfma_f32_16x16x32_bf16 v[6:9], v[170:173], v[210:213], v[6:9]
	v_mfma_f32_16x16x32_bf16 v[2:5], v[178:181], v[210:213], v[2:5]
	s_barrier
	s_add_i32 s15, s15, 2
	s_add_u32 s48, s48, 0x100
	s_addc_u32 s49, s49, 0
	s_add_u32 s13, s13, 0x100
	s_addc_u32 s14, s14, 0
	s_cmp_gt_u32 s15, 29
	s_cbranch_scc0 .LBB0_1117
	v_readlane_b32 s14, v252, 14
	v_readlane_b32 s15, v252, 15
	s_and_b64 vcc, exec, s[14:15]
	s_cbranch_vccz .LBB0_1120
	s_barrier

; #define PG8_STAGE(bufoff, gbase, voff) do { _Pragma("unroll") for (int _i = 0; _i < 2; ++_i) \
;         __builtin_amdgcn_global_load_lds((const unsigned*)((const char*)(gbase) + (voff)[_i]), (LAS unsigned*)(lds + (bufoff) + ldsw + _i * 8192), 16, 0, 0); } while (0)
; #define PG8_STAGE_A(bufoff, h, kp, nx) do { if constexpr (GATHER) { const unsigned _p = (nx) ? ng[h] : cg[h]; unsigned _v[2]; _v[0] = (_p & 0xffffu) * lda + CA2[0]; _v[1] = (_p >> 16) * lda + CA2[1]; PG8_STAGE(bufoff, kp, _v); } \
;         else { PG8_STAGE(bufoff, (kp) + (h) * hstepA, voffA); } } while (0)
; #define PG8_LDA(dst, b, h) do { _Pragma("unroll") for (int m = 0; m < 4; ++m) _Pragma("unroll") for (int k = 0; k < 2; ++k) dst[m][k] = *(const LAS bf16x8*)(lds + PG8_SA(b, h) + aoff + m * 2048 + k * 1024); } while (0)
; #define PG8_LDB(dst, b, h) do { _Pragma("unroll") for (int n = 0; n < 2; ++n) _Pragma("unroll") for (int k = 0; k < 2; ++k) dst[n][k] = *(const LAS bf16x8*)(lds + PG8_SB(b, h) + boff + n * 2048 + k * 1024); } while (0)
; #define PG8_MMA(ai, bj, At, Bt) do { __builtin_amdgcn_s_setprio(1); _Pragma("unroll") for (int m = 0; m < 4; ++m) _Pragma("unroll") for (int n = 0; n < 2; ++n) _Pragma("unroll") for (int k = 0; k < 2; ++k) \
;         acc[ai][bj][m][n] = __builtin_amdgcn_mfma_f32_16x16x32_bf16(Bt[n][k], At[m][k], acc[ai][bj][m][n], 0, 0, 0); __builtin_amdgcn_s_setprio(0); } while (0)
; #define PG8_WAIT_V(n) asm volatile("s_waitcnt vmcnt(" #n ")" ::: "memory")
;     ...
;         for (int t = 0; t < nt; t += 2) {
;             const bool last = (t == nt - 2);
;             const char* a1 = cA + (size_t)(t + 1) * kstep;
;             const char* a2 = last ? nA : cA + (size_t)(t + 2) * kstep; const char* b2 = last ? nB : cB + (size_t)(t + 2) * kstep;
;             const char* a3 = a2 + kstep; const char* b3 = b2 + kstep;
;             PG8_LDB(B0, 0, 0); PG8_LDB(B1, 0, 1); PG8_SCHED; PG8_LDA(At, 0, 0); PG8_STAGE_A(PG8_SA(1, 1), 1, a1, false);
;             PG8_WAIT_V(8); PG8_WAIT_L(0); PG8_BAR; if (cur.amask & 1) { PG8_MMA(0, 0, At, B0); PG8_MMA(0, 1, At, B1); } PG8_BAR; PG8_SCHED;
;             PG8_LDA(At, 0, 1); PG8_STAGE(PG8_SB(0, 0), b2, voffB); PG8_STAGE(PG8_SB(0, 1), b2 + hstepB, voffB); PG8_STAGE_A(PG8_SA(0, 0), 0, a2, last);
;             PG8_WAIT_V(8); PG8_WAIT_L(0); PG8_BAR; if (cur.amask & 2) { PG8_MMA(1, 0, At, B0); PG8_MMA(1, 1, At, B1); } PG8_BAR; PG8_SCHED;
.LBB0_1205:
	s_add_u32 s22, s44, 0xfff80080
	s_addc_u32 s23, s45, -1
	s_add_i32 s24, 0, 0x10000
	s_cmp_eq_u32 s21, 28
	s_cselect_b32 s49, s37, s23
	s_cselect_b32 s48, s36, s22
	v_add_u32_e32 v149, s24, v147
	s_cselect_b32 s47, s39, s20
	s_cselect_b32 s46, s38, s19
	s_add_i32 s25, 0, 0x14000
	ds_read_b128 v[142:145], v149
	ds_read_b128 v[150:153], v149 offset:1024
	ds_read_b128 v[154:157], v149 offset:2048
	ds_read_b128 v[158:161], v149 offset:3072
	v_add_u32_e32 v149, s25, v147
	ds_read_b128 v[162:165], v149
	ds_read_b128 v[166:169], v149 offset:1024
	ds_read_b128 v[170:173], v149 offset:2048
	ds_read_b128 v[174:177], v149 offset:3072
	v_lshl_add_u64 v[210:211], s[44:45], 0, v[138:139]
	s_add_i32 m0, s10, 0xc000
	ds_read_b128 v[178:181], v148
	ds_read_b128 v[182:185], v148 offset:1024
	ds_read_b128 v[186:189], v148 offset:2048
	ds_read_b128 v[190:193], v148 offset:3072
	ds_read_b128 v[194:197], v148 offset:4096
	ds_read_b128 v[198:201], v148 offset:5120
	ds_read_b128 v[202:205], v148 offset:6144
	ds_read_b128 v[206:209], v148 offset:7168
	global_load_lds_dwordx4 v[210:211], off
	v_lshl_add_u64 v[210:211], s[44:45], 0, v[140:141]
	s_add_i32 m0, s10, 0xe000
	s_nop 0
	global_load_lds_dwordx4 v[210:211], off
	s_waitcnt vmcnt(8)
	s_waitcnt lgkmcnt(0)
	s_barrier
	s_waitcnt lgkmcnt(0)
	v_mfma_f32_16x16x32_bf16 v[126:129], v[142:145], v[178:181], v[126:129]
	v_mfma_f32_16x16x32_bf16 v[122:125], v[154:157], v[178:181], v[122:125]
	v_mfma_f32_16x16x32_bf16 v[118:121], v[142:145], v[186:189], v[118:121]
	v_mfma_f32_16x16x32_bf16 v[110:113], v[154:157], v[186:189], v[110:113]
	v_mfma_f32_16x16x32_bf16 v[102:105], v[142:145], v[194:197], v[102:105]
	v_mfma_f32_16x16x32_bf16 v[94:97], v[154:157], v[194:197], v[94:97]
	v_mfma_f32_16x16x32_bf16 v[86:89], v[142:145], v[202:205], v[86:89]
	v_mfma_f32_16x16x32_bf16 v[78:81], v[154:157], v[202:205], v[78:81]
	v_mfma_f32_16x16x32_bf16 v[126:129], v[150:153], v[182:185], v[126:129]
	v_mfma_f32_16x16x32_bf16 v[122:125], v[158:161], v[182:185], v[122:125]
	v_mfma_f32_16x16x32_bf16 v[118:121], v[150:153], v[190:193], v[118:121]
	v_mfma_f32_16x16x32_bf16 v[110:113], v[158:161], v[190:193], v[110:113]
	v_mfma_f32_16x16x32_bf16 v[102:105], v[150:153], v[198:201], v[102:105]
	v_mfma_f32_16x16x32_bf16 v[94:97], v[158:161], v[198:201], v[94:97]
	v_mfma_f32_16x16x32_bf16 v[86:89], v[150:153], v[206:209], v[86:89]
	v_mfma_f32_16x16x32_bf16 v[78:81], v[158:161], v[206:209], v[78:81]
	v_mfma_f32_16x16x32_bf16 v[114:117], v[162:165], v[178:181], v[114:117]
	v_mfma_f32_16x16x32_bf16 v[106:109], v[170:173], v[178:181], v[106:109]
	v_mfma_f32_16x16x32_bf16 v[98:101], v[162:165], v[186:189], v[98:101]
	v_mfma_f32_16x16x32_bf16 v[90:93], v[170:173], v[186:189], v[90:93]
	v_mfma_f32_16x16x32_bf16 v[82:85], v[162:165], v[194:197], v[82:85]
	v_mfma_f32_16x16x32_bf16 v[74:77], v[170:173], v[194:197], v[74:77]
	v_mfma_f32_16x16x32_bf16 v[70:73], v[162:165], v[202:205], v[70:73]
	v_mfma_f32_16x16x32_bf16 v[66:69], v[170:173], v[202:205], v[66:69]
	v_mfma_f32_16x16x32_bf16 v[114:117], v[166:169], v[182:185], v[114:117]
	v_mfma_f32_16x16x32_bf16 v[106:109], v[174:177], v[182:185], v[106:109]
	v_mfma_f32_16x16x32_bf16 v[98:101], v[166:169], v[190:193], v[98:101]
	v_mfma_f32_16x16x32_bf16 v[90:93], v[174:177], v[190:193], v[90:93]
	v_mfma_f32_16x16x32_bf16 v[82:85], v[166:169], v[198:201], v[82:85]
	v_mfma_f32_16x16x32_bf16 v[74:77], v[174:177], v[198:201], v[74:77]
	v_mfma_f32_16x16x32_bf16 v[70:73], v[166:169], v[206:209], v[70:73]
	v_mfma_f32_16x16x32_bf16 v[66:69], v[174:177], v[206:209], v[66:69]
	s_barrier
	s_add_i32 s22, s24, s43
	v_lshl_add_u64 v[210:211], s[46:47], 0, v[0:1]
	s_mov_b32 m0, s22
	ds_read_b128 v[178:181], v148 offset:16384
	ds_read_b128 v[182:185], v148 offset:17408
	ds_read_b128 v[186:189], v148 offset:18432
	ds_read_b128 v[190:193], v148 offset:19456
	ds_read_b128 v[194:197], v148 offset:20480
	ds_read_b128 v[198:201], v148 offset:21504
	ds_read_b128 v[202:205], v148 offset:22528
	ds_read_b128 v[206:209], v148 offset:23552
	global_load_lds_dwordx4 v[210:211], off
	s_add_i32 m0, s22, 0x2000
	s_add_u32 s22, s46, 0x80000
	v_lshl_add_u64 v[212:213], s[46:47], 0, v[134:135]
	s_addc_u32 s23, s47, 0
	s_add_i32 s24, s25, s43
	global_load_lds_dwordx4 v[212:213], off
	v_lshl_add_u64 v[214:215], s[22:23], 0, v[0:1]
	s_mov_b32 m0, s24
	v_lshl_add_u64 v[224:225], s[48:49], 0, v[132:133]
	global_load_lds_dwordx4 v[214:215], off
	v_lshl_add_u64 v[214:215], s[22:23], 0, v[134:135]
	s_add_i32 m0, s24, 0x2000
	s_nop 0
	global_load_lds_dwordx4 v[214:215], off
	v_lshl_add_u64 v[214:215], s[48:49], 0, v[130:131]
	s_mov_b32 m0, s10
	s_nop 0
	global_load_lds_dwordx4 v[214:215], off
	s_mov_b32 m0, s11
	s_nop 0
	global_load_lds_dwordx4 v[224:225], off
	s_waitcnt vmcnt(8)
	s_waitcnt lgkmcnt(0)
	s_barrier
; #define PG8_STAGE(bufoff, gbase, voff) do { _Pragma("unroll") for (int _i = 0; _i < 2; ++_i) \
;         __builtin_amdgcn_global_load_lds((const unsigned*)((const char*)(gbase) + (voff)[_i]), (LAS unsigned*)(lds + (bufoff) + ldsw + _i * 8192), 16, 0, 0); } while (0)
; #define PG8_STAGE_A(bufoff, h, kp, nx) do { if constexpr (GATHER) { const unsigned _p = (nx) ? ng[h] : cg[h]; unsigned _v[2]; _v[0] = (_p & 0xffffu) * lda + CA2[0]; _v[1] = (_p >> 16) * lda + CA2[1]; PG8_STAGE(bufoff, kp, _v); } \
;         else { PG8_STAGE(bufoff, (kp) + (h) * hstepA, voffA); } } while (0)
; #define PG8_LDA(dst, b, h) do { _Pragma("unroll") for (int m = 0; m < 4; ++m) _Pragma("unroll") for (int k = 0; k < 2; ++k) dst[m][k] = *(const LAS bf16x8*)(lds + PG8_SA(b, h) + aoff + m * 2048 + k * 1024); } while (0)
; #define PG8_LDB(dst, b, h) do { _Pragma("unroll") for (int n = 0; n < 2; ++n) _Pragma("unroll") for (int k = 0; k < 2; ++k) dst[n][k] = *(const LAS bf16x8*)(lds + PG8_SB(b, h) + boff + n * 2048 + k * 1024); } while (0)
; #define PG8_MMA(ai, bj, At, Bt) do { __builtin_amdgcn_s_setprio(1); _Pragma("unroll") for (int m = 0; m < 4; ++m) _Pragma("unroll") for (int n = 0; n < 2; ++n) _Pragma("unroll") for (int k = 0; k < 2; ++k) \
;         acc[ai][bj][m][n] = __builtin_amdgcn_mfma_f32_16x16x32_bf16(Bt[n][k], At[m][k], acc[ai][bj][m][n], 0, 0, 0); __builtin_amdgcn_s_setprio(0); } while (0)
; #define PG8_WAIT_V(n) asm volatile("s_waitcnt vmcnt(" #n ")" ::: "memory")
; #define PG8_WAIT_L(n) asm volatile("s_waitcnt lgkmcnt(" #n ")" ::: "memory")
; #define PG8_BAR __builtin_amdgcn_s_barrier()
; #define PG8_SCHED __builtin_amdgcn_sched_barrier(0)
;     ...
;             PG8_WAIT_V(8); PG8_WAIT_L(0); PG8_BAR; if (cur.amask & 2) { PG8_MMA(1, 0, At, B0); PG8_MMA(1, 1, At, B1); } PG8_BAR; PG8_SCHED;
;             PG8_LDB(B0, 1, 0); PG8_LDB(B1, 1, 1); PG8_SCHED; PG8_LDA(At, 1, 0); PG8_STAGE_A(PG8_SA(0, 1), 1, a2, last);
;             PG8_WAIT_V(8); PG8_WAIT_L(0); PG8_BAR; if (cur.amask & 1) { PG8_MMA(0, 0, At, B0); PG8_MMA(0, 1, At, B1); } PG8_BAR; PG8_SCHED;
;             PG8_LDA(At, 1, 1); PG8_STAGE(PG8_SB(1, 0), b3, voffB); PG8_STAGE(PG8_SB(1, 1), b3 + hstepB, voffB); PG8_STAGE_A(PG8_SA(1, 0), 0, a3, last);
;             PG8_WAIT_V(8); PG8_WAIT_L(0); PG8_BAR; if (cur.amask & 2) { PG8_MMA(1, 0, At, B0); PG8_MMA(1, 1, At, B1); } PG8_BAR; PG8_SCHED;
	s_waitcnt lgkmcnt(0)
	v_mfma_f32_16x16x32_bf16 v[62:65], v[142:145], v[178:181], v[62:65]
	v_mfma_f32_16x16x32_bf16 v[58:61], v[154:157], v[178:181], v[58:61]
	v_mfma_f32_16x16x32_bf16 v[54:57], v[142:145], v[186:189], v[54:57]
	v_mfma_f32_16x16x32_bf16 v[46:49], v[154:157], v[186:189], v[46:49]
	v_mfma_f32_16x16x32_bf16 v[38:41], v[142:145], v[194:197], v[38:41]
	v_mfma_f32_16x16x32_bf16 v[30:33], v[154:157], v[194:197], v[30:33]
	v_mfma_f32_16x16x32_bf16 v[22:25], v[142:145], v[202:205], v[22:25]
	v_mfma_f32_16x16x32_bf16 v[14:17], v[154:157], v[202:205], v[14:17]
	v_mfma_f32_16x16x32_bf16 v[62:65], v[150:153], v[182:185], v[62:65]
	v_mfma_f32_16x16x32_bf16 v[58:61], v[158:161], v[182:185], v[58:61]
	v_mfma_f32_16x16x32_bf16 v[54:57], v[150:153], v[190:193], v[54:57]
	v_mfma_f32_16x16x32_bf16 v[46:49], v[158:161], v[190:193], v[46:49]
	v_mfma_f32_16x16x32_bf16 v[38:41], v[150:153], v[198:201], v[38:41]
	v_mfma_f32_16x16x32_bf16 v[30:33], v[158:161], v[198:201], v[30:33]
	v_mfma_f32_16x16x32_bf16 v[22:25], v[150:153], v[206:209], v[22:25]
	v_mfma_f32_16x16x32_bf16 v[14:17], v[158:161], v[206:209], v[14:17]
	v_mfma_f32_16x16x32_bf16 v[50:53], v[162:165], v[178:181], v[50:53]
	v_mfma_f32_16x16x32_bf16 v[42:45], v[170:173], v[178:181], v[42:45]
	v_mfma_f32_16x16x32_bf16 v[34:37], v[162:165], v[186:189], v[34:37]
	v_mfma_f32_16x16x32_bf16 v[26:29], v[170:173], v[186:189], v[26:29]
	v_mfma_f32_16x16x32_bf16 v[18:21], v[162:165], v[194:197], v[18:21]
	v_mfma_f32_16x16x32_bf16 v[10:13], v[170:173], v[194:197], v[10:13]
	v_mfma_f32_16x16x32_bf16 v[6:9], v[162:165], v[202:205], v[6:9]
	v_mfma_f32_16x16x32_bf16 v[2:5], v[170:173], v[202:205], v[2:5]
	v_mfma_f32_16x16x32_bf16 v[50:53], v[166:169], v[182:185], v[50:53]
	v_mfma_f32_16x16x32_bf16 v[42:45], v[174:177], v[182:185], v[42:45]
	v_mfma_f32_16x16x32_bf16 v[34:37], v[166:169], v[190:193], v[34:37]
	v_mfma_f32_16x16x32_bf16 v[26:29], v[174:177], v[190:193], v[26:29]
	v_mfma_f32_16x16x32_bf16 v[18:21], v[166:169], v[198:201], v[18:21]
	v_mfma_f32_16x16x32_bf16 v[10:13], v[174:177], v[198:201], v[10:13]
	v_mfma_f32_16x16x32_bf16 v[6:9], v[166:169], v[206:209], v[6:9]
	v_mfma_f32_16x16x32_bf16 v[2:5], v[174:177], v[206:209], v[2:5]
	s_barrier
	s_add_i32 s24, 0, 0x18000
	v_add_u32_e32 v149, s24, v147
	s_add_i32 s25, 0, 0x1c000
	ds_read_b128 v[142:145], v149
	ds_read_b128 v[150:153], v149 offset:1024
	ds_read_b128 v[154:157], v149 offset:2048
	ds_read_b128 v[158:161], v149 offset:3072
	v_add_u32_e32 v149, s25, v147
	ds_read_b128 v[162:165], v149
	ds_read_b128 v[166:169], v149 offset:1024
	ds_read_b128 v[170:173], v149 offset:2048
	ds_read_b128 v[174:177], v149 offset:3072
	s_add_u32 s22, s48, 0x80000
	s_addc_u32 s23, s49, 0
	s_mov_b32 m0, s12
	v_lshl_add_u64 v[226:227], s[22:23], 0, v[130:131]
	ds_read_b128 v[178:181], v148 offset:32768
	ds_read_b128 v[182:185], v148 offset:33792
	ds_read_b128 v[186:189], v148 offset:34816
	ds_read_b128 v[190:193], v148 offset:35840
	ds_read_b128 v[194:197], v148 offset:36864
	ds_read_b128 v[198:201], v148 offset:37888
	ds_read_b128 v[202:205], v148 offset:38912
	ds_read_b128 v[206:209], v148 offset:39936
	global_load_lds_dwordx4 v[226:227], off
	v_lshl_add_u64 v[226:227], s[22:23], 0, v[132:133]
	s_mov_b32 m0, s13
	s_nop 0
	global_load_lds_dwordx4 v[226:227], off
	s_waitcnt vmcnt(8)
	s_waitcnt lgkmcnt(0)
	s_barrier
	s_waitcnt lgkmcnt(0)
	v_mfma_f32_16x16x32_bf16 v[126:129], v[142:145], v[178:181], v[126:129]
	v_mfma_f32_16x16x32_bf16 v[122:125], v[154:157], v[178:181], v[122:125]
	v_mfma_f32_16x16x32_bf16 v[118:121], v[142:145], v[186:189], v[118:121]
	v_mfma_f32_16x16x32_bf16 v[110:113], v[154:157], v[186:189], v[110:113]
	v_mfma_f32_16x16x32_bf16 v[102:105], v[142:145], v[194:197], v[102:105]
	v_mfma_f32_16x16x32_bf16 v[94:97], v[154:157], v[194:197], v[94:97]
	v_mfma_f32_16x16x32_bf16 v[86:89], v[142:145], v[202:205], v[86:89]
	v_mfma_f32_16x16x32_bf16 v[78:81], v[154:157], v[202:205], v[78:81]
	v_mfma_f32_16x16x32_bf16 v[126:129], v[150:153], v[182:185], v[126:129]
	v_mfma_f32_16x16x32_bf16 v[122:125], v[158:161], v[182:185], v[122:125]
	v_mfma_f32_16x16x32_bf16 v[118:121], v[150:153], v[190:193], v[118:121]
	v_mfma_f32_16x16x32_bf16 v[110:113], v[158:161], v[190:193], v[110:113]
	v_mfma_f32_16x16x32_bf16 v[102:105], v[150:153], v[198:201], v[102:105]
	v_mfma_f32_16x16x32_bf16 v[94:97], v[158:161], v[198:201], v[94:97]
	v_mfma_f32_16x16x32_bf16 v[86:89], v[150:153], v[206:209], v[86:89]
	v_mfma_f32_16x16x32_bf16 v[78:81], v[158:161], v[206:209], v[78:81]
	v_mfma_f32_16x16x32_bf16 v[114:117], v[162:165], v[178:181], v[114:117]
	v_mfma_f32_16x16x32_bf16 v[106:109], v[170:173], v[178:181], v[106:109]
	v_mfma_f32_16x16x32_bf16 v[98:101], v[162:165], v[186:189], v[98:101]
	v_mfma_f32_16x16x32_bf16 v[90:93], v[170:173], v[186:189], v[90:93]
	v_mfma_f32_16x16x32_bf16 v[82:85], v[162:165], v[194:197], v[82:85]
	v_mfma_f32_16x16x32_bf16 v[74:77], v[170:173], v[194:197], v[74:77]
	v_mfma_f32_16x16x32_bf16 v[70:73], v[162:165], v[202:205], v[70:73]
	v_mfma_f32_16x16x32_bf16 v[66:69], v[170:173], v[202:205], v[66:69]
	v_mfma_f32_16x16x32_bf16 v[114:117], v[166:169], v[182:185], v[114:117]
	v_mfma_f32_16x16x32_bf16 v[106:109], v[174:177], v[182:185], v[106:109]
	v_mfma_f32_16x16x32_bf16 v[98:101], v[166:169], v[190:193], v[98:101]
	v_mfma_f32_16x16x32_bf16 v[90:93], v[174:177], v[190:193], v[90:93]
	v_mfma_f32_16x16x32_bf16 v[82:85], v[166:169], v[198:201], v[82:85]
	v_mfma_f32_16x16x32_bf16 v[74:77], v[174:177], v[198:201], v[74:77]
	v_mfma_f32_16x16x32_bf16 v[70:73], v[166:169], v[206:209], v[70:73]
	v_mfma_f32_16x16x32_bf16 v[66:69], v[174:177], v[206:209], v[66:69]
	s_barrier
; #define PG8_STAGE(bufoff, gbase, voff) do { _Pragma("unroll") for (int _i = 0; _i < 2; ++_i) \
;         __builtin_amdgcn_global_load_lds((const unsigned*)((const char*)(gbase) + (voff)[_i]), (LAS unsigned*)(lds + (bufoff) + ldsw + _i * 8192), 16, 0, 0); } while (0)
; #define PG8_STAGE_A(bufoff, h, kp, nx) do { if constexpr (GATHER) { const unsigned _p = (nx) ? ng[h] : cg[h]; unsigned _v[2]; _v[0] = (_p & 0xffffu) * lda + CA2[0]; _v[1] = (_p >> 16) * lda + CA2[1]; PG8_STAGE(bufoff, kp, _v); } \
;         else { PG8_STAGE(bufoff, (kp) + (h) * hstepA, voffA); } } while (0)
; #define PG8_LDA(dst, b, h) do { _Pragma("unroll") for (int m = 0; m < 4; ++m) _Pragma("unroll") for (int k = 0; k < 2; ++k) dst[m][k] = *(const LAS bf16x8*)(lds + PG8_SA(b, h) + aoff + m * 2048 + k * 1024); } while (0)
; #define PG8_MMA(ai, bj, At, Bt) do { __builtin_amdgcn_s_setprio(1); _Pragma("unroll") for (int m = 0; m < 4; ++m) _Pragma("unroll") for (int n = 0; n < 2; ++n) _Pragma("unroll") for (int k = 0; k < 2; ++k) \
;         acc[ai][bj][m][n] = __builtin_amdgcn_mfma_f32_16x16x32_bf16(Bt[n][k], At[m][k], acc[ai][bj][m][n], 0, 0, 0); __builtin_amdgcn_s_setprio(0); } while (0)
; #define PG8_WAIT_V(n) asm volatile("s_waitcnt vmcnt(" #n ")" ::: "memory")
; #define PG8_WAIT_L(n) asm volatile("s_waitcnt lgkmcnt(" #n ")" ::: "memory")
; #define PG8_BAR __builtin_amdgcn_s_barrier()
; #define PG8_SCHED __builtin_amdgcn_sched_barrier(0)
;     ...
;             PG8_LDA(At, 1, 1); PG8_STAGE(PG8_SB(1, 0), b3, voffB); PG8_STAGE(PG8_SB(1, 1), b3 + hstepB, voffB); PG8_STAGE_A(PG8_SA(1, 0), 0, a3, last);
;             PG8_WAIT_V(8); PG8_WAIT_L(0); PG8_BAR; if (cur.amask & 2) { PG8_MMA(1, 0, At, B0); PG8_MMA(1, 1, At, B1); } PG8_BAR; PG8_SCHED;
;         }
	s_add_i32 s22, s24, s43
	v_lshl_add_u64 v[210:211], v[210:211], 0, s[92:93]
	s_mov_b32 m0, s22
	ds_read_b128 v[178:181], v148 offset:49152
	ds_read_b128 v[182:185], v148 offset:50176
	ds_read_b128 v[186:189], v148 offset:51200
	ds_read_b128 v[190:193], v148 offset:52224
	ds_read_b128 v[194:197], v148 offset:53248
	ds_read_b128 v[198:201], v148 offset:54272
	ds_read_b128 v[202:205], v148 offset:55296
	ds_read_b128 v[206:209], v148 offset:56320
	global_load_lds_dwordx4 v[210:211], off
	s_add_i32 m0, s22, 0x2000
	s_add_u32 s22, s46, 0x80080
	v_lshl_add_u64 v[210:211], v[212:213], 0, s[92:93]
	s_addc_u32 s23, s47, 0
	s_add_i32 s24, s25, s43
	global_load_lds_dwordx4 v[210:211], off
	v_lshl_add_u64 v[210:211], s[22:23], 0, v[0:1]
	s_mov_b32 m0, s24
	s_nop 0
	global_load_lds_dwordx4 v[210:211], off
	v_lshl_add_u64 v[210:211], s[22:23], 0, v[134:135]
	s_add_i32 m0, s24, 0x2000
	s_nop 0
	global_load_lds_dwordx4 v[210:211], off
	v_lshl_add_u64 v[210:211], v[214:215], 0, s[92:93]
	s_mov_b32 m0, s16
	s_nop 0
	global_load_lds_dwordx4 v[210:211], off
	v_lshl_add_u64 v[210:211], v[224:225], 0, s[92:93]
	s_mov_b32 m0, s17
	s_nop 0
	global_load_lds_dwordx4 v[210:211], off
	s_waitcnt vmcnt(8)
	s_waitcnt lgkmcnt(0)
	s_barrier
	s_waitcnt lgkmcnt(0)
	v_mfma_f32_16x16x32_bf16 v[62:65], v[142:145], v[178:181], v[62:65]
	v_mfma_f32_16x16x32_bf16 v[58:61], v[154:157], v[178:181], v[58:61]
	v_mfma_f32_16x16x32_bf16 v[54:57], v[142:145], v[186:189], v[54:57]
	v_mfma_f32_16x16x32_bf16 v[46:49], v[154:157], v[186:189], v[46:49]
	v_mfma_f32_16x16x32_bf16 v[38:41], v[142:145], v[194:197], v[38:41]
	v_mfma_f32_16x16x32_bf16 v[30:33], v[154:157], v[194:197], v[30:33]
	v_mfma_f32_16x16x32_bf16 v[22:25], v[142:145], v[202:205], v[22:25]
	v_mfma_f32_16x16x32_bf16 v[14:17], v[154:157], v[202:205], v[14:17]
	v_mfma_f32_16x16x32_bf16 v[62:65], v[150:153], v[182:185], v[62:65]
	v_mfma_f32_16x16x32_bf16 v[58:61], v[158:161], v[182:185], v[58:61]
	v_mfma_f32_16x16x32_bf16 v[54:57], v[150:153], v[190:193], v[54:57]
	v_mfma_f32_16x16x32_bf16 v[46:49], v[158:161], v[190:193], v[46:49]
	v_mfma_f32_16x16x32_bf16 v[38:41], v[150:153], v[198:201], v[38:41]
	v_mfma_f32_16x16x32_bf16 v[30:33], v[158:161], v[198:201], v[30:33]
	v_mfma_f32_16x16x32_bf16 v[22:25], v[150:153], v[206:209], v[22:25]
	v_mfma_f32_16x16x32_bf16 v[14:17], v[158:161], v[206:209], v[14:17]
	v_mfma_f32_16x16x32_bf16 v[50:53], v[162:165], v[178:181], v[50:53]
	v_mfma_f32_16x16x32_bf16 v[42:45], v[170:173], v[178:181], v[42:45]
	v_mfma_f32_16x16x32_bf16 v[34:37], v[162:165], v[186:189], v[34:37]
	v_mfma_f32_16x16x32_bf16 v[26:29], v[170:173], v[186:189], v[26:29]
	v_mfma_f32_16x16x32_bf16 v[18:21], v[162:165], v[194:197], v[18:21]
	v_mfma_f32_16x16x32_bf16 v[10:13], v[170:173], v[194:197], v[10:13]
	v_mfma_f32_16x16x32_bf16 v[6:9], v[162:165], v[202:205], v[6:9]
	v_mfma_f32_16x16x32_bf16 v[2:5], v[170:173], v[202:205], v[2:5]
	v_mfma_f32_16x16x32_bf16 v[50:53], v[166:169], v[182:185], v[50:53]
	v_mfma_f32_16x16x32_bf16 v[42:45], v[174:177], v[182:185], v[42:45]
	v_mfma_f32_16x16x32_bf16 v[34:37], v[166:169], v[190:193], v[34:37]
	v_mfma_f32_16x16x32_bf16 v[26:29], v[174:177], v[190:193], v[26:29]
	v_mfma_f32_16x16x32_bf16 v[18:21], v[166:169], v[198:201], v[18:21]
	v_mfma_f32_16x16x32_bf16 v[10:13], v[174:177], v[198:201], v[10:13]
	v_mfma_f32_16x16x32_bf16 v[6:9], v[166:169], v[206:209], v[6:9]
	v_mfma_f32_16x16x32_bf16 v[2:5], v[174:177], v[206:209], v[2:5]
	s_barrier
	s_add_i32 s21, s21, 2
	s_add_u32 s44, s44, 0x100
	s_addc_u32 s45, s45, 0
	s_add_u32 s19, s19, 0x100
	s_addc_u32 s20, s20, 0
	s_cmp_gt_u32 s21, 29
	s_cbranch_scc0 .LBB0_1205
	v_readlane_b32 s20, v252, 14
	v_readlane_b32 s21, v252, 15
	s_and_b64 vcc, exec, s[20:21]
	s_cbranch_vccz .LBB0_1208
	s_barrier

; #define PG8_STAGE(bufoff, gbase, voff) do { _Pragma("unroll") for (int _i = 0; _i < 2; ++_i) \
;         __builtin_amdgcn_global_load_lds((const unsigned*)((const char*)(gbase) + (voff)[_i]), (LAS unsigned*)(lds + (bufoff) + ldsw + _i * 8192), 16, 0, 0); } while (0)
; #define PG8_STAGE_A(bufoff, h, kp, nx) do { if constexpr (GATHER) { const unsigned _p = (nx) ? ng[h] : cg[h]; unsigned _v[2]; _v[0] = (_p & 0xffffu) * lda + CA2[0]; _v[1] = (_p >> 16) * lda + CA2[1]; PG8_STAGE(bufoff, kp, _v); } \
;         else { PG8_STAGE(bufoff, (kp) + (h) * hstepA, voffA); } } while (0)
; #define PG8_LDA(dst, b, h) do { _Pragma("unroll") for (int m = 0; m < 4; ++m) _Pragma("unroll") for (int k = 0; k < 2; ++k) dst[m][k] = *(const LAS bf16x8*)(lds + PG8_SA(b, h) + aoff + m * 2048 + k * 1024); } while (0)
; #define PG8_LDB(dst, b, h) do { _Pragma("unroll") for (int n = 0; n < 2; ++n) _Pragma("unroll") for (int k = 0; k < 2; ++k) dst[n][k] = *(const LAS bf16x8*)(lds + PG8_SB(b, h) + boff + n * 2048 + k * 1024); } while (0)
; #define PG8_MMA(ai, bj, At, Bt) do { __builtin_amdgcn_s_setprio(1); _Pragma("unroll") for (int m = 0; m < 4; ++m) _Pragma("unroll") for (int n = 0; n < 2; ++n) _Pragma("unroll") for (int k = 0; k < 2; ++k) \
;         acc[ai][bj][m][n] = __builtin_amdgcn_mfma_f32_16x16x32_bf16(Bt[n][k], At[m][k], acc[ai][bj][m][n], 0, 0, 0); __builtin_amdgcn_s_setprio(0); } while (0)
; #define PG8_WAIT_V(n) asm volatile("s_waitcnt vmcnt(" #n ")" ::: "memory")
;     ...
;         for (int t = 0; t < nt; t += 2) {
;             const bool last = (t == nt - 2);
;             const char* a1 = cA + (size_t)(t + 1) * kstep;
;             const char* a2 = last ? nA : cA + (size_t)(t + 2) * kstep; const char* b2 = last ? nB : cB + (size_t)(t + 2) * kstep;
;             const char* a3 = a2 + kstep; const char* b3 = b2 + kstep;
;             PG8_LDB(B0, 0, 0); PG8_LDB(B1, 0, 1); PG8_SCHED; PG8_LDA(At, 0, 0); PG8_STAGE_A(PG8_SA(1, 1), 1, a1, false);
;             PG8_WAIT_V(8); PG8_WAIT_L(0); PG8_BAR; if (cur.amask & 1) { PG8_MMA(0, 0, At, B0); PG8_MMA(0, 1, At, B1); } PG8_BAR; PG8_SCHED;
;             PG8_LDA(At, 0, 1); PG8_STAGE(PG8_SB(0, 0), b2, voffB); PG8_STAGE(PG8_SB(0, 1), b2 + hstepB, voffB); PG8_STAGE_A(PG8_SA(0, 0), 0, a2, last);
;             PG8_WAIT_V(8); PG8_WAIT_L(0); PG8_BAR; if (cur.amask & 2) { PG8_MMA(1, 0, At, B0); PG8_MMA(1, 1, At, B1); } PG8_BAR; PG8_SCHED;
.LBB0_1280:
	s_add_u32 s23, s36, s56
	s_addc_u32 s24, s37, s57
	s_add_u32 s23, s23, 0x100
	s_addc_u32 s24, s24, 0
	s_add_u32 s25, s20, s56
	s_addc_u32 s26, s21, s57
	s_add_i32 s27, 0, 0x10000
	s_cmpk_eq_i32 s56, 0x300
	s_cselect_b32 s61, s53, s24
	s_cselect_b32 s60, s52, s23
	s_cselect_b32 s59, s41, s26
	s_cselect_b32 s58, s40, s25
	s_add_i32 s23, 0, 0x14000
	v_add_u32_e32 v160, s27, v146
	v_add_u32_e32 v176, s23, v146
	ds_read_b128 v[148:151], v160
	ds_read_b128 v[152:155], v160 offset:1024
	ds_read_b128 v[156:159], v160 offset:2048
	ds_read_b128 v[160:163], v160 offset:3072
	ds_read_b128 v[164:167], v176
	ds_read_b128 v[168:171], v176 offset:1024
	ds_read_b128 v[172:175], v176 offset:2048
	ds_read_b128 v[176:179], v176 offset:3072
	v_lshl_add_u64 v[212:213], v[140:141], 0, s[56:57]
	s_add_i32 m0, s10, 0xc000
	ds_read_b128 v[180:183], v147
	ds_read_b128 v[184:187], v147 offset:1024
	ds_read_b128 v[188:191], v147 offset:2048
	ds_read_b128 v[192:195], v147 offset:3072
	ds_read_b128 v[196:199], v147 offset:4096
	ds_read_b128 v[200:203], v147 offset:5120
	ds_read_b128 v[204:207], v147 offset:6144
	ds_read_b128 v[208:211], v147 offset:7168
	global_load_lds_dwordx4 v[212:213], off
	v_lshl_add_u64 v[212:213], v[142:143], 0, s[56:57]
	s_add_i32 m0, s10, 0xe000
	s_nop 0
	global_load_lds_dwordx4 v[212:213], off
	s_waitcnt vmcnt(8)
	s_waitcnt lgkmcnt(0)
	s_barrier
	s_waitcnt lgkmcnt(0)
	v_mfma_f32_16x16x32_bf16 v[126:129], v[148:151], v[180:183], v[126:129]
	v_mfma_f32_16x16x32_bf16 v[122:125], v[156:159], v[180:183], v[122:125]
	v_mfma_f32_16x16x32_bf16 v[114:117], v[148:151], v[188:191], v[114:117]
	v_mfma_f32_16x16x32_bf16 v[106:109], v[156:159], v[188:191], v[106:109]
	v_mfma_f32_16x16x32_bf16 v[102:105], v[148:151], v[196:199], v[102:105]
	v_mfma_f32_16x16x32_bf16 v[94:97], v[156:159], v[196:199], v[94:97]
	v_mfma_f32_16x16x32_bf16 v[86:89], v[148:151], v[204:207], v[86:89]
	v_mfma_f32_16x16x32_bf16 v[78:81], v[156:159], v[204:207], v[78:81]
	v_mfma_f32_16x16x32_bf16 v[126:129], v[152:155], v[184:187], v[126:129]
	v_mfma_f32_16x16x32_bf16 v[122:125], v[160:163], v[184:187], v[122:125]
	v_mfma_f32_16x16x32_bf16 v[114:117], v[152:155], v[192:195], v[114:117]
	v_mfma_f32_16x16x32_bf16 v[106:109], v[160:163], v[192:195], v[106:109]
	v_mfma_f32_16x16x32_bf16 v[102:105], v[152:155], v[200:203], v[102:105]
	v_mfma_f32_16x16x32_bf16 v[94:97], v[160:163], v[200:203], v[94:97]
	v_mfma_f32_16x16x32_bf16 v[86:89], v[152:155], v[208:211], v[86:89]
	v_mfma_f32_16x16x32_bf16 v[78:81], v[160:163], v[208:211], v[78:81]
	v_mfma_f32_16x16x32_bf16 v[118:121], v[164:167], v[180:183], v[118:121]
	v_mfma_f32_16x16x32_bf16 v[110:113], v[172:175], v[180:183], v[110:113]
	v_mfma_f32_16x16x32_bf16 v[98:101], v[164:167], v[188:191], v[98:101]
	v_mfma_f32_16x16x32_bf16 v[90:93], v[172:175], v[188:191], v[90:93]
	v_mfma_f32_16x16x32_bf16 v[82:85], v[164:167], v[196:199], v[82:85]
	v_mfma_f32_16x16x32_bf16 v[74:77], v[172:175], v[196:199], v[74:77]
	v_mfma_f32_16x16x32_bf16 v[70:73], v[164:167], v[204:207], v[70:73]
	v_mfma_f32_16x16x32_bf16 v[66:69], v[172:175], v[204:207], v[66:69]
	v_mfma_f32_16x16x32_bf16 v[118:121], v[168:171], v[184:187], v[118:121]
	v_mfma_f32_16x16x32_bf16 v[110:113], v[176:179], v[184:187], v[110:113]
	v_mfma_f32_16x16x32_bf16 v[98:101], v[168:171], v[192:195], v[98:101]
	v_mfma_f32_16x16x32_bf16 v[90:93], v[176:179], v[192:195], v[90:93]
	v_mfma_f32_16x16x32_bf16 v[82:85], v[168:171], v[200:203], v[82:85]
	v_mfma_f32_16x16x32_bf16 v[74:77], v[176:179], v[200:203], v[74:77]
	v_mfma_f32_16x16x32_bf16 v[70:73], v[168:171], v[208:211], v[70:73]
	v_mfma_f32_16x16x32_bf16 v[66:69], v[176:179], v[208:211], v[66:69]
	s_barrier
	s_add_i32 s24, s27, s43
	v_lshl_add_u64 v[212:213], s[58:59], 0, v[0:1]
	s_mov_b32 m0, s24
	ds_read_b128 v[180:183], v147 offset:16384
	ds_read_b128 v[184:187], v147 offset:17408
	ds_read_b128 v[188:191], v147 offset:18432
	ds_read_b128 v[192:195], v147 offset:19456
	ds_read_b128 v[196:199], v147 offset:20480
	ds_read_b128 v[200:203], v147 offset:21504
	ds_read_b128 v[204:207], v147 offset:22528
	ds_read_b128 v[208:211], v147 offset:23552
	global_load_lds_dwordx4 v[212:213], off
	s_add_i32 m0, s24, 0x2000
	s_add_u32 s24, s58, 0x80000
	v_lshl_add_u64 v[214:215], s[58:59], 0, v[130:131]
	s_addc_u32 s25, s59, 0
	s_add_i32 s23, s23, s43
	global_load_lds_dwordx4 v[214:215], off
	v_lshl_add_u64 v[224:225], s[24:25], 0, v[0:1]
	s_mov_b32 m0, s23
	v_lshl_add_u64 v[226:227], s[60:61], 0, v[132:133]
	global_load_lds_dwordx4 v[224:225], off
	v_lshl_add_u64 v[224:225], s[24:25], 0, v[130:131]
	s_add_i32 m0, s23, 0x2000
	s_nop 0
	global_load_lds_dwordx4 v[224:225], off
	v_lshl_add_u64 v[224:225], s[60:61], 0, v[134:135]
	s_mov_b32 m0, s10
	s_nop 0
	global_load_lds_dwordx4 v[224:225], off
	s_mov_b32 m0, s11
	s_nop 0
	global_load_lds_dwordx4 v[226:227], off
	s_waitcnt vmcnt(8)
	s_waitcnt lgkmcnt(0)
	s_barrier
; #define PG8_STAGE(bufoff, gbase, voff) do { _Pragma("unroll") for (int _i = 0; _i < 2; ++_i) \
;         __builtin_amdgcn_global_load_lds((const unsigned*)((const char*)(gbase) + (voff)[_i]), (LAS unsigned*)(lds + (bufoff) + ldsw + _i * 8192), 16, 0, 0); } while (0)
; #define PG8_STAGE_A(bufoff, h, kp, nx) do { if constexpr (GATHER) { const unsigned _p = (nx) ? ng[h] : cg[h]; unsigned _v[2]; _v[0] = (_p & 0xffffu) * lda + CA2[0]; _v[1] = (_p >> 16) * lda + CA2[1]; PG8_STAGE(bufoff, kp, _v); } \
;         else { PG8_STAGE(bufoff, (kp) + (h) * hstepA, voffA); } } while (0)
; #define PG8_LDA(dst, b, h) do { _Pragma("unroll") for (int m = 0; m < 4; ++m) _Pragma("unroll") for (int k = 0; k < 2; ++k) dst[m][k] = *(const LAS bf16x8*)(lds + PG8_SA(b, h) + aoff + m * 2048 + k * 1024); } while (0)
; #define PG8_LDB(dst, b, h) do { _Pragma("unroll") for (int n = 0; n < 2; ++n) _Pragma("unroll") for (int k = 0; k < 2; ++k) dst[n][k] = *(const LAS bf16x8*)(lds + PG8_SB(b, h) + boff + n * 2048 + k * 1024); } while (0)
; #define PG8_MMA(ai, bj, At, Bt) do { __builtin_amdgcn_s_setprio(1); _Pragma("unroll") for (int m = 0; m < 4; ++m) _Pragma("unroll") for (int n = 0; n < 2; ++n) _Pragma("unroll") for (int k = 0; k < 2; ++k) \
;         acc[ai][bj][m][n] = __builtin_amdgcn_mfma_f32_16x16x32_bf16(Bt[n][k], At[m][k], acc[ai][bj][m][n], 0, 0, 0); __builtin_amdgcn_s_setprio(0); } while (0)
; #define PG8_WAIT_V(n) asm volatile("s_waitcnt vmcnt(" #n ")" ::: "memory")
; #define PG8_WAIT_L(n) asm volatile("s_waitcnt lgkmcnt(" #n ")" ::: "memory")
; #define PG8_BAR __builtin_amdgcn_s_barrier()
; #define PG8_SCHED __builtin_amdgcn_sched_barrier(0)
;     ...
;             PG8_WAIT_V(8); PG8_WAIT_L(0); PG8_BAR; if (cur.amask & 2) { PG8_MMA(1, 0, At, B0); PG8_MMA(1, 1, At, B1); } PG8_BAR; PG8_SCHED;
;             PG8_LDB(B0, 1, 0); PG8_LDB(B1, 1, 1); PG8_SCHED; PG8_LDA(At, 1, 0); PG8_STAGE_A(PG8_SA(0, 1), 1, a2, last);
;             PG8_WAIT_V(8); PG8_WAIT_L(0); PG8_BAR; if (cur.amask & 1) { PG8_MMA(0, 0, At, B0); PG8_MMA(0, 1, At, B1); } PG8_BAR; PG8_SCHED;
;             PG8_LDA(At, 1, 1); PG8_STAGE(PG8_SB(1, 0), b3, voffB); PG8_STAGE(PG8_SB(1, 1), b3 + hstepB, voffB); PG8_STAGE_A(PG8_SA(1, 0), 0, a3, last);
;             PG8_WAIT_V(8); PG8_WAIT_L(0); PG8_BAR; if (cur.amask & 2) { PG8_MMA(1, 0, At, B0); PG8_MMA(1, 1, At, B1); } PG8_BAR; PG8_SCHED;
	s_waitcnt lgkmcnt(0)
	v_mfma_f32_16x16x32_bf16 v[62:65], v[148:151], v[180:183], v[62:65]
	v_mfma_f32_16x16x32_bf16 v[58:61], v[156:159], v[180:183], v[58:61]
	v_mfma_f32_16x16x32_bf16 v[54:57], v[148:151], v[188:191], v[54:57]
	v_mfma_f32_16x16x32_bf16 v[46:49], v[156:159], v[188:191], v[46:49]
	v_mfma_f32_16x16x32_bf16 v[38:41], v[148:151], v[196:199], v[38:41]
	v_mfma_f32_16x16x32_bf16 v[30:33], v[156:159], v[196:199], v[30:33]
	v_mfma_f32_16x16x32_bf16 v[22:25], v[148:151], v[204:207], v[22:25]
	v_mfma_f32_16x16x32_bf16 v[14:17], v[156:159], v[204:207], v[14:17]
	v_mfma_f32_16x16x32_bf16 v[62:65], v[152:155], v[184:187], v[62:65]
	v_mfma_f32_16x16x32_bf16 v[58:61], v[160:163], v[184:187], v[58:61]
	v_mfma_f32_16x16x32_bf16 v[54:57], v[152:155], v[192:195], v[54:57]
	v_mfma_f32_16x16x32_bf16 v[46:49], v[160:163], v[192:195], v[46:49]
	v_mfma_f32_16x16x32_bf16 v[38:41], v[152:155], v[200:203], v[38:41]
	v_mfma_f32_16x16x32_bf16 v[30:33], v[160:163], v[200:203], v[30:33]
	v_mfma_f32_16x16x32_bf16 v[22:25], v[152:155], v[208:211], v[22:25]
	v_mfma_f32_16x16x32_bf16 v[14:17], v[160:163], v[208:211], v[14:17]
	v_mfma_f32_16x16x32_bf16 v[50:53], v[164:167], v[180:183], v[50:53]
	v_mfma_f32_16x16x32_bf16 v[42:45], v[172:175], v[180:183], v[42:45]
	v_mfma_f32_16x16x32_bf16 v[34:37], v[164:167], v[188:191], v[34:37]
	v_mfma_f32_16x16x32_bf16 v[26:29], v[172:175], v[188:191], v[26:29]
	v_mfma_f32_16x16x32_bf16 v[18:21], v[164:167], v[196:199], v[18:21]
	v_mfma_f32_16x16x32_bf16 v[10:13], v[172:175], v[196:199], v[10:13]
	v_mfma_f32_16x16x32_bf16 v[6:9], v[164:167], v[204:207], v[6:9]
	v_mfma_f32_16x16x32_bf16 v[2:5], v[172:175], v[204:207], v[2:5]
	v_mfma_f32_16x16x32_bf16 v[50:53], v[168:171], v[184:187], v[50:53]
	v_mfma_f32_16x16x32_bf16 v[42:45], v[176:179], v[184:187], v[42:45]
	v_mfma_f32_16x16x32_bf16 v[34:37], v[168:171], v[192:195], v[34:37]
	v_mfma_f32_16x16x32_bf16 v[26:29], v[176:179], v[192:195], v[26:29]
	v_mfma_f32_16x16x32_bf16 v[18:21], v[168:171], v[200:203], v[18:21]
	v_mfma_f32_16x16x32_bf16 v[10:13], v[176:179], v[200:203], v[10:13]
	v_mfma_f32_16x16x32_bf16 v[6:9], v[168:171], v[208:211], v[6:9]
	v_mfma_f32_16x16x32_bf16 v[2:5], v[176:179], v[208:211], v[2:5]
	s_barrier
	s_add_i32 s23, 0, 0x18000
	s_add_i32 s26, 0, 0x1c000
	v_add_u32_e32 v160, s23, v146
	v_add_u32_e32 v176, s26, v146
	ds_read_b128 v[148:151], v160
	ds_read_b128 v[152:155], v160 offset:1024
	ds_read_b128 v[156:159], v160 offset:2048
	ds_read_b128 v[160:163], v160 offset:3072
	ds_read_b128 v[164:167], v176
	ds_read_b128 v[168:171], v176 offset:1024
	ds_read_b128 v[172:175], v176 offset:2048
	ds_read_b128 v[176:179], v176 offset:3072
	s_add_u32 s24, s60, 0x80000
	s_addc_u32 s25, s61, 0
	s_mov_b32 m0, s12
	v_lshl_add_u64 v[228:229], s[24:25], 0, v[134:135]
	ds_read_b128 v[180:183], v147 offset:32768
	ds_read_b128 v[184:187], v147 offset:33792
	ds_read_b128 v[188:191], v147 offset:34816
	ds_read_b128 v[192:195], v147 offset:35840
	ds_read_b128 v[196:199], v147 offset:36864
	ds_read_b128 v[200:203], v147 offset:37888
	ds_read_b128 v[204:207], v147 offset:38912
	ds_read_b128 v[208:211], v147 offset:39936
	global_load_lds_dwordx4 v[228:229], off
	v_lshl_add_u64 v[228:229], s[24:25], 0, v[132:133]
	s_mov_b32 m0, s13
	s_nop 0
	global_load_lds_dwordx4 v[228:229], off
	s_waitcnt vmcnt(8)
	s_waitcnt lgkmcnt(0)
	s_barrier
	s_waitcnt lgkmcnt(0)
	v_mfma_f32_16x16x32_bf16 v[126:129], v[148:151], v[180:183], v[126:129]
	v_mfma_f32_16x16x32_bf16 v[122:125], v[156:159], v[180:183], v[122:125]
	v_mfma_f32_16x16x32_bf16 v[114:117], v[148:151], v[188:191], v[114:117]
	v_mfma_f32_16x16x32_bf16 v[106:109], v[156:159], v[188:191], v[106:109]
	v_mfma_f32_16x16x32_bf16 v[102:105], v[148:151], v[196:199], v[102:105]
	v_mfma_f32_16x16x32_bf16 v[94:97], v[156:159], v[196:199], v[94:97]
	v_mfma_f32_16x16x32_bf16 v[86:89], v[148:151], v[204:207], v[86:89]
	v_mfma_f32_16x16x32_bf16 v[78:81], v[156:159], v[204:207], v[78:81]
	v_mfma_f32_16x16x32_bf16 v[126:129], v[152:155], v[184:187], v[126:129]
	v_mfma_f32_16x16x32_bf16 v[122:125], v[160:163], v[184:187], v[122:125]
	v_mfma_f32_16x16x32_bf16 v[114:117], v[152:155], v[192:195], v[114:117]
	v_mfma_f32_16x16x32_bf16 v[106:109], v[160:163], v[192:195], v[106:109]
	v_mfma_f32_16x16x32_bf16 v[102:105], v[152:155], v[200:203], v[102:105]
	v_mfma_f32_16x16x32_bf16 v[94:97], v[160:163], v[200:203], v[94:97]
	v_mfma_f32_16x16x32_bf16 v[86:89], v[152:155], v[208:211], v[86:89]
	v_mfma_f32_16x16x32_bf16 v[78:81], v[160:163], v[208:211], v[78:81]
	v_mfma_f32_16x16x32_bf16 v[118:121], v[164:167], v[180:183], v[118:121]
	v_mfma_f32_16x16x32_bf16 v[110:113], v[172:175], v[180:183], v[110:113]
	v_mfma_f32_16x16x32_bf16 v[98:101], v[164:167], v[188:191], v[98:101]
	v_mfma_f32_16x16x32_bf16 v[90:93], v[172:175], v[188:191], v[90:93]
	v_mfma_f32_16x16x32_bf16 v[82:85], v[164:167], v[196:199], v[82:85]
	v_mfma_f32_16x16x32_bf16 v[74:77], v[172:175], v[196:199], v[74:77]
	v_mfma_f32_16x16x32_bf16 v[70:73], v[164:167], v[204:207], v[70:73]
	v_mfma_f32_16x16x32_bf16 v[66:69], v[172:175], v[204:207], v[66:69]
	v_mfma_f32_16x16x32_bf16 v[118:121], v[168:171], v[184:187], v[118:121]
	v_mfma_f32_16x16x32_bf16 v[110:113], v[176:179], v[184:187], v[110:113]
	v_mfma_f32_16x16x32_bf16 v[98:101], v[168:171], v[192:195], v[98:101]
	v_mfma_f32_16x16x32_bf16 v[90:93], v[176:179], v[192:195], v[90:93]
	v_mfma_f32_16x16x32_bf16 v[82:85], v[168:171], v[200:203], v[82:85]
	v_mfma_f32_16x16x32_bf16 v[74:77], v[176:179], v[200:203], v[74:77]
	v_mfma_f32_16x16x32_bf16 v[70:73], v[168:171], v[208:211], v[70:73]
	v_mfma_f32_16x16x32_bf16 v[66:69], v[176:179], v[208:211], v[66:69]
	s_barrier
; #define PG8_STAGE(bufoff, gbase, voff) do { _Pragma("unroll") for (int _i = 0; _i < 2; ++_i) \
;         __builtin_amdgcn_global_load_lds((const unsigned*)((const char*)(gbase) + (voff)[_i]), (LAS unsigned*)(lds + (bufoff) + ldsw + _i * 8192), 16, 0, 0); } while (0)
; #define PG8_STAGE_A(bufoff, h, kp, nx) do { if constexpr (GATHER) { const unsigned _p = (nx) ? ng[h] : cg[h]; unsigned _v[2]; _v[0] = (_p & 0xffffu) * lda + CA2[0]; _v[1] = (_p >> 16) * lda + CA2[1]; PG8_STAGE(bufoff, kp, _v); } \
;         else { PG8_STAGE(bufoff, (kp) + (h) * hstepA, voffA); } } while (0)
; #define PG8_LDA(dst, b, h) do { _Pragma("unroll") for (int m = 0; m < 4; ++m) _Pragma("unroll") for (int k = 0; k < 2; ++k) dst[m][k] = *(const LAS bf16x8*)(lds + PG8_SA(b, h) + aoff + m * 2048 + k * 1024); } while (0)
; #define PG8_MMA(ai, bj, At, Bt) do { __builtin_amdgcn_s_setprio(1); _Pragma("unroll") for (int m = 0; m < 4; ++m) _Pragma("unroll") for (int n = 0; n < 2; ++n) _Pragma("unroll") for (int k = 0; k < 2; ++k) \
;         acc[ai][bj][m][n] = __builtin_amdgcn_mfma_f32_16x16x32_bf16(Bt[n][k], At[m][k], acc[ai][bj][m][n], 0, 0, 0); __builtin_amdgcn_s_setprio(0); } while (0)
; #define PG8_WAIT_V(n) asm volatile("s_waitcnt vmcnt(" #n ")" ::: "memory")
; #define PG8_WAIT_L(n) asm volatile("s_waitcnt lgkmcnt(" #n ")" ::: "memory")
; #define PG8_BAR __builtin_amdgcn_s_barrier()
; #define PG8_SCHED __builtin_amdgcn_sched_barrier(0)
;     ...
;             PG8_LDA(At, 1, 1); PG8_STAGE(PG8_SB(1, 0), b3, voffB); PG8_STAGE(PG8_SB(1, 1), b3 + hstepB, voffB); PG8_STAGE_A(PG8_SA(1, 0), 0, a3, last);
;             PG8_WAIT_V(8); PG8_WAIT_L(0); PG8_BAR; if (cur.amask & 2) { PG8_MMA(1, 0, At, B0); PG8_MMA(1, 1, At, B1); } PG8_BAR; PG8_SCHED;
;         }
;     ...
; #pragma unroll
;         for (int a = 0; a < 2; ++a)
; #pragma unroll
;             for (int b = 0; b < 2; ++b)
; #pragma unroll
;                 for (int m = 0; m < 4; ++m)
; #pragma unroll
;                     for (int n = 0; n < 2; ++n) acc[a][b][m][n] = (f32x4){0.f, 0.f, 0.f, 0.f};
;         cur = nxt; cA = nA; cB = nB; ++ui; nt = PG8_NT(cur);
	s_add_i32 s23, s23, s43
	v_lshl_add_u64 v[212:213], v[212:213], 0, s[92:93]
	s_mov_b32 m0, s23
	ds_read_b128 v[180:183], v147 offset:49152
	ds_read_b128 v[184:187], v147 offset:50176
	ds_read_b128 v[188:191], v147 offset:51200
	ds_read_b128 v[192:195], v147 offset:52224
	ds_read_b128 v[196:199], v147 offset:53248
	ds_read_b128 v[200:203], v147 offset:54272
	ds_read_b128 v[204:207], v147 offset:55296
	ds_read_b128 v[208:211], v147 offset:56320
	global_load_lds_dwordx4 v[212:213], off
	s_add_i32 m0, s23, 0x2000
	s_add_u32 s24, s58, 0x80080
	v_lshl_add_u64 v[212:213], v[214:215], 0, s[92:93]
	s_addc_u32 s25, s59, 0
	s_add_i32 s23, s26, s43
	global_load_lds_dwordx4 v[212:213], off
	v_lshl_add_u64 v[212:213], s[24:25], 0, v[0:1]
	s_mov_b32 m0, s23
	s_nop 0
	global_load_lds_dwordx4 v[212:213], off
	v_lshl_add_u64 v[212:213], s[24:25], 0, v[130:131]
	s_add_i32 m0, s23, 0x2000
	s_nop 0
	global_load_lds_dwordx4 v[212:213], off
	v_lshl_add_u64 v[212:213], v[224:225], 0, s[92:93]
	s_mov_b32 m0, s16
	s_nop 0
	global_load_lds_dwordx4 v[212:213], off
	v_lshl_add_u64 v[212:213], v[226:227], 0, s[92:93]
	s_mov_b32 m0, s17
	s_nop 0
	global_load_lds_dwordx4 v[212:213], off
	s_waitcnt vmcnt(8)
	s_waitcnt lgkmcnt(0)
	s_barrier
	s_waitcnt lgkmcnt(0)
	v_mfma_f32_16x16x32_bf16 v[62:65], v[148:151], v[180:183], v[62:65]
	v_mfma_f32_16x16x32_bf16 v[58:61], v[156:159], v[180:183], v[58:61]
	v_mfma_f32_16x16x32_bf16 v[54:57], v[148:151], v[188:191], v[54:57]
	v_mfma_f32_16x16x32_bf16 v[46:49], v[156:159], v[188:191], v[46:49]
	v_mfma_f32_16x16x32_bf16 v[38:41], v[148:151], v[196:199], v[38:41]
	v_mfma_f32_16x16x32_bf16 v[30:33], v[156:159], v[196:199], v[30:33]
	v_mfma_f32_16x16x32_bf16 v[22:25], v[148:151], v[204:207], v[22:25]
	v_mfma_f32_16x16x32_bf16 v[14:17], v[156:159], v[204:207], v[14:17]
	v_mfma_f32_16x16x32_bf16 v[62:65], v[152:155], v[184:187], v[62:65]
	v_mfma_f32_16x16x32_bf16 v[58:61], v[160:163], v[184:187], v[58:61]
	v_mfma_f32_16x16x32_bf16 v[54:57], v[152:155], v[192:195], v[54:57]
	v_mfma_f32_16x16x32_bf16 v[46:49], v[160:163], v[192:195], v[46:49]
	v_mfma_f32_16x16x32_bf16 v[38:41], v[152:155], v[200:203], v[38:41]
	v_mfma_f32_16x16x32_bf16 v[30:33], v[160:163], v[200:203], v[30:33]
	v_mfma_f32_16x16x32_bf16 v[22:25], v[152:155], v[208:211], v[22:25]
	v_mfma_f32_16x16x32_bf16 v[14:17], v[160:163], v[208:211], v[14:17]
	v_mfma_f32_16x16x32_bf16 v[50:53], v[164:167], v[180:183], v[50:53]
	v_mfma_f32_16x16x32_bf16 v[42:45], v[172:175], v[180:183], v[42:45]
	v_mfma_f32_16x16x32_bf16 v[34:37], v[164:167], v[188:191], v[34:37]
	v_mfma_f32_16x16x32_bf16 v[26:29], v[172:175], v[188:191], v[26:29]
	v_mfma_f32_16x16x32_bf16 v[18:21], v[164:167], v[196:199], v[18:21]
	v_mfma_f32_16x16x32_bf16 v[10:13], v[172:175], v[196:199], v[10:13]
	v_mfma_f32_16x16x32_bf16 v[6:9], v[164:167], v[204:207], v[6:9]
	v_mfma_f32_16x16x32_bf16 v[2:5], v[172:175], v[204:207], v[2:5]
	v_mfma_f32_16x16x32_bf16 v[50:53], v[168:171], v[184:187], v[50:53]
	v_mfma_f32_16x16x32_bf16 v[42:45], v[176:179], v[184:187], v[42:45]
	v_mfma_f32_16x16x32_bf16 v[34:37], v[168:171], v[192:195], v[34:37]
	v_mfma_f32_16x16x32_bf16 v[26:29], v[176:179], v[192:195], v[26:29]
	v_mfma_f32_16x16x32_bf16 v[18:21], v[168:171], v[200:203], v[18:21]
	v_mfma_f32_16x16x32_bf16 v[10:13], v[176:179], v[200:203], v[10:13]
	v_mfma_f32_16x16x32_bf16 v[6:9], v[168:171], v[208:211], v[6:9]
	v_mfma_f32_16x16x32_bf16 v[2:5], v[176:179], v[208:211], v[2:5]
	s_barrier
	s_add_i32 s22, s22, 2
	s_add_u32 s56, s56, 0x100
	s_addc_u32 s57, s57, 0
	s_cmp_gt_u32 s22, 5
	s_cbranch_scc0 .LBB0_1280
	s_add_u32 s56, s20, 0xffffff00
	s_addc_u32 s57, s21, -1
	s_andn2_b64 vcc, exec, s[50:51]
	s_cbranch_vccnz .LBB0_1283
	v_mov_b32_e32 v2, 0
	s_mov_b64 s[4:5], s[38:39]
	s_mov_b64 s[36:37], s[52:53]
	s_mov_b32 s18, s19
	v_mov_b32_e32 v3, v2
	v_mov_b32_e32 v4, v2
	v_mov_b32_e32 v5, v2
	v_mov_b32_e32 v6, v2
	v_mov_b32_e32 v7, v2
	v_mov_b32_e32 v8, v2
	v_mov_b32_e32 v9, v2
	v_mov_b32_e32 v10, v2
	v_mov_b32_e32 v11, v2
	v_mov_b32_e32 v12, v2
	v_mov_b32_e32 v13, v2
	v_mov_b32_e32 v18, v2
	v_mov_b32_e32 v19, v2
	v_mov_b32_e32 v20, v2
	v_mov_b32_e32 v21, v2
	v_mov_b32_e32 v26, v2
	v_mov_b32_e32 v27, v2
	v_mov_b32_e32 v28, v2
	v_mov_b32_e32 v29, v2
	v_mov_b32_e32 v34, v2
	v_mov_b32_e32 v35, v2
	v_mov_b32_e32 v36, v2
	v_mov_b32_e32 v37, v2
	v_mov_b32_e32 v42, v2
	v_mov_b32_e32 v43, v2
	v_mov_b32_e32 v44, v2
	v_mov_b32_e32 v45, v2
	v_mov_b32_e32 v50, v2
	v_mov_b32_e32 v51, v2
	v_mov_b32_e32 v52, v2
	v_mov_b32_e32 v53, v2
	v_mov_b32_e32 v14, v2
	v_mov_b32_e32 v15, v2
	v_mov_b32_e32 v16, v2
	v_mov_b32_e32 v17, v2
	v_mov_b32_e32 v22, v2
	v_mov_b32_e32 v23, v2
	v_mov_b32_e32 v24, v2
	v_mov_b32_e32 v25, v2
	v_mov_b32_e32 v30, v2
	v_mov_b32_e32 v31, v2
	v_mov_b32_e32 v32, v2
	v_mov_b32_e32 v33, v2
	v_mov_b32_e32 v38, v2
	v_mov_b32_e32 v39, v2
	v_mov_b32_e32 v40, v2
	v_mov_b32_e32 v41, v2
	v_mov_b32_e32 v46, v2
	v_mov_b32_e32 v47, v2
	v_mov_b32_e32 v48, v2
	v_mov_b32_e32 v49, v2
	v_mov_b32_e32 v54, v2
	v_mov_b32_e32 v55, v2
	v_mov_b32_e32 v56, v2
	v_mov_b32_e32 v57, v2
	v_mov_b32_e32 v58, v2
	v_mov_b32_e32 v59, v2
	v_mov_b32_e32 v60, v2
	v_mov_b32_e32 v61, v2
	v_mov_b32_e32 v62, v2
	v_mov_b32_e32 v63, v2
	v_mov_b32_e32 v64, v2
	v_mov_b32_e32 v65, v2
	v_mov_b32_e32 v66, v2
	v_mov_b32_e32 v67, v2
	v_mov_b32_e32 v68, v2
	v_mov_b32_e32 v69, v2
	v_mov_b32_e32 v70, v2
	v_mov_b32_e32 v71, v2
	v_mov_b32_e32 v72, v2
	v_mov_b32_e32 v73, v2
	v_mov_b32_e32 v74, v2
	v_mov_b32_e32 v75, v2
	v_mov_b32_e32 v76, v2
	v_mov_b32_e32 v77, v2
	v_mov_b32_e32 v82, v2
	v_mov_b32_e32 v83, v2
	v_mov_b32_e32 v84, v2
	v_mov_b32_e32 v85, v2
	v_mov_b32_e32 v90, v2
	v_mov_b32_e32 v91, v2
	v_mov_b32_e32 v92, v2
	v_mov_b32_e32 v93, v2
	v_mov_b32_e32 v98, v2
	v_mov_b32_e32 v99, v2
	v_mov_b32_e32 v100, v2
	v_mov_b32_e32 v101, v2
	v_mov_b32_e32 v110, v2
	v_mov_b32_e32 v111, v2
	v_mov_b32_e32 v112, v2
	v_mov_b32_e32 v113, v2
	v_mov_b32_e32 v118, v2
	v_mov_b32_e32 v119, v2
	v_mov_b32_e32 v120, v2
	v_mov_b32_e32 v121, v2
	v_mov_b32_e32 v78, v2
	v_mov_b32_e32 v79, v2
	v_mov_b32_e32 v80, v2
	v_mov_b32_e32 v81, v2
	v_mov_b32_e32 v86, v2
	v_mov_b32_e32 v87, v2
	v_mov_b32_e32 v88, v2
	v_mov_b32_e32 v89, v2
	v_mov_b32_e32 v94, v2
	v_mov_b32_e32 v95, v2
	v_mov_b32_e32 v96, v2
	v_mov_b32_e32 v97, v2
	v_mov_b32_e32 v102, v2
	v_mov_b32_e32 v103, v2
	v_mov_b32_e32 v104, v2
	v_mov_b32_e32 v105, v2
	v_mov_b32_e32 v106, v2
	v_mov_b32_e32 v107, v2
	v_mov_b32_e32 v108, v2
	v_mov_b32_e32 v109, v2
	v_mov_b32_e32 v114, v2
	v_mov_b32_e32 v115, v2
	v_mov_b32_e32 v116, v2
	v_mov_b32_e32 v117, v2
	v_mov_b32_e32 v122, v2
	v_mov_b32_e32 v123, v2
	v_mov_b32_e32 v124, v2
	v_mov_b32_e32 v125, v2
	v_mov_b32_e32 v126, v2
	v_mov_b32_e32 v127, v2
	v_mov_b32_e32 v128, v2
	v_mov_b32_e32 v129, v2
	s_branch .LBB0_1284

; #define PG8_STAGE(bufoff, gbase, voff) do { _Pragma("unroll") for (int _i = 0; _i < 2; ++_i) \
;         __builtin_amdgcn_global_load_lds((const unsigned*)((const char*)(gbase) + (voff)[_i]), (LAS unsigned*)(lds + (bufoff) + ldsw + _i * 8192), 16, 0, 0); } while (0)
; #define PG8_STAGE_A(bufoff, h, kp, nx) do { if constexpr (GATHER) { const unsigned _p = (nx) ? ng[h] : cg[h]; unsigned _v[2]; _v[0] = (_p & 0xffffu) * lda + CA2[0]; _v[1] = (_p >> 16) * lda + CA2[1]; PG8_STAGE(bufoff, kp, _v); } \
;         else { PG8_STAGE(bufoff, (kp) + (h) * hstepA, voffA); } } while (0)
; #define PG8_LDA(dst, b, h) do { _Pragma("unroll") for (int m = 0; m < 4; ++m) _Pragma("unroll") for (int k = 0; k < 2; ++k) dst[m][k] = *(const LAS bf16x8*)(lds + PG8_SA(b, h) + aoff + m * 2048 + k * 1024); } while (0)
; #define PG8_LDB(dst, b, h) do { _Pragma("unroll") for (int n = 0; n < 2; ++n) _Pragma("unroll") for (int k = 0; k < 2; ++k) dst[n][k] = *(const LAS bf16x8*)(lds + PG8_SB(b, h) + boff + n * 2048 + k * 1024); } while (0)
; #define PG8_MMA(ai, bj, At, Bt) do { __builtin_amdgcn_s_setprio(1); _Pragma("unroll") for (int m = 0; m < 4; ++m) _Pragma("unroll") for (int n = 0; n < 2; ++n) _Pragma("unroll") for (int k = 0; k < 2; ++k) \
;         acc[ai][bj][m][n] = __builtin_amdgcn_mfma_f32_16x16x32_bf16(Bt[n][k], At[m][k], acc[ai][bj][m][n], 0, 0, 0); __builtin_amdgcn_s_setprio(0); } while (0)
; #define PG8_WAIT_V(n) asm volatile("s_waitcnt vmcnt(" #n ")" ::: "memory")
;     ...
;         for (int t = 0; t < nt; t += 2) {
;             const bool last = (t == nt - 2);
;             const char* a1 = cA + (size_t)(t + 1) * kstep;
;             const char* a2 = last ? nA : cA + (size_t)(t + 2) * kstep; const char* b2 = last ? nB : cB + (size_t)(t + 2) * kstep;
;             const char* a3 = a2 + kstep; const char* b3 = b2 + kstep;
;             PG8_LDB(B0, 0, 0); PG8_LDB(B1, 0, 1); PG8_SCHED; PG8_LDA(At, 0, 0); PG8_STAGE_A(PG8_SA(1, 1), 1, a1, false);
;             PG8_WAIT_V(8); PG8_WAIT_L(0); PG8_BAR; if (cur.amask & 1) { PG8_MMA(0, 0, At, B0); PG8_MMA(0, 1, At, B1); } PG8_BAR; PG8_SCHED;
;             PG8_LDA(At, 0, 1); PG8_STAGE(PG8_SB(0, 0), b2, voffB); PG8_STAGE(PG8_SB(0, 1), b2 + hstepB, voffB); PG8_STAGE_A(PG8_SA(0, 0), 0, a2, last);
;             PG8_WAIT_V(8); PG8_WAIT_L(0); PG8_BAR; if (cur.amask & 2) { PG8_MMA(1, 0, At, B0); PG8_MMA(1, 1, At, B1); } PG8_BAR; PG8_SCHED;
.LBB0_1315:
	s_add_u32 s22, s48, 0xfff80080
	s_addc_u32 s23, s49, -1
	s_add_i32 s24, 0, 0x10000
	s_cmp_eq_u32 s21, 4
	s_cselect_b32 s53, s5, s23
	s_cselect_b32 s52, s4, s22
	v_add_u32_e32 v149, s24, v147
	s_cselect_b32 s51, s37, s20
	s_cselect_b32 s50, s36, s19
	s_add_i32 s25, 0, 0x14000
	ds_read_b128 v[142:145], v149
	ds_read_b128 v[150:153], v149 offset:1024
	ds_read_b128 v[154:157], v149 offset:2048
	ds_read_b128 v[158:161], v149 offset:3072
	v_add_u32_e32 v149, s25, v147
	ds_read_b128 v[162:165], v149
	ds_read_b128 v[166:169], v149 offset:1024
	ds_read_b128 v[170:173], v149 offset:2048
	ds_read_b128 v[174:177], v149 offset:3072
	v_lshl_add_u64 v[210:211], s[48:49], 0, v[138:139]
	s_add_i32 m0, s10, 0xc000
	ds_read_b128 v[178:181], v148
	ds_read_b128 v[182:185], v148 offset:1024
	ds_read_b128 v[186:189], v148 offset:2048
	ds_read_b128 v[190:193], v148 offset:3072
	ds_read_b128 v[194:197], v148 offset:4096
	ds_read_b128 v[198:201], v148 offset:5120
	ds_read_b128 v[202:205], v148 offset:6144
	ds_read_b128 v[206:209], v148 offset:7168
	global_load_lds_dwordx4 v[210:211], off
	v_lshl_add_u64 v[210:211], s[48:49], 0, v[140:141]
	s_add_i32 m0, s10, 0xe000
	s_nop 0
	global_load_lds_dwordx4 v[210:211], off
	s_waitcnt vmcnt(8)
	s_waitcnt lgkmcnt(0)
	s_barrier
	s_waitcnt lgkmcnt(0)
	v_mfma_f32_16x16x32_bf16 v[126:129], v[142:145], v[178:181], v[126:129]
	v_mfma_f32_16x16x32_bf16 v[122:125], v[154:157], v[178:181], v[122:125]
	v_mfma_f32_16x16x32_bf16 v[118:121], v[142:145], v[186:189], v[118:121]
	v_mfma_f32_16x16x32_bf16 v[110:113], v[154:157], v[186:189], v[110:113]
	v_mfma_f32_16x16x32_bf16 v[102:105], v[142:145], v[194:197], v[102:105]
	v_mfma_f32_16x16x32_bf16 v[94:97], v[154:157], v[194:197], v[94:97]
	v_mfma_f32_16x16x32_bf16 v[86:89], v[142:145], v[202:205], v[86:89]
	v_mfma_f32_16x16x32_bf16 v[78:81], v[154:157], v[202:205], v[78:81]
	v_mfma_f32_16x16x32_bf16 v[126:129], v[150:153], v[182:185], v[126:129]
	v_mfma_f32_16x16x32_bf16 v[122:125], v[158:161], v[182:185], v[122:125]
	v_mfma_f32_16x16x32_bf16 v[118:121], v[150:153], v[190:193], v[118:121]
	v_mfma_f32_16x16x32_bf16 v[110:113], v[158:161], v[190:193], v[110:113]
	v_mfma_f32_16x16x32_bf16 v[102:105], v[150:153], v[198:201], v[102:105]
	v_mfma_f32_16x16x32_bf16 v[94:97], v[158:161], v[198:201], v[94:97]
	v_mfma_f32_16x16x32_bf16 v[86:89], v[150:153], v[206:209], v[86:89]
	v_mfma_f32_16x16x32_bf16 v[78:81], v[158:161], v[206:209], v[78:81]
	v_mfma_f32_16x16x32_bf16 v[114:117], v[162:165], v[178:181], v[114:117]
	v_mfma_f32_16x16x32_bf16 v[106:109], v[170:173], v[178:181], v[106:109]
	v_mfma_f32_16x16x32_bf16 v[98:101], v[162:165], v[186:189], v[98:101]
	v_mfma_f32_16x16x32_bf16 v[90:93], v[170:173], v[186:189], v[90:93]
	v_mfma_f32_16x16x32_bf16 v[82:85], v[162:165], v[194:197], v[82:85]
	v_mfma_f32_16x16x32_bf16 v[74:77], v[170:173], v[194:197], v[74:77]
	v_mfma_f32_16x16x32_bf16 v[70:73], v[162:165], v[202:205], v[70:73]
	v_mfma_f32_16x16x32_bf16 v[66:69], v[170:173], v[202:205], v[66:69]
	v_mfma_f32_16x16x32_bf16 v[114:117], v[166:169], v[182:185], v[114:117]
	v_mfma_f32_16x16x32_bf16 v[106:109], v[174:177], v[182:185], v[106:109]
	v_mfma_f32_16x16x32_bf16 v[98:101], v[166:169], v[190:193], v[98:101]
	v_mfma_f32_16x16x32_bf16 v[90:93], v[174:177], v[190:193], v[90:93]
	v_mfma_f32_16x16x32_bf16 v[82:85], v[166:169], v[198:201], v[82:85]
	v_mfma_f32_16x16x32_bf16 v[74:77], v[174:177], v[198:201], v[74:77]
	v_mfma_f32_16x16x32_bf16 v[70:73], v[166:169], v[206:209], v[70:73]
	v_mfma_f32_16x16x32_bf16 v[66:69], v[174:177], v[206:209], v[66:69]
	s_barrier
	s_add_i32 s22, s24, s43
	v_lshl_add_u64 v[210:211], s[50:51], 0, v[0:1]
	s_mov_b32 m0, s22
	ds_read_b128 v[178:181], v148 offset:16384
	ds_read_b128 v[182:185], v148 offset:17408
	ds_read_b128 v[186:189], v148 offset:18432
	ds_read_b128 v[190:193], v148 offset:19456
	ds_read_b128 v[194:197], v148 offset:20480
	ds_read_b128 v[198:201], v148 offset:21504
	ds_read_b128 v[202:205], v148 offset:22528
	ds_read_b128 v[206:209], v148 offset:23552
	global_load_lds_dwordx4 v[210:211], off
	s_add_i32 m0, s22, 0x2000
	s_add_u32 s22, s50, 0x80000
	v_lshl_add_u64 v[212:213], s[50:51], 0, v[130:131]
	s_addc_u32 s23, s51, 0
	s_add_i32 s24, s25, s43
	global_load_lds_dwordx4 v[212:213], off
	v_lshl_add_u64 v[214:215], s[22:23], 0, v[0:1]
	s_mov_b32 m0, s24
	v_lshl_add_u64 v[224:225], s[52:53], 0, v[132:133]
	global_load_lds_dwordx4 v[214:215], off
	v_lshl_add_u64 v[214:215], s[22:23], 0, v[130:131]
	s_add_i32 m0, s24, 0x2000
	s_nop 0
	global_load_lds_dwordx4 v[214:215], off
	v_lshl_add_u64 v[214:215], s[52:53], 0, v[134:135]
	s_mov_b32 m0, s10
	s_nop 0
	global_load_lds_dwordx4 v[214:215], off
	s_mov_b32 m0, s11
	s_nop 0
	global_load_lds_dwordx4 v[224:225], off
	s_waitcnt vmcnt(8)
	s_waitcnt lgkmcnt(0)
	s_barrier
; #define PG8_STAGE(bufoff, gbase, voff) do { _Pragma("unroll") for (int _i = 0; _i < 2; ++_i) \
;         __builtin_amdgcn_global_load_lds((const unsigned*)((const char*)(gbase) + (voff)[_i]), (LAS unsigned*)(lds + (bufoff) + ldsw + _i * 8192), 16, 0, 0); } while (0)
; #define PG8_STAGE_A(bufoff, h, kp, nx) do { if constexpr (GATHER) { const unsigned _p = (nx) ? ng[h] : cg[h]; unsigned _v[2]; _v[0] = (_p & 0xffffu) * lda + CA2[0]; _v[1] = (_p >> 16) * lda + CA2[1]; PG8_STAGE(bufoff, kp, _v); } \
;         else { PG8_STAGE(bufoff, (kp) + (h) * hstepA, voffA); } } while (0)
; #define PG8_LDA(dst, b, h) do { _Pragma("unroll") for (int m = 0; m < 4; ++m) _Pragma("unroll") for (int k = 0; k < 2; ++k) dst[m][k] = *(const LAS bf16x8*)(lds + PG8_SA(b, h) + aoff + m * 2048 + k * 1024); } while (0)
; #define PG8_LDB(dst, b, h) do { _Pragma("unroll") for (int n = 0; n < 2; ++n) _Pragma("unroll") for (int k = 0; k < 2; ++k) dst[n][k] = *(const LAS bf16x8*)(lds + PG8_SB(b, h) + boff + n * 2048 + k * 1024); } while (0)
; #define PG8_MMA(ai, bj, At, Bt) do { __builtin_amdgcn_s_setprio(1); _Pragma("unroll") for (int m = 0; m < 4; ++m) _Pragma("unroll") for (int n = 0; n < 2; ++n) _Pragma("unroll") for (int k = 0; k < 2; ++k) \
;         acc[ai][bj][m][n] = __builtin_amdgcn_mfma_f32_16x16x32_bf16(Bt[n][k], At[m][k], acc[ai][bj][m][n], 0, 0, 0); __builtin_amdgcn_s_setprio(0); } while (0)
; #define PG8_WAIT_V(n) asm volatile("s_waitcnt vmcnt(" #n ")" ::: "memory")
; #define PG8_WAIT_L(n) asm volatile("s_waitcnt lgkmcnt(" #n ")" ::: "memory")
; #define PG8_BAR __builtin_amdgcn_s_barrier()
; #define PG8_SCHED __builtin_amdgcn_sched_barrier(0)
;     ...
;             PG8_WAIT_V(8); PG8_WAIT_L(0); PG8_BAR; if (cur.amask & 2) { PG8_MMA(1, 0, At, B0); PG8_MMA(1, 1, At, B1); } PG8_BAR; PG8_SCHED;
;             PG8_LDB(B0, 1, 0); PG8_LDB(B1, 1, 1); PG8_SCHED; PG8_LDA(At, 1, 0); PG8_STAGE_A(PG8_SA(0, 1), 1, a2, last);
;             PG8_WAIT_V(8); PG8_WAIT_L(0); PG8_BAR; if (cur.amask & 1) { PG8_MMA(0, 0, At, B0); PG8_MMA(0, 1, At, B1); } PG8_BAR; PG8_SCHED;
;             PG8_LDA(At, 1, 1); PG8_STAGE(PG8_SB(1, 0), b3, voffB); PG8_STAGE(PG8_SB(1, 1), b3 + hstepB, voffB); PG8_STAGE_A(PG8_SA(1, 0), 0, a3, last);
;             PG8_WAIT_V(8); PG8_WAIT_L(0); PG8_BAR; if (cur.amask & 2) { PG8_MMA(1, 0, At, B0); PG8_MMA(1, 1, At, B1); } PG8_BAR; PG8_SCHED;
	s_waitcnt lgkmcnt(0)
	v_mfma_f32_16x16x32_bf16 v[62:65], v[142:145], v[178:181], v[62:65]
	v_mfma_f32_16x16x32_bf16 v[58:61], v[154:157], v[178:181], v[58:61]
	v_mfma_f32_16x16x32_bf16 v[54:57], v[142:145], v[186:189], v[54:57]
	v_mfma_f32_16x16x32_bf16 v[46:49], v[154:157], v[186:189], v[46:49]
	v_mfma_f32_16x16x32_bf16 v[38:41], v[142:145], v[194:197], v[38:41]
	v_mfma_f32_16x16x32_bf16 v[30:33], v[154:157], v[194:197], v[30:33]
	v_mfma_f32_16x16x32_bf16 v[22:25], v[142:145], v[202:205], v[22:25]
	v_mfma_f32_16x16x32_bf16 v[14:17], v[154:157], v[202:205], v[14:17]
	v_mfma_f32_16x16x32_bf16 v[62:65], v[150:153], v[182:185], v[62:65]
	v_mfma_f32_16x16x32_bf16 v[58:61], v[158:161], v[182:185], v[58:61]
	v_mfma_f32_16x16x32_bf16 v[54:57], v[150:153], v[190:193], v[54:57]
	v_mfma_f32_16x16x32_bf16 v[46:49], v[158:161], v[190:193], v[46:49]
	v_mfma_f32_16x16x32_bf16 v[38:41], v[150:153], v[198:201], v[38:41]
	v_mfma_f32_16x16x32_bf16 v[30:33], v[158:161], v[198:201], v[30:33]
	v_mfma_f32_16x16x32_bf16 v[22:25], v[150:153], v[206:209], v[22:25]
	v_mfma_f32_16x16x32_bf16 v[14:17], v[158:161], v[206:209], v[14:17]
	v_mfma_f32_16x16x32_bf16 v[50:53], v[162:165], v[178:181], v[50:53]
	v_mfma_f32_16x16x32_bf16 v[42:45], v[170:173], v[178:181], v[42:45]
	v_mfma_f32_16x16x32_bf16 v[34:37], v[162:165], v[186:189], v[34:37]
	v_mfma_f32_16x16x32_bf16 v[26:29], v[170:173], v[186:189], v[26:29]
	v_mfma_f32_16x16x32_bf16 v[18:21], v[162:165], v[194:197], v[18:21]
	v_mfma_f32_16x16x32_bf16 v[10:13], v[170:173], v[194:197], v[10:13]
	v_mfma_f32_16x16x32_bf16 v[6:9], v[162:165], v[202:205], v[6:9]
	v_mfma_f32_16x16x32_bf16 v[2:5], v[170:173], v[202:205], v[2:5]
	v_mfma_f32_16x16x32_bf16 v[50:53], v[166:169], v[182:185], v[50:53]
	v_mfma_f32_16x16x32_bf16 v[42:45], v[174:177], v[182:185], v[42:45]
	v_mfma_f32_16x16x32_bf16 v[34:37], v[166:169], v[190:193], v[34:37]
	v_mfma_f32_16x16x32_bf16 v[26:29], v[174:177], v[190:193], v[26:29]
	v_mfma_f32_16x16x32_bf16 v[18:21], v[166:169], v[198:201], v[18:21]
	v_mfma_f32_16x16x32_bf16 v[10:13], v[174:177], v[198:201], v[10:13]
	v_mfma_f32_16x16x32_bf16 v[6:9], v[166:169], v[206:209], v[6:9]
	v_mfma_f32_16x16x32_bf16 v[2:5], v[174:177], v[206:209], v[2:5]
	s_barrier
	s_add_i32 s24, 0, 0x18000
	v_add_u32_e32 v149, s24, v147
	s_add_i32 s25, 0, 0x1c000
	ds_read_b128 v[142:145], v149
	ds_read_b128 v[150:153], v149 offset:1024
	ds_read_b128 v[154:157], v149 offset:2048
	ds_read_b128 v[158:161], v149 offset:3072
	v_add_u32_e32 v149, s25, v147
	ds_read_b128 v[162:165], v149
	ds_read_b128 v[166:169], v149 offset:1024
	ds_read_b128 v[170:173], v149 offset:2048
	ds_read_b128 v[174:177], v149 offset:3072
	s_add_u32 s22, s52, 0x80000
	s_addc_u32 s23, s53, 0
	s_mov_b32 m0, s12
	v_lshl_add_u64 v[226:227], s[22:23], 0, v[134:135]
	ds_read_b128 v[178:181], v148 offset:32768
	ds_read_b128 v[182:185], v148 offset:33792
	ds_read_b128 v[186:189], v148 offset:34816
	ds_read_b128 v[190:193], v148 offset:35840
	ds_read_b128 v[194:197], v148 offset:36864
	ds_read_b128 v[198:201], v148 offset:37888
	ds_read_b128 v[202:205], v148 offset:38912
	ds_read_b128 v[206:209], v148 offset:39936
	global_load_lds_dwordx4 v[226:227], off
	v_lshl_add_u64 v[226:227], s[22:23], 0, v[132:133]
	s_mov_b32 m0, s13
	s_nop 0
	global_load_lds_dwordx4 v[226:227], off
	s_waitcnt vmcnt(8)
	s_waitcnt lgkmcnt(0)
	s_barrier
	s_waitcnt lgkmcnt(0)
	v_mfma_f32_16x16x32_bf16 v[126:129], v[142:145], v[178:181], v[126:129]
	v_mfma_f32_16x16x32_bf16 v[122:125], v[154:157], v[178:181], v[122:125]
	v_mfma_f32_16x16x32_bf16 v[118:121], v[142:145], v[186:189], v[118:121]
	v_mfma_f32_16x16x32_bf16 v[110:113], v[154:157], v[186:189], v[110:113]
	v_mfma_f32_16x16x32_bf16 v[102:105], v[142:145], v[194:197], v[102:105]
	v_mfma_f32_16x16x32_bf16 v[94:97], v[154:157], v[194:197], v[94:97]
	v_mfma_f32_16x16x32_bf16 v[86:89], v[142:145], v[202:205], v[86:89]
	v_mfma_f32_16x16x32_bf16 v[78:81], v[154:157], v[202:205], v[78:81]
	v_mfma_f32_16x16x32_bf16 v[126:129], v[150:153], v[182:185], v[126:129]
	v_mfma_f32_16x16x32_bf16 v[122:125], v[158:161], v[182:185], v[122:125]
	v_mfma_f32_16x16x32_bf16 v[118:121], v[150:153], v[190:193], v[118:121]
	v_mfma_f32_16x16x32_bf16 v[110:113], v[158:161], v[190:193], v[110:113]
	v_mfma_f32_16x16x32_bf16 v[102:105], v[150:153], v[198:201], v[102:105]
	v_mfma_f32_16x16x32_bf16 v[94:97], v[158:161], v[198:201], v[94:97]
	v_mfma_f32_16x16x32_bf16 v[86:89], v[150:153], v[206:209], v[86:89]
	v_mfma_f32_16x16x32_bf16 v[78:81], v[158:161], v[206:209], v[78:81]
	v_mfma_f32_16x16x32_bf16 v[114:117], v[162:165], v[178:181], v[114:117]
	v_mfma_f32_16x16x32_bf16 v[106:109], v[170:173], v[178:181], v[106:109]
	v_mfma_f32_16x16x32_bf16 v[98:101], v[162:165], v[186:189], v[98:101]
	v_mfma_f32_16x16x32_bf16 v[90:93], v[170:173], v[186:189], v[90:93]
	v_mfma_f32_16x16x32_bf16 v[82:85], v[162:165], v[194:197], v[82:85]
	v_mfma_f32_16x16x32_bf16 v[74:77], v[170:173], v[194:197], v[74:77]
	v_mfma_f32_16x16x32_bf16 v[70:73], v[162:165], v[202:205], v[70:73]
	v_mfma_f32_16x16x32_bf16 v[66:69], v[170:173], v[202:205], v[66:69]
	v_mfma_f32_16x16x32_bf16 v[114:117], v[166:169], v[182:185], v[114:117]
	v_mfma_f32_16x16x32_bf16 v[106:109], v[174:177], v[182:185], v[106:109]
	v_mfma_f32_16x16x32_bf16 v[98:101], v[166:169], v[190:193], v[98:101]
	v_mfma_f32_16x16x32_bf16 v[90:93], v[174:177], v[190:193], v[90:93]
	v_mfma_f32_16x16x32_bf16 v[82:85], v[166:169], v[198:201], v[82:85]
	v_mfma_f32_16x16x32_bf16 v[74:77], v[174:177], v[198:201], v[74:77]
	v_mfma_f32_16x16x32_bf16 v[70:73], v[166:169], v[206:209], v[70:73]
	v_mfma_f32_16x16x32_bf16 v[66:69], v[174:177], v[206:209], v[66:69]
	s_barrier
; #define PG8_STAGE(bufoff, gbase, voff) do { _Pragma("unroll") for (int _i = 0; _i < 2; ++_i) \
;         __builtin_amdgcn_global_load_lds((const unsigned*)((const char*)(gbase) + (voff)[_i]), (LAS unsigned*)(lds + (bufoff) + ldsw + _i * 8192), 16, 0, 0); } while (0)
; #define PG8_STAGE_A(bufoff, h, kp, nx) do { if constexpr (GATHER) { const unsigned _p = (nx) ? ng[h] : cg[h]; unsigned _v[2]; _v[0] = (_p & 0xffffu) * lda + CA2[0]; _v[1] = (_p >> 16) * lda + CA2[1]; PG8_STAGE(bufoff, kp, _v); } \
;         else { PG8_STAGE(bufoff, (kp) + (h) * hstepA, voffA); } } while (0)
; #define PG8_LDA(dst, b, h) do { _Pragma("unroll") for (int m = 0; m < 4; ++m) _Pragma("unroll") for (int k = 0; k < 2; ++k) dst[m][k] = *(const LAS bf16x8*)(lds + PG8_SA(b, h) + aoff + m * 2048 + k * 1024); } while (0)
; #define PG8_MMA(ai, bj, At, Bt) do { __builtin_amdgcn_s_setprio(1); _Pragma("unroll") for (int m = 0; m < 4; ++m) _Pragma("unroll") for (int n = 0; n < 2; ++n) _Pragma("unroll") for (int k = 0; k < 2; ++k) \
;         acc[ai][bj][m][n] = __builtin_amdgcn_mfma_f32_16x16x32_bf16(Bt[n][k], At[m][k], acc[ai][bj][m][n], 0, 0, 0); __builtin_amdgcn_s_setprio(0); } while (0)
; #define PG8_WAIT_V(n) asm volatile("s_waitcnt vmcnt(" #n ")" ::: "memory")
; #define PG8_WAIT_L(n) asm volatile("s_waitcnt lgkmcnt(" #n ")" ::: "memory")
; #define PG8_BAR __builtin_amdgcn_s_barrier()
; #define PG8_SCHED __builtin_amdgcn_sched_barrier(0)
;     ...
;             PG8_LDA(At, 1, 1); PG8_STAGE(PG8_SB(1, 0), b3, voffB); PG8_STAGE(PG8_SB(1, 1), b3 + hstepB, voffB); PG8_STAGE_A(PG8_SA(1, 0), 0, a3, last);
;             PG8_WAIT_V(8); PG8_WAIT_L(0); PG8_BAR; if (cur.amask & 2) { PG8_MMA(1, 0, At, B0); PG8_MMA(1, 1, At, B1); } PG8_BAR; PG8_SCHED;
;         }
	s_add_i32 s22, s24, s43
	v_lshl_add_u64 v[210:211], v[210:211], 0, s[92:93]
	s_mov_b32 m0, s22
	ds_read_b128 v[178:181], v148 offset:49152
	ds_read_b128 v[182:185], v148 offset:50176
	ds_read_b128 v[186:189], v148 offset:51200
	ds_read_b128 v[190:193], v148 offset:52224
	ds_read_b128 v[194:197], v148 offset:53248
	ds_read_b128 v[198:201], v148 offset:54272
	ds_read_b128 v[202:205], v148 offset:55296
	ds_read_b128 v[206:209], v148 offset:56320
	global_load_lds_dwordx4 v[210:211], off
	s_add_i32 m0, s22, 0x2000
	s_add_u32 s22, s50, 0x80080
	v_lshl_add_u64 v[210:211], v[212:213], 0, s[92:93]
	s_addc_u32 s23, s51, 0
	s_add_i32 s24, s25, s43
	global_load_lds_dwordx4 v[210:211], off
	v_lshl_add_u64 v[210:211], s[22:23], 0, v[0:1]
	s_mov_b32 m0, s24
	s_nop 0
	global_load_lds_dwordx4 v[210:211], off
	v_lshl_add_u64 v[210:211], s[22:23], 0, v[130:131]
	s_add_i32 m0, s24, 0x2000
	s_nop 0
	global_load_lds_dwordx4 v[210:211], off
	v_lshl_add_u64 v[210:211], v[214:215], 0, s[92:93]
	s_mov_b32 m0, s16
	s_nop 0
	global_load_lds_dwordx4 v[210:211], off
	v_lshl_add_u64 v[210:211], v[224:225], 0, s[92:93]
	s_mov_b32 m0, s17
	s_nop 0
	global_load_lds_dwordx4 v[210:211], off
	s_waitcnt vmcnt(8)
	s_waitcnt lgkmcnt(0)
	s_barrier
	s_waitcnt lgkmcnt(0)
	v_mfma_f32_16x16x32_bf16 v[62:65], v[142:145], v[178:181], v[62:65]
	v_mfma_f32_16x16x32_bf16 v[58:61], v[154:157], v[178:181], v[58:61]
	v_mfma_f32_16x16x32_bf16 v[54:57], v[142:145], v[186:189], v[54:57]
	v_mfma_f32_16x16x32_bf16 v[46:49], v[154:157], v[186:189], v[46:49]
	v_mfma_f32_16x16x32_bf16 v[38:41], v[142:145], v[194:197], v[38:41]
	v_mfma_f32_16x16x32_bf16 v[30:33], v[154:157], v[194:197], v[30:33]
	v_mfma_f32_16x16x32_bf16 v[22:25], v[142:145], v[202:205], v[22:25]
	v_mfma_f32_16x16x32_bf16 v[14:17], v[154:157], v[202:205], v[14:17]
	v_mfma_f32_16x16x32_bf16 v[62:65], v[150:153], v[182:185], v[62:65]
	v_mfma_f32_16x16x32_bf16 v[58:61], v[158:161], v[182:185], v[58:61]
	v_mfma_f32_16x16x32_bf16 v[54:57], v[150:153], v[190:193], v[54:57]
	v_mfma_f32_16x16x32_bf16 v[46:49], v[158:161], v[190:193], v[46:49]
	v_mfma_f32_16x16x32_bf16 v[38:41], v[150:153], v[198:201], v[38:41]
	v_mfma_f32_16x16x32_bf16 v[30:33], v[158:161], v[198:201], v[30:33]
	v_mfma_f32_16x16x32_bf16 v[22:25], v[150:153], v[206:209], v[22:25]
	v_mfma_f32_16x16x32_bf16 v[14:17], v[158:161], v[206:209], v[14:17]
	v_mfma_f32_16x16x32_bf16 v[50:53], v[162:165], v[178:181], v[50:53]
	v_mfma_f32_16x16x32_bf16 v[42:45], v[170:173], v[178:181], v[42:45]
	v_mfma_f32_16x16x32_bf16 v[34:37], v[162:165], v[186:189], v[34:37]
	v_mfma_f32_16x16x32_bf16 v[26:29], v[170:173], v[186:189], v[26:29]
	v_mfma_f32_16x16x32_bf16 v[18:21], v[162:165], v[194:197], v[18:21]
	v_mfma_f32_16x16x32_bf16 v[10:13], v[170:173], v[194:197], v[10:13]
	v_mfma_f32_16x16x32_bf16 v[6:9], v[162:165], v[202:205], v[6:9]
	v_mfma_f32_16x16x32_bf16 v[2:5], v[170:173], v[202:205], v[2:5]
	v_mfma_f32_16x16x32_bf16 v[50:53], v[166:169], v[182:185], v[50:53]
	v_mfma_f32_16x16x32_bf16 v[42:45], v[174:177], v[182:185], v[42:45]
	v_mfma_f32_16x16x32_bf16 v[34:37], v[166:169], v[190:193], v[34:37]
	v_mfma_f32_16x16x32_bf16 v[26:29], v[174:177], v[190:193], v[26:29]
	v_mfma_f32_16x16x32_bf16 v[18:21], v[166:169], v[198:201], v[18:21]
	v_mfma_f32_16x16x32_bf16 v[10:13], v[174:177], v[198:201], v[10:13]
	v_mfma_f32_16x16x32_bf16 v[6:9], v[166:169], v[206:209], v[6:9]
	v_mfma_f32_16x16x32_bf16 v[2:5], v[174:177], v[206:209], v[2:5]
	s_barrier
	s_add_i32 s21, s21, 2
	s_add_u32 s48, s48, 0x100
	s_addc_u32 s49, s49, 0
	s_add_u32 s19, s19, 0x100
	s_addc_u32 s20, s20, 0
	s_cmp_gt_u32 s21, 5
	s_cbranch_scc0 .LBB0_1315
	v_readlane_b32 s20, v252, 14
	v_readlane_b32 s21, v252, 15
	s_and_b64 vcc, exec, s[20:21]
	s_cbranch_vccz .LBB0_1318
	s_barrier

; #define PG8_STAGE(bufoff, gbase, voff) do { _Pragma("unroll") for (int _i = 0; _i < 2; ++_i) \
;         __builtin_amdgcn_global_load_lds((const unsigned*)((const char*)(gbase) + (voff)[_i]), (LAS unsigned*)(lds + (bufoff) + ldsw + _i * 8192), 16, 0, 0); } while (0)
; #define PG8_STAGE_A(bufoff, h, kp, nx) do { if constexpr (GATHER) { const unsigned _p = (nx) ? ng[h] : cg[h]; unsigned _v[2]; _v[0] = (_p & 0xffffu) * lda + CA2[0]; _v[1] = (_p >> 16) * lda + CA2[1]; PG8_STAGE(bufoff, kp, _v); } \
;         else { PG8_STAGE(bufoff, (kp) + (h) * hstepA, voffA); } } while (0)
; #define PG8_LDA(dst, b, h) do { _Pragma("unroll") for (int m = 0; m < 4; ++m) _Pragma("unroll") for (int k = 0; k < 2; ++k) dst[m][k] = *(const LAS bf16x8*)(lds + PG8_SA(b, h) + aoff + m * 2048 + k * 1024); } while (0)
; #define PG8_LDB(dst, b, h) do { _Pragma("unroll") for (int n = 0; n < 2; ++n) _Pragma("unroll") for (int k = 0; k < 2; ++k) dst[n][k] = *(const LAS bf16x8*)(lds + PG8_SB(b, h) + boff + n * 2048 + k * 1024); } while (0)
; #define PG8_MMA(ai, bj, At, Bt) do { __builtin_amdgcn_s_setprio(1); _Pragma("unroll") for (int m = 0; m < 4; ++m) _Pragma("unroll") for (int n = 0; n < 2; ++n) _Pragma("unroll") for (int k = 0; k < 2; ++k) \
;         acc[ai][bj][m][n] = __builtin_amdgcn_mfma_f32_16x16x32_bf16(Bt[n][k], At[m][k], acc[ai][bj][m][n], 0, 0, 0); __builtin_amdgcn_s_setprio(0); } while (0)
; #define PG8_WAIT_V(n) asm volatile("s_waitcnt vmcnt(" #n ")" ::: "memory")
;     ...
;         for (int t = 0; t < nt; t += 2) {
;             const bool last = (t == nt - 2);
;             const char* a1 = cA + (size_t)(t + 1) * kstep;
;             const char* a2 = last ? nA : cA + (size_t)(t + 2) * kstep; const char* b2 = last ? nB : cB + (size_t)(t + 2) * kstep;
;             const char* a3 = a2 + kstep; const char* b3 = b2 + kstep;
;             PG8_LDB(B0, 0, 0); PG8_LDB(B1, 0, 1); PG8_SCHED; PG8_LDA(At, 0, 0); PG8_STAGE_A(PG8_SA(1, 1), 1, a1, false);
;             PG8_WAIT_V(8); PG8_WAIT_L(0); PG8_BAR; if (cur.amask & 1) { PG8_MMA(0, 0, At, B0); PG8_MMA(0, 1, At, B1); } PG8_BAR; PG8_SCHED;
;             PG8_LDA(At, 0, 1); PG8_STAGE(PG8_SB(0, 0), b2, voffB); PG8_STAGE(PG8_SB(0, 1), b2 + hstepB, voffB); PG8_STAGE_A(PG8_SA(0, 0), 0, a2, last);
;             PG8_WAIT_V(8); PG8_WAIT_L(0); PG8_BAR; if (cur.amask & 2) { PG8_MMA(1, 0, At, B0); PG8_MMA(1, 1, At, B1); } PG8_BAR; PG8_SCHED;
.LBB0_1392:
	s_add_u32 s20, s48, 0xfffc0080
	s_addc_u32 s21, s49, -1
	s_add_i32 s22, 0, 0x10000
	s_cmp_eq_u32 s19, 12
	s_cselect_b32 s53, s39, s21
	s_cselect_b32 s52, s38, s20
	v_add_u32_e32 v148, s22, v151
	s_cselect_b32 s51, s41, s18
	s_cselect_b32 s50, s40, s17
	s_add_i32 s23, 0, 0x14000
	ds_read_b128 v[144:147], v148
	ds_read_b128 v[154:157], v148 offset:1024
	ds_read_b128 v[158:161], v148 offset:2048
	ds_read_b128 v[162:165], v148 offset:3072
	v_add_u32_e32 v148, s23, v151
	ds_read_b128 v[166:169], v148
	ds_read_b128 v[170:173], v148 offset:1024
	ds_read_b128 v[174:177], v148 offset:2048
	ds_read_b128 v[178:181], v148 offset:3072
	v_lshl_add_u64 v[148:149], s[48:49], 0, v[140:141]
	s_add_i32 m0, s10, 0xc000
	ds_read_b128 v[182:185], v152
	ds_read_b128 v[186:189], v152 offset:1024
	ds_read_b128 v[190:193], v152 offset:2048
	ds_read_b128 v[194:197], v152 offset:3072
	ds_read_b128 v[198:201], v152 offset:4096
	ds_read_b128 v[202:205], v152 offset:5120
	ds_read_b128 v[206:209], v152 offset:6144
	ds_read_b128 v[210:213], v152 offset:7168
	global_load_lds_dwordx4 v[148:149], off
	v_lshl_add_u64 v[148:149], s[48:49], 0, v[142:143]
	s_add_i32 m0, s10, 0xe000
	s_nop 0
	global_load_lds_dwordx4 v[148:149], off
	s_waitcnt vmcnt(8)
	s_waitcnt lgkmcnt(0)
	s_barrier
	s_waitcnt lgkmcnt(0)
	v_mfma_f32_16x16x32_bf16 v[126:129], v[144:147], v[182:185], v[126:129]
	v_mfma_f32_16x16x32_bf16 v[122:125], v[158:161], v[182:185], v[122:125]
	v_mfma_f32_16x16x32_bf16 v[110:113], v[144:147], v[190:193], v[110:113]
	v_mfma_f32_16x16x32_bf16 v[106:109], v[158:161], v[190:193], v[106:109]
	v_mfma_f32_16x16x32_bf16 v[94:97], v[144:147], v[198:201], v[94:97]
	v_mfma_f32_16x16x32_bf16 v[90:93], v[158:161], v[198:201], v[90:93]
	v_mfma_f32_16x16x32_bf16 v[78:81], v[144:147], v[206:209], v[78:81]
	v_mfma_f32_16x16x32_bf16 v[74:77], v[158:161], v[206:209], v[74:77]
	v_mfma_f32_16x16x32_bf16 v[126:129], v[154:157], v[186:189], v[126:129]
	v_mfma_f32_16x16x32_bf16 v[122:125], v[162:165], v[186:189], v[122:125]
	v_mfma_f32_16x16x32_bf16 v[110:113], v[154:157], v[194:197], v[110:113]
	v_mfma_f32_16x16x32_bf16 v[106:109], v[162:165], v[194:197], v[106:109]
	v_mfma_f32_16x16x32_bf16 v[94:97], v[154:157], v[202:205], v[94:97]
	v_mfma_f32_16x16x32_bf16 v[90:93], v[162:165], v[202:205], v[90:93]
	v_mfma_f32_16x16x32_bf16 v[78:81], v[154:157], v[210:213], v[78:81]
	v_mfma_f32_16x16x32_bf16 v[74:77], v[162:165], v[210:213], v[74:77]
	v_mfma_f32_16x16x32_bf16 v[118:121], v[166:169], v[182:185], v[118:121]
	v_mfma_f32_16x16x32_bf16 v[114:117], v[174:177], v[182:185], v[114:117]
	v_mfma_f32_16x16x32_bf16 v[102:105], v[166:169], v[190:193], v[102:105]
	v_mfma_f32_16x16x32_bf16 v[98:101], v[174:177], v[190:193], v[98:101]
	v_mfma_f32_16x16x32_bf16 v[86:89], v[166:169], v[198:201], v[86:89]
	v_mfma_f32_16x16x32_bf16 v[82:85], v[174:177], v[198:201], v[82:85]
	v_mfma_f32_16x16x32_bf16 v[70:73], v[166:169], v[206:209], v[70:73]
	v_mfma_f32_16x16x32_bf16 v[66:69], v[174:177], v[206:209], v[66:69]
	v_mfma_f32_16x16x32_bf16 v[118:121], v[170:173], v[186:189], v[118:121]
	v_mfma_f32_16x16x32_bf16 v[114:117], v[178:181], v[186:189], v[114:117]
	v_mfma_f32_16x16x32_bf16 v[102:105], v[170:173], v[194:197], v[102:105]
	v_mfma_f32_16x16x32_bf16 v[98:101], v[178:181], v[194:197], v[98:101]
	v_mfma_f32_16x16x32_bf16 v[86:89], v[170:173], v[202:205], v[86:89]
	v_mfma_f32_16x16x32_bf16 v[82:85], v[178:181], v[202:205], v[82:85]
	v_mfma_f32_16x16x32_bf16 v[70:73], v[170:173], v[210:213], v[70:73]
	v_mfma_f32_16x16x32_bf16 v[66:69], v[178:181], v[210:213], v[66:69]
	s_barrier
	s_add_i32 s20, s22, s43
	v_lshl_add_u64 v[148:149], s[50:51], 0, v[0:1]
	s_mov_b32 m0, s20
	ds_read_b128 v[182:185], v152 offset:16384
	ds_read_b128 v[186:189], v152 offset:17408
	ds_read_b128 v[190:193], v152 offset:18432
	ds_read_b128 v[194:197], v152 offset:19456
	ds_read_b128 v[198:201], v152 offset:20480
	ds_read_b128 v[202:205], v152 offset:21504
	ds_read_b128 v[206:209], v152 offset:22528
	ds_read_b128 v[210:213], v152 offset:23552
	global_load_lds_dwordx4 v[148:149], off
	s_add_i32 m0, s20, 0x2000
	s_add_u32 s20, s50, 0x40000
	v_lshl_add_u64 v[214:215], s[50:51], 0, v[130:131]
	s_addc_u32 s21, s51, 0
	s_add_i32 s22, s23, s43
	global_load_lds_dwordx4 v[214:215], off
	v_lshl_add_u64 v[224:225], s[20:21], 0, v[0:1]
	s_mov_b32 m0, s22
	v_lshl_add_u64 v[226:227], s[52:53], 0, v[132:133]
	global_load_lds_dwordx4 v[224:225], off
	v_lshl_add_u64 v[224:225], s[20:21], 0, v[130:131]
	s_add_i32 m0, s22, 0x2000
	s_nop 0
	global_load_lds_dwordx4 v[224:225], off
	v_lshl_add_u64 v[224:225], s[52:53], 0, v[134:135]
	s_mov_b32 m0, s10
	s_nop 0
	global_load_lds_dwordx4 v[224:225], off
	s_mov_b32 m0, s11
	s_nop 0
	global_load_lds_dwordx4 v[226:227], off
	s_waitcnt vmcnt(8)
	s_waitcnt lgkmcnt(0)
	s_barrier
; #define PG8_STAGE(bufoff, gbase, voff) do { _Pragma("unroll") for (int _i = 0; _i < 2; ++_i) \
;         __builtin_amdgcn_global_load_lds((const unsigned*)((const char*)(gbase) + (voff)[_i]), (LAS unsigned*)(lds + (bufoff) + ldsw + _i * 8192), 16, 0, 0); } while (0)
; #define PG8_STAGE_A(bufoff, h, kp, nx) do { if constexpr (GATHER) { const unsigned _p = (nx) ? ng[h] : cg[h]; unsigned _v[2]; _v[0] = (_p & 0xffffu) * lda + CA2[0]; _v[1] = (_p >> 16) * lda + CA2[1]; PG8_STAGE(bufoff, kp, _v); } \
;         else { PG8_STAGE(bufoff, (kp) + (h) * hstepA, voffA); } } while (0)
; #define PG8_LDA(dst, b, h) do { _Pragma("unroll") for (int m = 0; m < 4; ++m) _Pragma("unroll") for (int k = 0; k < 2; ++k) dst[m][k] = *(const LAS bf16x8*)(lds + PG8_SA(b, h) + aoff + m * 2048 + k * 1024); } while (0)
; #define PG8_LDB(dst, b, h) do { _Pragma("unroll") for (int n = 0; n < 2; ++n) _Pragma("unroll") for (int k = 0; k < 2; ++k) dst[n][k] = *(const LAS bf16x8*)(lds + PG8_SB(b, h) + boff + n * 2048 + k * 1024); } while (0)
; #define PG8_MMA(ai, bj, At, Bt) do { __builtin_amdgcn_s_setprio(1); _Pragma("unroll") for (int m = 0; m < 4; ++m) _Pragma("unroll") for (int n = 0; n < 2; ++n) _Pragma("unroll") for (int k = 0; k < 2; ++k) \
;         acc[ai][bj][m][n] = __builtin_amdgcn_mfma_f32_16x16x32_bf16(Bt[n][k], At[m][k], acc[ai][bj][m][n], 0, 0, 0); __builtin_amdgcn_s_setprio(0); } while (0)
; #define PG8_WAIT_V(n) asm volatile("s_waitcnt vmcnt(" #n ")" ::: "memory")
; #define PG8_WAIT_L(n) asm volatile("s_waitcnt lgkmcnt(" #n ")" ::: "memory")
; #define PG8_BAR __builtin_amdgcn_s_barrier()
; #define PG8_SCHED __builtin_amdgcn_sched_barrier(0)
;     ...
;             PG8_WAIT_V(8); PG8_WAIT_L(0); PG8_BAR; if (cur.amask & 2) { PG8_MMA(1, 0, At, B0); PG8_MMA(1, 1, At, B1); } PG8_BAR; PG8_SCHED;
;             PG8_LDB(B0, 1, 0); PG8_LDB(B1, 1, 1); PG8_SCHED; PG8_LDA(At, 1, 0); PG8_STAGE_A(PG8_SA(0, 1), 1, a2, last);
;             PG8_WAIT_V(8); PG8_WAIT_L(0); PG8_BAR; if (cur.amask & 1) { PG8_MMA(0, 0, At, B0); PG8_MMA(0, 1, At, B1); } PG8_BAR; PG8_SCHED;
;             PG8_LDA(At, 1, 1); PG8_STAGE(PG8_SB(1, 0), b3, voffB); PG8_STAGE(PG8_SB(1, 1), b3 + hstepB, voffB); PG8_STAGE_A(PG8_SA(1, 0), 0, a3, last);
;             PG8_WAIT_V(8); PG8_WAIT_L(0); PG8_BAR; if (cur.amask & 2) { PG8_MMA(1, 0, At, B0); PG8_MMA(1, 1, At, B1); } PG8_BAR; PG8_SCHED;
	s_waitcnt lgkmcnt(0)
	v_mfma_f32_16x16x32_bf16 v[62:65], v[144:147], v[182:185], v[62:65]
	v_mfma_f32_16x16x32_bf16 v[58:61], v[158:161], v[182:185], v[58:61]
	v_mfma_f32_16x16x32_bf16 v[46:49], v[144:147], v[190:193], v[46:49]
	v_mfma_f32_16x16x32_bf16 v[42:45], v[158:161], v[190:193], v[42:45]
	v_mfma_f32_16x16x32_bf16 v[30:33], v[144:147], v[198:201], v[30:33]
	v_mfma_f32_16x16x32_bf16 v[26:29], v[158:161], v[198:201], v[26:29]
	v_mfma_f32_16x16x32_bf16 v[14:17], v[144:147], v[206:209], v[14:17]
	v_mfma_f32_16x16x32_bf16 v[10:13], v[158:161], v[206:209], v[10:13]
	v_mfma_f32_16x16x32_bf16 v[62:65], v[154:157], v[186:189], v[62:65]
	v_mfma_f32_16x16x32_bf16 v[58:61], v[162:165], v[186:189], v[58:61]
	v_mfma_f32_16x16x32_bf16 v[46:49], v[154:157], v[194:197], v[46:49]
	v_mfma_f32_16x16x32_bf16 v[42:45], v[162:165], v[194:197], v[42:45]
	v_mfma_f32_16x16x32_bf16 v[30:33], v[154:157], v[202:205], v[30:33]
	v_mfma_f32_16x16x32_bf16 v[26:29], v[162:165], v[202:205], v[26:29]
	v_mfma_f32_16x16x32_bf16 v[14:17], v[154:157], v[210:213], v[14:17]
	v_mfma_f32_16x16x32_bf16 v[10:13], v[162:165], v[210:213], v[10:13]
	v_mfma_f32_16x16x32_bf16 v[54:57], v[166:169], v[182:185], v[54:57]
	v_mfma_f32_16x16x32_bf16 v[50:53], v[174:177], v[182:185], v[50:53]
	v_mfma_f32_16x16x32_bf16 v[38:41], v[166:169], v[190:193], v[38:41]
	v_mfma_f32_16x16x32_bf16 v[34:37], v[174:177], v[190:193], v[34:37]
	v_mfma_f32_16x16x32_bf16 v[22:25], v[166:169], v[198:201], v[22:25]
	v_mfma_f32_16x16x32_bf16 v[18:21], v[174:177], v[198:201], v[18:21]
	v_mfma_f32_16x16x32_bf16 v[6:9], v[166:169], v[206:209], v[6:9]
	v_mfma_f32_16x16x32_bf16 v[2:5], v[174:177], v[206:209], v[2:5]
	v_mfma_f32_16x16x32_bf16 v[54:57], v[170:173], v[186:189], v[54:57]
	v_mfma_f32_16x16x32_bf16 v[50:53], v[178:181], v[186:189], v[50:53]
	v_mfma_f32_16x16x32_bf16 v[38:41], v[170:173], v[194:197], v[38:41]
	v_mfma_f32_16x16x32_bf16 v[34:37], v[178:181], v[194:197], v[34:37]
	v_mfma_f32_16x16x32_bf16 v[22:25], v[170:173], v[202:205], v[22:25]
	v_mfma_f32_16x16x32_bf16 v[18:21], v[178:181], v[202:205], v[18:21]
	v_mfma_f32_16x16x32_bf16 v[6:9], v[170:173], v[210:213], v[6:9]
	v_mfma_f32_16x16x32_bf16 v[2:5], v[178:181], v[210:213], v[2:5]
	s_barrier
	s_add_i32 s22, 0, 0x18000
	v_add_u32_e32 v153, s22, v151
	s_add_i32 s23, 0, 0x1c000
	ds_read_b128 v[144:147], v153
	ds_read_b128 v[154:157], v153 offset:1024
	ds_read_b128 v[158:161], v153 offset:2048
	ds_read_b128 v[162:165], v153 offset:3072
	v_add_u32_e32 v153, s23, v151
	ds_read_b128 v[166:169], v153
	ds_read_b128 v[170:173], v153 offset:1024
	ds_read_b128 v[174:177], v153 offset:2048
	ds_read_b128 v[178:181], v153 offset:3072
	s_add_u32 s20, s52, 0x40000
	s_addc_u32 s21, s53, 0
	s_mov_b32 m0, s12
	v_lshl_add_u64 v[228:229], s[20:21], 0, v[134:135]
	ds_read_b128 v[182:185], v152 offset:32768
	ds_read_b128 v[186:189], v152 offset:33792
	ds_read_b128 v[190:193], v152 offset:34816
	ds_read_b128 v[194:197], v152 offset:35840
	ds_read_b128 v[198:201], v152 offset:36864
	ds_read_b128 v[202:205], v152 offset:37888
	ds_read_b128 v[206:209], v152 offset:38912
	ds_read_b128 v[210:213], v152 offset:39936
	global_load_lds_dwordx4 v[228:229], off
	v_lshl_add_u64 v[228:229], s[20:21], 0, v[132:133]
	s_mov_b32 m0, s13
	s_nop 0
	global_load_lds_dwordx4 v[228:229], off
	s_waitcnt vmcnt(8)
	s_waitcnt lgkmcnt(0)
	s_barrier
	s_waitcnt lgkmcnt(0)
	v_mfma_f32_16x16x32_bf16 v[126:129], v[144:147], v[182:185], v[126:129]
	v_mfma_f32_16x16x32_bf16 v[122:125], v[158:161], v[182:185], v[122:125]
	v_mfma_f32_16x16x32_bf16 v[110:113], v[144:147], v[190:193], v[110:113]
	v_mfma_f32_16x16x32_bf16 v[106:109], v[158:161], v[190:193], v[106:109]
	v_mfma_f32_16x16x32_bf16 v[94:97], v[144:147], v[198:201], v[94:97]
	v_mfma_f32_16x16x32_bf16 v[90:93], v[158:161], v[198:201], v[90:93]
	v_mfma_f32_16x16x32_bf16 v[78:81], v[144:147], v[206:209], v[78:81]
	v_mfma_f32_16x16x32_bf16 v[74:77], v[158:161], v[206:209], v[74:77]
	v_mfma_f32_16x16x32_bf16 v[126:129], v[154:157], v[186:189], v[126:129]
	v_mfma_f32_16x16x32_bf16 v[122:125], v[162:165], v[186:189], v[122:125]
	v_mfma_f32_16x16x32_bf16 v[110:113], v[154:157], v[194:197], v[110:113]
	v_mfma_f32_16x16x32_bf16 v[106:109], v[162:165], v[194:197], v[106:109]
	v_mfma_f32_16x16x32_bf16 v[94:97], v[154:157], v[202:205], v[94:97]
	v_mfma_f32_16x16x32_bf16 v[90:93], v[162:165], v[202:205], v[90:93]
	v_mfma_f32_16x16x32_bf16 v[78:81], v[154:157], v[210:213], v[78:81]
	v_mfma_f32_16x16x32_bf16 v[74:77], v[162:165], v[210:213], v[74:77]
	v_mfma_f32_16x16x32_bf16 v[118:121], v[166:169], v[182:185], v[118:121]
	v_mfma_f32_16x16x32_bf16 v[114:117], v[174:177], v[182:185], v[114:117]
	v_mfma_f32_16x16x32_bf16 v[102:105], v[166:169], v[190:193], v[102:105]
	v_mfma_f32_16x16x32_bf16 v[98:101], v[174:177], v[190:193], v[98:101]
	v_mfma_f32_16x16x32_bf16 v[86:89], v[166:169], v[198:201], v[86:89]
	v_mfma_f32_16x16x32_bf16 v[82:85], v[174:177], v[198:201], v[82:85]
	v_mfma_f32_16x16x32_bf16 v[70:73], v[166:169], v[206:209], v[70:73]
	v_mfma_f32_16x16x32_bf16 v[66:69], v[174:177], v[206:209], v[66:69]
	v_mfma_f32_16x16x32_bf16 v[118:121], v[170:173], v[186:189], v[118:121]
	v_mfma_f32_16x16x32_bf16 v[114:117], v[178:181], v[186:189], v[114:117]
	v_mfma_f32_16x16x32_bf16 v[102:105], v[170:173], v[194:197], v[102:105]
	v_mfma_f32_16x16x32_bf16 v[98:101], v[178:181], v[194:197], v[98:101]
	v_mfma_f32_16x16x32_bf16 v[86:89], v[170:173], v[202:205], v[86:89]
	v_mfma_f32_16x16x32_bf16 v[82:85], v[178:181], v[202:205], v[82:85]
	v_mfma_f32_16x16x32_bf16 v[70:73], v[170:173], v[210:213], v[70:73]
	v_mfma_f32_16x16x32_bf16 v[66:69], v[178:181], v[210:213], v[66:69]
	s_barrier
; #define PG8_STAGE(bufoff, gbase, voff) do { _Pragma("unroll") for (int _i = 0; _i < 2; ++_i) \
;         __builtin_amdgcn_global_load_lds((const unsigned*)((const char*)(gbase) + (voff)[_i]), (LAS unsigned*)(lds + (bufoff) + ldsw + _i * 8192), 16, 0, 0); } while (0)
; #define PG8_STAGE_A(bufoff, h, kp, nx) do { if constexpr (GATHER) { const unsigned _p = (nx) ? ng[h] : cg[h]; unsigned _v[2]; _v[0] = (_p & 0xffffu) * lda + CA2[0]; _v[1] = (_p >> 16) * lda + CA2[1]; PG8_STAGE(bufoff, kp, _v); } \
;         else { PG8_STAGE(bufoff, (kp) + (h) * hstepA, voffA); } } while (0)
; #define PG8_LDA(dst, b, h) do { _Pragma("unroll") for (int m = 0; m < 4; ++m) _Pragma("unroll") for (int k = 0; k < 2; ++k) dst[m][k] = *(const LAS bf16x8*)(lds + PG8_SA(b, h) + aoff + m * 2048 + k * 1024); } while (0)
; #define PG8_MMA(ai, bj, At, Bt) do { __builtin_amdgcn_s_setprio(1); _Pragma("unroll") for (int m = 0; m < 4; ++m) _Pragma("unroll") for (int n = 0; n < 2; ++n) _Pragma("unroll") for (int k = 0; k < 2; ++k) \
;         acc[ai][bj][m][n] = __builtin_amdgcn_mfma_f32_16x16x32_bf16(Bt[n][k], At[m][k], acc[ai][bj][m][n], 0, 0, 0); __builtin_amdgcn_s_setprio(0); } while (0)
; #define PG8_WAIT_V(n) asm volatile("s_waitcnt vmcnt(" #n ")" ::: "memory")
; #define PG8_WAIT_L(n) asm volatile("s_waitcnt lgkmcnt(" #n ")" ::: "memory")
; #define PG8_BAR __builtin_amdgcn_s_barrier()
; #define PG8_SCHED __builtin_amdgcn_sched_barrier(0)
;     ...
;             PG8_LDA(At, 1, 1); PG8_STAGE(PG8_SB(1, 0), b3, voffB); PG8_STAGE(PG8_SB(1, 1), b3 + hstepB, voffB); PG8_STAGE_A(PG8_SA(1, 0), 0, a3, last);
;             PG8_WAIT_V(8); PG8_WAIT_L(0); PG8_BAR; if (cur.amask & 2) { PG8_MMA(1, 0, At, B0); PG8_MMA(1, 1, At, B1); } PG8_BAR; PG8_SCHED;
;         }
	s_add_i32 s20, s22, s43
	v_lshl_add_u64 v[148:149], v[148:149], 0, s[92:93]
	s_mov_b32 m0, s20
	ds_read_b128 v[182:185], v152 offset:49152
	ds_read_b128 v[186:189], v152 offset:50176
	ds_read_b128 v[190:193], v152 offset:51200
	ds_read_b128 v[194:197], v152 offset:52224
	ds_read_b128 v[198:201], v152 offset:53248
	ds_read_b128 v[202:205], v152 offset:54272
	ds_read_b128 v[206:209], v152 offset:55296
	ds_read_b128 v[210:213], v152 offset:56320
	global_load_lds_dwordx4 v[148:149], off
	s_add_i32 m0, s20, 0x2000
	s_add_u32 s20, s50, 0x40080
	v_lshl_add_u64 v[148:149], v[214:215], 0, s[92:93]
	s_addc_u32 s21, s51, 0
	s_add_i32 s22, s23, s43
	global_load_lds_dwordx4 v[148:149], off
	v_lshl_add_u64 v[148:149], s[20:21], 0, v[0:1]
	s_mov_b32 m0, s22
	s_nop 0
	global_load_lds_dwordx4 v[148:149], off
	v_lshl_add_u64 v[148:149], s[20:21], 0, v[130:131]
	s_add_i32 m0, s22, 0x2000
	s_nop 0
	global_load_lds_dwordx4 v[148:149], off
	v_lshl_add_u64 v[148:149], v[224:225], 0, s[92:93]
	s_mov_b32 m0, s14
	s_nop 0
	global_load_lds_dwordx4 v[148:149], off
	v_lshl_add_u64 v[148:149], v[226:227], 0, s[92:93]
	s_mov_b32 m0, s15
	s_nop 0
	global_load_lds_dwordx4 v[148:149], off
	s_waitcnt vmcnt(8)
	s_waitcnt lgkmcnt(0)
	s_barrier
	s_waitcnt lgkmcnt(0)
	v_mfma_f32_16x16x32_bf16 v[62:65], v[144:147], v[182:185], v[62:65]
	v_mfma_f32_16x16x32_bf16 v[58:61], v[158:161], v[182:185], v[58:61]
	v_mfma_f32_16x16x32_bf16 v[46:49], v[144:147], v[190:193], v[46:49]
	v_mfma_f32_16x16x32_bf16 v[42:45], v[158:161], v[190:193], v[42:45]
	v_mfma_f32_16x16x32_bf16 v[30:33], v[144:147], v[198:201], v[30:33]
	v_mfma_f32_16x16x32_bf16 v[26:29], v[158:161], v[198:201], v[26:29]
	v_mfma_f32_16x16x32_bf16 v[14:17], v[144:147], v[206:209], v[14:17]
	v_mfma_f32_16x16x32_bf16 v[10:13], v[158:161], v[206:209], v[10:13]
	v_mfma_f32_16x16x32_bf16 v[62:65], v[154:157], v[186:189], v[62:65]
	v_mfma_f32_16x16x32_bf16 v[58:61], v[162:165], v[186:189], v[58:61]
	v_mfma_f32_16x16x32_bf16 v[46:49], v[154:157], v[194:197], v[46:49]
	v_mfma_f32_16x16x32_bf16 v[42:45], v[162:165], v[194:197], v[42:45]
	v_mfma_f32_16x16x32_bf16 v[30:33], v[154:157], v[202:205], v[30:33]
	v_mfma_f32_16x16x32_bf16 v[26:29], v[162:165], v[202:205], v[26:29]
	v_mfma_f32_16x16x32_bf16 v[14:17], v[154:157], v[210:213], v[14:17]
	v_mfma_f32_16x16x32_bf16 v[10:13], v[162:165], v[210:213], v[10:13]
	v_mfma_f32_16x16x32_bf16 v[54:57], v[166:169], v[182:185], v[54:57]
	v_mfma_f32_16x16x32_bf16 v[50:53], v[174:177], v[182:185], v[50:53]
	v_mfma_f32_16x16x32_bf16 v[38:41], v[166:169], v[190:193], v[38:41]
	v_mfma_f32_16x16x32_bf16 v[34:37], v[174:177], v[190:193], v[34:37]
	v_mfma_f32_16x16x32_bf16 v[22:25], v[166:169], v[198:201], v[22:25]
	v_mfma_f32_16x16x32_bf16 v[18:21], v[174:177], v[198:201], v[18:21]
	v_mfma_f32_16x16x32_bf16 v[6:9], v[166:169], v[206:209], v[6:9]
	v_mfma_f32_16x16x32_bf16 v[2:5], v[174:177], v[206:209], v[2:5]
	v_mfma_f32_16x16x32_bf16 v[54:57], v[170:173], v[186:189], v[54:57]
	v_mfma_f32_16x16x32_bf16 v[50:53], v[178:181], v[186:189], v[50:53]
	v_mfma_f32_16x16x32_bf16 v[38:41], v[170:173], v[194:197], v[38:41]
	v_mfma_f32_16x16x32_bf16 v[34:37], v[178:181], v[194:197], v[34:37]
	v_mfma_f32_16x16x32_bf16 v[22:25], v[170:173], v[202:205], v[22:25]
	v_mfma_f32_16x16x32_bf16 v[18:21], v[178:181], v[202:205], v[18:21]
	v_mfma_f32_16x16x32_bf16 v[6:9], v[170:173], v[210:213], v[6:9]
	v_mfma_f32_16x16x32_bf16 v[2:5], v[178:181], v[210:213], v[2:5]
	s_barrier
	s_add_i32 s19, s19, 2
	s_add_u32 s48, s48, 0x100
	s_addc_u32 s49, s49, 0
	s_add_u32 s17, s17, 0x100
	s_addc_u32 s18, s18, 0
	s_cmp_gt_u32 s19, 13
	s_cbranch_scc0 .LBB0_1392
	v_readlane_b32 s18, v252, 14
	v_readlane_b32 s19, v252, 15
	s_and_b64 vcc, exec, s[18:19]
	s_cbranch_vccz .LBB0_1395
	s_barrier

; #define PG8_STAGE(bufoff, gbase, voff) do { _Pragma("unroll") for (int _i = 0; _i < 2; ++_i) \
;         __builtin_amdgcn_global_load_lds((const unsigned*)((const char*)(gbase) + (voff)[_i]), (LAS unsigned*)(lds + (bufoff) + ldsw + _i * 8192), 16, 0, 0); } while (0)
; #define PG8_STAGE_A(bufoff, h, kp, nx) do { if constexpr (GATHER) { const unsigned _p = (nx) ? ng[h] : cg[h]; unsigned _v[2]; _v[0] = (_p & 0xffffu) * lda + CA2[0]; _v[1] = (_p >> 16) * lda + CA2[1]; PG8_STAGE(bufoff, kp, _v); } \
;         else { PG8_STAGE(bufoff, (kp) + (h) * hstepA, voffA); } } while (0)
; #define PG8_LDA(dst, b, h) do { _Pragma("unroll") for (int m = 0; m < 4; ++m) _Pragma("unroll") for (int k = 0; k < 2; ++k) dst[m][k] = *(const LAS bf16x8*)(lds + PG8_SA(b, h) + aoff + m * 2048 + k * 1024); } while (0)
; #define PG8_LDB(dst, b, h) do { _Pragma("unroll") for (int n = 0; n < 2; ++n) _Pragma("unroll") for (int k = 0; k < 2; ++k) dst[n][k] = *(const LAS bf16x8*)(lds + PG8_SB(b, h) + boff + n * 2048 + k * 1024); } while (0)
; #define PG8_MMA(ai, bj, At, Bt) do { __builtin_amdgcn_s_setprio(1); _Pragma("unroll") for (int m = 0; m < 4; ++m) _Pragma("unroll") for (int n = 0; n < 2; ++n) _Pragma("unroll") for (int k = 0; k < 2; ++k) \
;         acc[ai][bj][m][n] = __builtin_amdgcn_mfma_f32_16x16x32_bf16(Bt[n][k], At[m][k], acc[ai][bj][m][n], 0, 0, 0); __builtin_amdgcn_s_setprio(0); } while (0)
; #define PG8_WAIT_V(n) asm volatile("s_waitcnt vmcnt(" #n ")" ::: "memory")
;     ...
;         for (int t = 0; t < nt; t += 2) {
;             const bool last = (t == nt - 2);
;             const char* a1 = cA + (size_t)(t + 1) * kstep;
;             const char* a2 = last ? nA : cA + (size_t)(t + 2) * kstep; const char* b2 = last ? nB : cB + (size_t)(t + 2) * kstep;
;             const char* a3 = a2 + kstep; const char* b3 = b2 + kstep;
;             PG8_LDB(B0, 0, 0); PG8_LDB(B1, 0, 1); PG8_SCHED; PG8_LDA(At, 0, 0); PG8_STAGE_A(PG8_SA(1, 1), 1, a1, false);
;             PG8_WAIT_V(8); PG8_WAIT_L(0); PG8_BAR; if (cur.amask & 1) { PG8_MMA(0, 0, At, B0); PG8_MMA(0, 1, At, B1); } PG8_BAR; PG8_SCHED;
;             PG8_LDA(At, 0, 1); PG8_STAGE(PG8_SB(0, 0), b2, voffB); PG8_STAGE(PG8_SB(0, 1), b2 + hstepB, voffB); PG8_STAGE_A(PG8_SA(0, 0), 0, a2, last);
;             PG8_WAIT_V(8); PG8_WAIT_L(0); PG8_BAR; if (cur.amask & 2) { PG8_MMA(1, 0, At, B0); PG8_MMA(1, 1, At, B1); } PG8_BAR; PG8_SCHED;
.LBB0_1598:
	v_add_u32_e32 v0, 0x10000, v215
	ds_read_b128 v[146:149], v0
	ds_read_b128 v[150:153], v0 offset:1024
	ds_read_b128 v[154:157], v0 offset:2048
	ds_read_b128 v[158:161], v0 offset:3072
	v_add_u32_e32 v0, 0x14000, v215
	ds_read_b128 v[130:133], v0
	ds_read_b128 v[134:137], v0 offset:1024
	ds_read_b128 v[138:141], v0 offset:2048
	ds_read_b128 v[142:145], v0 offset:3072
	v_lshl_add_u64 v[204:205], s[40:41], 0, v[200:201]
	s_add_i32 m0, s85, 0xc000
	s_waitcnt lgkmcnt(0)
	ds_read_b128 v[186:189], v223
	ds_read_b128 v[190:193], v223 offset:1024
	ds_read_b128 v[178:181], v223 offset:2048
	ds_read_b128 v[182:185], v223 offset:3072
	ds_read_b128 v[170:173], v223 offset:4096
	ds_read_b128 v[174:177], v223 offset:5120
	ds_read_b128 v[162:165], v223 offset:6144
	ds_read_b128 v[166:169], v223 offset:7168
	global_load_lds_dwordx4 v[204:205], off
	v_lshl_add_u64 v[204:205], s[40:41], 0, v[202:203]
	s_add_i32 m0, s85, 0xe000
	v_cndmask_b32_e64 v0, 0, 1, s[38:39]
	global_load_lds_dwordx4 v[204:205], off
	s_waitcnt vmcnt(8)
	s_waitcnt lgkmcnt(0)
	v_cmp_ne_u32_e64 s[62:63], 1, v0
	s_andn2_b64 vcc, exec, s[38:39]
	s_barrier
	s_cbranch_vccnz .LBB0_1600
	s_waitcnt lgkmcnt(0)
	v_mfma_f32_16x16x32_bf16 v[126:129], v[146:149], v[186:189], v[126:129]
	v_mfma_f32_16x16x32_bf16 v[118:121], v[154:157], v[186:189], v[118:121]
	v_mfma_f32_16x16x32_bf16 v[110:113], v[146:149], v[178:181], v[110:113]
	v_mfma_f32_16x16x32_bf16 v[102:105], v[154:157], v[178:181], v[102:105]
	v_mfma_f32_16x16x32_bf16 v[94:97], v[146:149], v[170:173], v[94:97]
	v_mfma_f32_16x16x32_bf16 v[86:89], v[154:157], v[170:173], v[86:89]
	v_mfma_f32_16x16x32_bf16 v[78:81], v[146:149], v[162:165], v[78:81]
	v_mfma_f32_16x16x32_bf16 v[70:73], v[154:157], v[162:165], v[70:73]
	v_mfma_f32_16x16x32_bf16 v[126:129], v[150:153], v[190:193], v[126:129]
	v_mfma_f32_16x16x32_bf16 v[118:121], v[158:161], v[190:193], v[118:121]
	v_mfma_f32_16x16x32_bf16 v[110:113], v[150:153], v[182:185], v[110:113]
	v_mfma_f32_16x16x32_bf16 v[102:105], v[158:161], v[182:185], v[102:105]
	v_mfma_f32_16x16x32_bf16 v[94:97], v[150:153], v[174:177], v[94:97]
	v_mfma_f32_16x16x32_bf16 v[86:89], v[158:161], v[174:177], v[86:89]
	v_mfma_f32_16x16x32_bf16 v[78:81], v[150:153], v[166:169], v[78:81]
	v_mfma_f32_16x16x32_bf16 v[70:73], v[158:161], v[166:169], v[70:73]
	v_mfma_f32_16x16x32_bf16 v[122:125], v[130:133], v[186:189], v[122:125]
	v_mfma_f32_16x16x32_bf16 v[114:117], v[138:141], v[186:189], v[114:117]
	v_mfma_f32_16x16x32_bf16 v[106:109], v[130:133], v[178:181], v[106:109]
	v_mfma_f32_16x16x32_bf16 v[98:101], v[138:141], v[178:181], v[98:101]
	v_mfma_f32_16x16x32_bf16 v[90:93], v[130:133], v[170:173], v[90:93]
	v_mfma_f32_16x16x32_bf16 v[82:85], v[138:141], v[170:173], v[82:85]
	v_mfma_f32_16x16x32_bf16 v[74:77], v[130:133], v[162:165], v[74:77]
	v_mfma_f32_16x16x32_bf16 v[66:69], v[138:141], v[162:165], v[66:69]
	v_mfma_f32_16x16x32_bf16 v[122:125], v[134:137], v[190:193], v[122:125]
	v_mfma_f32_16x16x32_bf16 v[114:117], v[142:145], v[190:193], v[114:117]
	v_mfma_f32_16x16x32_bf16 v[106:109], v[134:137], v[182:185], v[106:109]
	v_mfma_f32_16x16x32_bf16 v[98:101], v[142:145], v[182:185], v[98:101]
	v_mfma_f32_16x16x32_bf16 v[90:93], v[134:137], v[174:177], v[90:93]
	v_mfma_f32_16x16x32_bf16 v[82:85], v[142:145], v[174:177], v[82:85]
	v_mfma_f32_16x16x32_bf16 v[74:77], v[134:137], v[166:169], v[74:77]
	v_mfma_f32_16x16x32_bf16 v[66:69], v[142:145], v[166:169], v[66:69]
.LBB0_1600:
	s_add_u32 s60, s40, 0x80
	s_addc_u32 s61, s41, 0
	s_cmp_eq_u32 s67, 28
	s_cselect_b64 s[64:65], -1, 0
	s_and_b64 s[50:51], s[64:65], exec
	s_cselect_b32 s81, s73, s61
	s_cselect_b32 s80, s72, s60
	s_cselect_b32 s51, s77, s31
	s_cselect_b32 s50, s76, s5
	s_barrier
	s_mov_b32 m0, s6
	v_lshl_add_u64 v[204:205], s[50:51], 0, v[194:195]
	s_add_u32 s60, s50, 0x80000
	s_waitcnt lgkmcnt(0)
	ds_read_b128 v[186:189], v223 offset:16384
	ds_read_b128 v[190:193], v223 offset:17408
	ds_read_b128 v[178:181], v223 offset:18432
	ds_read_b128 v[182:185], v223 offset:19456
	ds_read_b128 v[170:173], v223 offset:20480
	ds_read_b128 v[174:177], v223 offset:21504
	ds_read_b128 v[162:165], v223 offset:22528
	ds_read_b128 v[166:169], v223 offset:23552
	global_load_lds_dwordx4 v[204:205], off
	v_lshl_add_u64 v[206:207], s[50:51], 0, v[196:197]
	s_mov_b32 m0, s7
	s_addc_u32 s61, s51, 0
	global_load_lds_dwordx4 v[206:207], off
	v_lshl_add_u64 v[208:209], s[60:61], 0, v[194:195]
	s_mov_b32 m0, s8
	s_andn2_b64 vcc, exec, s[48:49]
	global_load_lds_dwordx4 v[208:209], off
	v_lshl_add_u64 v[208:209], s[60:61], 0, v[196:197]
	s_mov_b32 m0, s9
	s_nop 0
	global_load_lds_dwordx4 v[208:209], off
	v_cndmask_b32_e64 v208, v226, v224, s[64:65]
	v_lshlrev_b32_e32 v0, 12, v208
	v_and_b32_e32 v0, 0xffff000, v0
	v_add_u32_e32 v0, v0, v212
	v_bfe_u32 v208, v208, 16, 16
	s_mov_b32 m0, s85
	v_lshl_add_u32 v208, v208, 12, v213
	global_load_lds_dwordx4 v0, s[80:81]
	s_mov_b32 m0, s10
	v_cndmask_b32_e64 v209, 0, 1, s[48:49]
	global_load_lds_dwordx4 v208, s[80:81]
	s_waitcnt vmcnt(8)
	s_waitcnt lgkmcnt(0)
	v_cmp_ne_u32_e64 s[60:61], 1, v209
	s_barrier
	s_cbranch_vccnz .LBB0_1602
; #define PG8_STAGE(bufoff, gbase, voff) do { _Pragma("unroll") for (int _i = 0; _i < 2; ++_i) \
;         __builtin_amdgcn_global_load_lds((const unsigned*)((const char*)(gbase) + (voff)[_i]), (LAS unsigned*)(lds + (bufoff) + ldsw + _i * 8192), 16, 0, 0); } while (0)
; #define PG8_STAGE_A(bufoff, h, kp, nx) do { if constexpr (GATHER) { const unsigned _p = (nx) ? ng[h] : cg[h]; unsigned _v[2]; _v[0] = (_p & 0xffffu) * lda + CA2[0]; _v[1] = (_p >> 16) * lda + CA2[1]; PG8_STAGE(bufoff, kp, _v); } \
;         else { PG8_STAGE(bufoff, (kp) + (h) * hstepA, voffA); } } while (0)
; #define PG8_LDA(dst, b, h) do { _Pragma("unroll") for (int m = 0; m < 4; ++m) _Pragma("unroll") for (int k = 0; k < 2; ++k) dst[m][k] = *(const LAS bf16x8*)(lds + PG8_SA(b, h) + aoff + m * 2048 + k * 1024); } while (0)
; #define PG8_LDB(dst, b, h) do { _Pragma("unroll") for (int n = 0; n < 2; ++n) _Pragma("unroll") for (int k = 0; k < 2; ++k) dst[n][k] = *(const LAS bf16x8*)(lds + PG8_SB(b, h) + boff + n * 2048 + k * 1024); } while (0)
; #define PG8_MMA(ai, bj, At, Bt) do { __builtin_amdgcn_s_setprio(1); _Pragma("unroll") for (int m = 0; m < 4; ++m) _Pragma("unroll") for (int n = 0; n < 2; ++n) _Pragma("unroll") for (int k = 0; k < 2; ++k) \
;         acc[ai][bj][m][n] = __builtin_amdgcn_mfma_f32_16x16x32_bf16(Bt[n][k], At[m][k], acc[ai][bj][m][n], 0, 0, 0); __builtin_amdgcn_s_setprio(0); } while (0)
; #define PG8_WAIT_V(n) asm volatile("s_waitcnt vmcnt(" #n ")" ::: "memory")
; #define PG8_WAIT_L(n) asm volatile("s_waitcnt lgkmcnt(" #n ")" ::: "memory")
; #define PG8_BAR __builtin_amdgcn_s_barrier()
; #define PG8_SCHED __builtin_amdgcn_sched_barrier(0)
;     ...
;             PG8_WAIT_V(8); PG8_WAIT_L(0); PG8_BAR; if (cur.amask & 2) { PG8_MMA(1, 0, At, B0); PG8_MMA(1, 1, At, B1); } PG8_BAR; PG8_SCHED;
;             PG8_LDB(B0, 1, 0); PG8_LDB(B1, 1, 1); PG8_SCHED; PG8_LDA(At, 1, 0); PG8_STAGE_A(PG8_SA(0, 1), 1, a2, last);
;             PG8_WAIT_V(8); PG8_WAIT_L(0); PG8_BAR; if (cur.amask & 1) { PG8_MMA(0, 0, At, B0); PG8_MMA(0, 1, At, B1); } PG8_BAR; PG8_SCHED;
;             PG8_LDA(At, 1, 1); PG8_STAGE(PG8_SB(1, 0), b3, voffB); PG8_STAGE(PG8_SB(1, 1), b3 + hstepB, voffB); PG8_STAGE_A(PG8_SA(1, 0), 0, a3, last);
;             PG8_WAIT_V(8); PG8_WAIT_L(0); PG8_BAR; if (cur.amask & 2) { PG8_MMA(1, 0, At, B0); PG8_MMA(1, 1, At, B1); } PG8_BAR; PG8_SCHED;
	s_waitcnt lgkmcnt(0)
	v_mfma_f32_16x16x32_bf16 v[58:61], v[146:149], v[186:189], v[58:61]
	v_mfma_f32_16x16x32_bf16 v[54:57], v[154:157], v[186:189], v[54:57]
	v_mfma_f32_16x16x32_bf16 v[46:49], v[146:149], v[178:181], v[46:49]
	v_mfma_f32_16x16x32_bf16 v[38:41], v[154:157], v[178:181], v[38:41]
	v_mfma_f32_16x16x32_bf16 v[30:33], v[146:149], v[170:173], v[30:33]
	v_mfma_f32_16x16x32_bf16 v[22:25], v[154:157], v[170:173], v[22:25]
	v_mfma_f32_16x16x32_bf16 v[14:17], v[146:149], v[162:165], v[14:17]
	v_mfma_f32_16x16x32_bf16 v[6:9], v[154:157], v[162:165], v[6:9]
	v_mfma_f32_16x16x32_bf16 v[58:61], v[150:153], v[190:193], v[58:61]
	v_mfma_f32_16x16x32_bf16 v[54:57], v[158:161], v[190:193], v[54:57]
	v_mfma_f32_16x16x32_bf16 v[46:49], v[150:153], v[182:185], v[46:49]
	v_mfma_f32_16x16x32_bf16 v[38:41], v[158:161], v[182:185], v[38:41]
	v_mfma_f32_16x16x32_bf16 v[30:33], v[150:153], v[174:177], v[30:33]
	v_mfma_f32_16x16x32_bf16 v[22:25], v[158:161], v[174:177], v[22:25]
	v_mfma_f32_16x16x32_bf16 v[14:17], v[150:153], v[166:169], v[14:17]
	v_mfma_f32_16x16x32_bf16 v[6:9], v[158:161], v[166:169], v[6:9]
	v_mfma_f32_16x16x32_bf16 v[62:65], v[130:133], v[186:189], v[62:65]
	v_mfma_f32_16x16x32_bf16 v[50:53], v[138:141], v[186:189], v[50:53]
	v_mfma_f32_16x16x32_bf16 v[42:45], v[130:133], v[178:181], v[42:45]
	v_mfma_f32_16x16x32_bf16 v[34:37], v[138:141], v[178:181], v[34:37]
	v_mfma_f32_16x16x32_bf16 v[26:29], v[130:133], v[170:173], v[26:29]
	v_mfma_f32_16x16x32_bf16 v[18:21], v[138:141], v[170:173], v[18:21]
	v_mfma_f32_16x16x32_bf16 v[10:13], v[130:133], v[162:165], v[10:13]
	v_mfma_f32_16x16x32_bf16 v[2:5], v[138:141], v[162:165], v[2:5]
	v_mfma_f32_16x16x32_bf16 v[62:65], v[134:137], v[190:193], v[62:65]
	v_mfma_f32_16x16x32_bf16 v[50:53], v[142:145], v[190:193], v[50:53]
	v_mfma_f32_16x16x32_bf16 v[42:45], v[134:137], v[182:185], v[42:45]
	v_mfma_f32_16x16x32_bf16 v[34:37], v[142:145], v[182:185], v[34:37]
	v_mfma_f32_16x16x32_bf16 v[26:29], v[134:137], v[174:177], v[26:29]
	v_mfma_f32_16x16x32_bf16 v[18:21], v[142:145], v[174:177], v[18:21]
	v_mfma_f32_16x16x32_bf16 v[10:13], v[134:137], v[166:169], v[10:13]
	v_mfma_f32_16x16x32_bf16 v[2:5], v[142:145], v[166:169], v[2:5]
.LBB0_1602:
	s_barrier
	v_add_u32_e32 v130, 0x18000, v215
	v_add_u32_e32 v142, 0x1c000, v215
	ds_read_b128 v[146:149], v130
	ds_read_b128 v[150:153], v130 offset:1024
	ds_read_b128 v[154:157], v130 offset:2048
	ds_read_b128 v[158:161], v130 offset:3072
	ds_read_b128 v[130:133], v142
	ds_read_b128 v[134:137], v142 offset:1024
	ds_read_b128 v[138:141], v142 offset:2048
	ds_read_b128 v[142:145], v142 offset:3072
	v_cndmask_b32_e64 v209, v227, v225, s[64:65]
	v_lshlrev_b32_e32 v228, 12, v209
	v_and_b32_e32 v228, 0xffff000, v228
	s_mov_b32 m0, s11
	v_add_u32_e32 v228, v228, v212
	v_bfe_u32 v209, v209, 16, 16
	s_waitcnt lgkmcnt(0)
	ds_read_b128 v[186:189], v223 offset:32768
	ds_read_b128 v[190:193], v223 offset:33792
	ds_read_b128 v[178:181], v223 offset:34816
	ds_read_b128 v[182:185], v223 offset:35840
	ds_read_b128 v[170:173], v223 offset:36864
	ds_read_b128 v[174:177], v223 offset:37888
	ds_read_b128 v[162:165], v223 offset:38912
	ds_read_b128 v[166:169], v223 offset:39936
	v_lshl_add_u32 v209, v209, 12, v213
	global_load_lds_dwordx4 v228, s[80:81]
	s_mov_b32 m0, s12
	s_and_b64 vcc, exec, s[62:63]
	global_load_lds_dwordx4 v209, s[80:81]
	s_waitcnt vmcnt(8)
	s_waitcnt lgkmcnt(0)
	s_barrier
	s_cbranch_vccnz .LBB0_1604
	s_waitcnt lgkmcnt(0)
	v_mfma_f32_16x16x32_bf16 v[126:129], v[146:149], v[186:189], v[126:129]
	v_mfma_f32_16x16x32_bf16 v[118:121], v[154:157], v[186:189], v[118:121]
	v_mfma_f32_16x16x32_bf16 v[110:113], v[146:149], v[178:181], v[110:113]
	v_mfma_f32_16x16x32_bf16 v[102:105], v[154:157], v[178:181], v[102:105]
	v_mfma_f32_16x16x32_bf16 v[94:97], v[146:149], v[170:173], v[94:97]
	v_mfma_f32_16x16x32_bf16 v[86:89], v[154:157], v[170:173], v[86:89]
	v_mfma_f32_16x16x32_bf16 v[78:81], v[146:149], v[162:165], v[78:81]
	v_mfma_f32_16x16x32_bf16 v[70:73], v[154:157], v[162:165], v[70:73]
	v_mfma_f32_16x16x32_bf16 v[126:129], v[150:153], v[190:193], v[126:129]
	v_mfma_f32_16x16x32_bf16 v[118:121], v[158:161], v[190:193], v[118:121]
	v_mfma_f32_16x16x32_bf16 v[110:113], v[150:153], v[182:185], v[110:113]
	v_mfma_f32_16x16x32_bf16 v[102:105], v[158:161], v[182:185], v[102:105]
	v_mfma_f32_16x16x32_bf16 v[94:97], v[150:153], v[174:177], v[94:97]
	v_mfma_f32_16x16x32_bf16 v[86:89], v[158:161], v[174:177], v[86:89]
	v_mfma_f32_16x16x32_bf16 v[78:81], v[150:153], v[166:169], v[78:81]
	v_mfma_f32_16x16x32_bf16 v[70:73], v[158:161], v[166:169], v[70:73]
	v_mfma_f32_16x16x32_bf16 v[122:125], v[130:133], v[186:189], v[122:125]
	v_mfma_f32_16x16x32_bf16 v[114:117], v[138:141], v[186:189], v[114:117]
	v_mfma_f32_16x16x32_bf16 v[106:109], v[130:133], v[178:181], v[106:109]
	v_mfma_f32_16x16x32_bf16 v[98:101], v[138:141], v[178:181], v[98:101]
	v_mfma_f32_16x16x32_bf16 v[90:93], v[130:133], v[170:173], v[90:93]
	v_mfma_f32_16x16x32_bf16 v[82:85], v[138:141], v[170:173], v[82:85]
	v_mfma_f32_16x16x32_bf16 v[74:77], v[130:133], v[162:165], v[74:77]
	v_mfma_f32_16x16x32_bf16 v[66:69], v[138:141], v[162:165], v[66:69]
	v_mfma_f32_16x16x32_bf16 v[122:125], v[134:137], v[190:193], v[122:125]
	v_mfma_f32_16x16x32_bf16 v[114:117], v[142:145], v[190:193], v[114:117]
	v_mfma_f32_16x16x32_bf16 v[106:109], v[134:137], v[182:185], v[106:109]
	v_mfma_f32_16x16x32_bf16 v[98:101], v[142:145], v[182:185], v[98:101]
	v_mfma_f32_16x16x32_bf16 v[90:93], v[134:137], v[174:177], v[90:93]
	v_mfma_f32_16x16x32_bf16 v[82:85], v[142:145], v[174:177], v[82:85]
	v_mfma_f32_16x16x32_bf16 v[74:77], v[134:137], v[166:169], v[74:77]
	v_mfma_f32_16x16x32_bf16 v[66:69], v[142:145], v[166:169], v[66:69]
; #define PG8_STAGE(bufoff, gbase, voff) do { _Pragma("unroll") for (int _i = 0; _i < 2; ++_i) \
;         __builtin_amdgcn_global_load_lds((const unsigned*)((const char*)(gbase) + (voff)[_i]), (LAS unsigned*)(lds + (bufoff) + ldsw + _i * 8192), 16, 0, 0); } while (0)
; #define PG8_STAGE_A(bufoff, h, kp, nx) do { if constexpr (GATHER) { const unsigned _p = (nx) ? ng[h] : cg[h]; unsigned _v[2]; _v[0] = (_p & 0xffffu) * lda + CA2[0]; _v[1] = (_p >> 16) * lda + CA2[1]; PG8_STAGE(bufoff, kp, _v); } \
;         else { PG8_STAGE(bufoff, (kp) + (h) * hstepA, voffA); } } while (0)
; #define PG8_LDA(dst, b, h) do { _Pragma("unroll") for (int m = 0; m < 4; ++m) _Pragma("unroll") for (int k = 0; k < 2; ++k) dst[m][k] = *(const LAS bf16x8*)(lds + PG8_SA(b, h) + aoff + m * 2048 + k * 1024); } while (0)
; #define PG8_MMA(ai, bj, At, Bt) do { __builtin_amdgcn_s_setprio(1); _Pragma("unroll") for (int m = 0; m < 4; ++m) _Pragma("unroll") for (int n = 0; n < 2; ++n) _Pragma("unroll") for (int k = 0; k < 2; ++k) \
;         acc[ai][bj][m][n] = __builtin_amdgcn_mfma_f32_16x16x32_bf16(Bt[n][k], At[m][k], acc[ai][bj][m][n], 0, 0, 0); __builtin_amdgcn_s_setprio(0); } while (0)
; #define PG8_WAIT_V(n) asm volatile("s_waitcnt vmcnt(" #n ")" ::: "memory")
; #define PG8_WAIT_L(n) asm volatile("s_waitcnt lgkmcnt(" #n ")" ::: "memory")
; #define PG8_BAR __builtin_amdgcn_s_barrier()
; #define PG8_SCHED __builtin_amdgcn_sched_barrier(0)
;     ...
;             PG8_LDA(At, 1, 1); PG8_STAGE(PG8_SB(1, 0), b3, voffB); PG8_STAGE(PG8_SB(1, 1), b3 + hstepB, voffB); PG8_STAGE_A(PG8_SA(1, 0), 0, a3, last);
;             PG8_WAIT_V(8); PG8_WAIT_L(0); PG8_BAR; if (cur.amask & 2) { PG8_MMA(1, 0, At, B0); PG8_MMA(1, 1, At, B1); } PG8_BAR; PG8_SCHED;
;         }
.LBB0_1604:
	v_mov_b32_e32 v209, v1
	v_lshl_add_u64 v[228:229], s[80:81], 0, v[0:1]
	v_lshl_add_u64 v[208:209], s[80:81], 0, v[208:209]
	s_barrier
	s_mov_b32 m0, s18
	v_lshl_add_u64 v[204:205], v[204:205], 0, s[92:93]
	s_add_u32 s50, s50, 0x80080
	s_waitcnt lgkmcnt(0)
	ds_read_b128 v[186:189], v223 offset:49152
	ds_read_b128 v[190:193], v223 offset:50176
	ds_read_b128 v[178:181], v223 offset:51200
	ds_read_b128 v[182:185], v223 offset:52224
	ds_read_b128 v[170:173], v223 offset:53248
	ds_read_b128 v[174:177], v223 offset:54272
	ds_read_b128 v[162:165], v223 offset:55296
	ds_read_b128 v[166:169], v223 offset:56320
	global_load_lds_dwordx4 v[204:205], off
	v_lshl_add_u64 v[204:205], v[206:207], 0, s[92:93]
	s_mov_b32 m0, s19
	s_addc_u32 s51, s51, 0
	global_load_lds_dwordx4 v[204:205], off
	v_lshl_add_u64 v[204:205], s[50:51], 0, v[194:195]
	s_mov_b32 m0, s22
	s_and_b64 vcc, exec, s[60:61]
	global_load_lds_dwordx4 v[204:205], off
	v_lshl_add_u64 v[204:205], s[50:51], 0, v[196:197]
	s_mov_b32 m0, s23
	s_nop 0
	global_load_lds_dwordx4 v[204:205], off
	v_lshl_add_u64 v[204:205], v[228:229], 0, s[92:93]
	s_mov_b32 m0, s20
	s_nop 0
	global_load_lds_dwordx4 v[204:205], off
	v_lshl_add_u64 v[204:205], v[208:209], 0, s[92:93]
	s_mov_b32 m0, s21
	s_nop 0
	global_load_lds_dwordx4 v[204:205], off
	s_waitcnt vmcnt(8)
	s_waitcnt lgkmcnt(0)
	s_barrier
	s_cbranch_vccnz .LBB0_1597
	s_waitcnt lgkmcnt(0)
	v_mfma_f32_16x16x32_bf16 v[58:61], v[146:149], v[186:189], v[58:61]
	v_mfma_f32_16x16x32_bf16 v[54:57], v[154:157], v[186:189], v[54:57]
	v_mfma_f32_16x16x32_bf16 v[46:49], v[146:149], v[178:181], v[46:49]
	v_mfma_f32_16x16x32_bf16 v[38:41], v[154:157], v[178:181], v[38:41]
	v_mfma_f32_16x16x32_bf16 v[30:33], v[146:149], v[170:173], v[30:33]
	v_mfma_f32_16x16x32_bf16 v[22:25], v[154:157], v[170:173], v[22:25]
	v_mfma_f32_16x16x32_bf16 v[14:17], v[146:149], v[162:165], v[14:17]
	v_mfma_f32_16x16x32_bf16 v[6:9], v[154:157], v[162:165], v[6:9]
	v_mfma_f32_16x16x32_bf16 v[58:61], v[150:153], v[190:193], v[58:61]
	v_mfma_f32_16x16x32_bf16 v[54:57], v[158:161], v[190:193], v[54:57]
	v_mfma_f32_16x16x32_bf16 v[46:49], v[150:153], v[182:185], v[46:49]
	v_mfma_f32_16x16x32_bf16 v[38:41], v[158:161], v[182:185], v[38:41]
	v_mfma_f32_16x16x32_bf16 v[30:33], v[150:153], v[174:177], v[30:33]
	v_mfma_f32_16x16x32_bf16 v[22:25], v[158:161], v[174:177], v[22:25]
	v_mfma_f32_16x16x32_bf16 v[14:17], v[150:153], v[166:169], v[14:17]
	v_mfma_f32_16x16x32_bf16 v[6:9], v[158:161], v[166:169], v[6:9]
	v_mfma_f32_16x16x32_bf16 v[62:65], v[130:133], v[186:189], v[62:65]
	v_mfma_f32_16x16x32_bf16 v[50:53], v[138:141], v[186:189], v[50:53]
	v_mfma_f32_16x16x32_bf16 v[42:45], v[130:133], v[178:181], v[42:45]
	v_mfma_f32_16x16x32_bf16 v[34:37], v[138:141], v[178:181], v[34:37]
	v_mfma_f32_16x16x32_bf16 v[26:29], v[130:133], v[170:173], v[26:29]
	v_mfma_f32_16x16x32_bf16 v[18:21], v[138:141], v[170:173], v[18:21]
	v_mfma_f32_16x16x32_bf16 v[10:13], v[130:133], v[162:165], v[10:13]
	v_mfma_f32_16x16x32_bf16 v[2:5], v[138:141], v[162:165], v[2:5]
	v_mfma_f32_16x16x32_bf16 v[62:65], v[134:137], v[190:193], v[62:65]
	v_mfma_f32_16x16x32_bf16 v[50:53], v[142:145], v[190:193], v[50:53]
	v_mfma_f32_16x16x32_bf16 v[42:45], v[134:137], v[182:185], v[42:45]
	v_mfma_f32_16x16x32_bf16 v[34:37], v[142:145], v[182:185], v[34:37]
	v_mfma_f32_16x16x32_bf16 v[26:29], v[134:137], v[174:177], v[26:29]
	v_mfma_f32_16x16x32_bf16 v[18:21], v[142:145], v[174:177], v[18:21]
	v_mfma_f32_16x16x32_bf16 v[10:13], v[134:137], v[166:169], v[10:13]
	v_mfma_f32_16x16x32_bf16 v[2:5], v[142:145], v[166:169], v[2:5]
	s_branch .LBB0_1597

; #define PG8_STAGE(bufoff, gbase, voff) do { _Pragma("unroll") for (int _i = 0; _i < 2; ++_i) \
;         __builtin_amdgcn_global_load_lds((const unsigned*)((const char*)(gbase) + (voff)[_i]), (LAS unsigned*)(lds + (bufoff) + ldsw + _i * 8192), 16, 0, 0); } while (0)
; #define PG8_STAGE_A(bufoff, h, kp, nx) do { if constexpr (GATHER) { const unsigned _p = (nx) ? ng[h] : cg[h]; unsigned _v[2]; _v[0] = (_p & 0xffffu) * lda + CA2[0]; _v[1] = (_p >> 16) * lda + CA2[1]; PG8_STAGE(bufoff, kp, _v); } \
;         else { PG8_STAGE(bufoff, (kp) + (h) * hstepA, voffA); } } while (0)
; #define PG8_LDA(dst, b, h) do { _Pragma("unroll") for (int m = 0; m < 4; ++m) _Pragma("unroll") for (int k = 0; k < 2; ++k) dst[m][k] = *(const LAS bf16x8*)(lds + PG8_SA(b, h) + aoff + m * 2048 + k * 1024); } while (0)
; #define PG8_LDB(dst, b, h) do { _Pragma("unroll") for (int n = 0; n < 2; ++n) _Pragma("unroll") for (int k = 0; k < 2; ++k) dst[n][k] = *(const LAS bf16x8*)(lds + PG8_SB(b, h) + boff + n * 2048 + k * 1024); } while (0)
; #define PG8_MMA(ai, bj, At, Bt) do { __builtin_amdgcn_s_setprio(1); _Pragma("unroll") for (int m = 0; m < 4; ++m) _Pragma("unroll") for (int n = 0; n < 2; ++n) _Pragma("unroll") for (int k = 0; k < 2; ++k) \
;         acc[ai][bj][m][n] = __builtin_amdgcn_mfma_f32_16x16x32_bf16(Bt[n][k], At[m][k], acc[ai][bj][m][n], 0, 0, 0); __builtin_amdgcn_s_setprio(0); } while (0)
; #define PG8_WAIT_V(n) asm volatile("s_waitcnt vmcnt(" #n ")" ::: "memory")
;     ...
;         for (int t = 0; t < nt; t += 2) {
;             const bool last = (t == nt - 2);
;             const char* a1 = cA + (size_t)(t + 1) * kstep;
;             const char* a2 = last ? nA : cA + (size_t)(t + 2) * kstep; const char* b2 = last ? nB : cB + (size_t)(t + 2) * kstep;
;             const char* a3 = a2 + kstep; const char* b3 = b2 + kstep;
;             PG8_LDB(B0, 0, 0); PG8_LDB(B1, 0, 1); PG8_SCHED; PG8_LDA(At, 0, 0); PG8_STAGE_A(PG8_SA(1, 1), 1, a1, false);
;             PG8_WAIT_V(8); PG8_WAIT_L(0); PG8_BAR; if (cur.amask & 1) { PG8_MMA(0, 0, At, B0); PG8_MMA(0, 1, At, B1); } PG8_BAR; PG8_SCHED;
;             PG8_LDA(At, 0, 1); PG8_STAGE(PG8_SB(0, 0), b2, voffB); PG8_STAGE(PG8_SB(0, 1), b2 + hstepB, voffB); PG8_STAGE_A(PG8_SA(0, 0), 0, a2, last);
;             PG8_WAIT_V(8); PG8_WAIT_L(0); PG8_BAR; if (cur.amask & 2) { PG8_MMA(1, 0, At, B0); PG8_MMA(1, 1, At, B1); } PG8_BAR; PG8_SCHED;
.LBB0_1626:
	v_add_u32_e32 v0, 0x10000, v224
	ds_read_b128 v[148:151], v0
	ds_read_b128 v[152:155], v0 offset:1024
	ds_read_b128 v[156:159], v0 offset:2048
	ds_read_b128 v[160:163], v0 offset:3072
	v_add_u32_e32 v0, 0x14000, v224
	ds_read_b128 v[132:135], v0
	ds_read_b128 v[136:139], v0 offset:1024
	ds_read_b128 v[140:143], v0 offset:2048
	ds_read_b128 v[144:147], v0 offset:3072
	v_lshl_add_u64 v[2:3], s[60:61], 0, v[206:207]
	s_add_i32 m0, s15, 0xc000
	s_waitcnt lgkmcnt(0)
	ds_read_b128 v[188:191], v225
	ds_read_b128 v[192:195], v225 offset:1024
	ds_read_b128 v[180:183], v225 offset:2048
	ds_read_b128 v[184:187], v225 offset:3072
	ds_read_b128 v[172:175], v225 offset:4096
	ds_read_b128 v[176:179], v225 offset:5120
	ds_read_b128 v[164:167], v225 offset:6144
	ds_read_b128 v[168:171], v225 offset:7168
	global_load_lds_dwordx4 v[2:3], off
	v_lshl_add_u64 v[2:3], s[60:61], 0, v[208:209]
	s_add_i32 m0, s15, 0xe000
	v_cndmask_b32_e64 v0, 0, 1, s[50:51]
	global_load_lds_dwordx4 v[2:3], off
	s_waitcnt vmcnt(8)
	s_waitcnt lgkmcnt(0)
	v_cmp_ne_u32_e64 s[58:59], 1, v0
	s_andn2_b64 vcc, exec, s[50:51]
	s_barrier
	s_cbranch_vccnz .LBB0_1628
	s_waitcnt lgkmcnt(0)
	v_mfma_f32_16x16x32_bf16 v[128:131], v[148:151], v[188:191], v[128:131]
	v_mfma_f32_16x16x32_bf16 v[124:127], v[156:159], v[188:191], v[124:127]
	v_mfma_f32_16x16x32_bf16 v[112:115], v[148:151], v[180:183], v[112:115]
	v_mfma_f32_16x16x32_bf16 v[108:111], v[156:159], v[180:183], v[108:111]
	v_mfma_f32_16x16x32_bf16 v[96:99], v[148:151], v[172:175], v[96:99]
	v_mfma_f32_16x16x32_bf16 v[92:95], v[156:159], v[172:175], v[92:95]
	v_mfma_f32_16x16x32_bf16 v[80:83], v[148:151], v[164:167], v[80:83]
	v_mfma_f32_16x16x32_bf16 v[76:79], v[156:159], v[164:167], v[76:79]
	v_mfma_f32_16x16x32_bf16 v[128:131], v[152:155], v[192:195], v[128:131]
	v_mfma_f32_16x16x32_bf16 v[124:127], v[160:163], v[192:195], v[124:127]
	v_mfma_f32_16x16x32_bf16 v[112:115], v[152:155], v[184:187], v[112:115]
	v_mfma_f32_16x16x32_bf16 v[108:111], v[160:163], v[184:187], v[108:111]
	v_mfma_f32_16x16x32_bf16 v[96:99], v[152:155], v[176:179], v[96:99]
	v_mfma_f32_16x16x32_bf16 v[92:95], v[160:163], v[176:179], v[92:95]
	v_mfma_f32_16x16x32_bf16 v[80:83], v[152:155], v[168:171], v[80:83]
	v_mfma_f32_16x16x32_bf16 v[76:79], v[160:163], v[168:171], v[76:79]
	v_mfma_f32_16x16x32_bf16 v[120:123], v[132:135], v[188:191], v[120:123]
	v_mfma_f32_16x16x32_bf16 v[116:119], v[140:143], v[188:191], v[116:119]
	v_mfma_f32_16x16x32_bf16 v[104:107], v[132:135], v[180:183], v[104:107]
	v_mfma_f32_16x16x32_bf16 v[100:103], v[140:143], v[180:183], v[100:103]
	v_mfma_f32_16x16x32_bf16 v[88:91], v[132:135], v[172:175], v[88:91]
	v_mfma_f32_16x16x32_bf16 v[84:87], v[140:143], v[172:175], v[84:87]
	v_mfma_f32_16x16x32_bf16 v[72:75], v[132:135], v[164:167], v[72:75]
	v_mfma_f32_16x16x32_bf16 v[68:71], v[140:143], v[164:167], v[68:71]
	v_mfma_f32_16x16x32_bf16 v[120:123], v[136:139], v[192:195], v[120:123]
	v_mfma_f32_16x16x32_bf16 v[116:119], v[144:147], v[192:195], v[116:119]
	v_mfma_f32_16x16x32_bf16 v[104:107], v[136:139], v[184:187], v[104:107]
	v_mfma_f32_16x16x32_bf16 v[100:103], v[144:147], v[184:187], v[100:103]
	v_mfma_f32_16x16x32_bf16 v[88:91], v[136:139], v[176:179], v[88:91]
	v_mfma_f32_16x16x32_bf16 v[84:87], v[144:147], v[176:179], v[84:87]
	v_mfma_f32_16x16x32_bf16 v[72:75], v[136:139], v[168:171], v[72:75]
	v_mfma_f32_16x16x32_bf16 v[68:71], v[144:147], v[168:171], v[68:71]
.LBB0_1628:
	s_add_u32 s56, s60, 0xfffe0080
	s_addc_u32 s57, s61, -1
	s_cmp_eq_u32 s67, 4
	s_cselect_b32 s65, s47, s57
	s_cselect_b32 s64, s46, s56
	s_cselect_b32 s63, s49, s66
	s_cselect_b32 s62, s48, s55
	s_barrier
	s_mov_b32 m0, s16
	v_lshl_add_u64 v[2:3], s[62:63], 0, v[200:201]
	s_add_u32 s56, s62, 0x20000
	s_waitcnt lgkmcnt(0)
	ds_read_b128 v[188:191], v225 offset:16384
	ds_read_b128 v[192:195], v225 offset:17408
	ds_read_b128 v[180:183], v225 offset:18432
	ds_read_b128 v[184:187], v225 offset:19456
	ds_read_b128 v[172:175], v225 offset:20480
	ds_read_b128 v[176:179], v225 offset:21504
	ds_read_b128 v[164:167], v225 offset:22528
	ds_read_b128 v[168:171], v225 offset:23552
	global_load_lds_dwordx4 v[2:3], off
	v_lshl_add_u64 v[210:211], s[62:63], 0, v[196:197]
	s_mov_b32 m0, s17
	s_addc_u32 s57, s63, 0
	global_load_lds_dwordx4 v[210:211], off
	v_lshl_add_u64 v[212:213], s[56:57], 0, v[200:201]
	s_mov_b32 m0, s18
	v_lshl_add_u64 v[214:215], s[64:65], 0, v[198:199]
	global_load_lds_dwordx4 v[212:213], off
	v_lshl_add_u64 v[212:213], s[56:57], 0, v[196:197]
	s_mov_b32 m0, s19
	v_cndmask_b32_e64 v0, 0, 1, s[52:53]
	global_load_lds_dwordx4 v[212:213], off
	v_lshl_add_u64 v[212:213], s[64:65], 0, v[202:203]
	s_mov_b32 m0, s15
	v_cmp_ne_u32_e64 s[56:57], 1, v0
	global_load_lds_dwordx4 v[212:213], off
	s_mov_b32 m0, s20
	s_andn2_b64 vcc, exec, s[52:53]
	global_load_lds_dwordx4 v[214:215], off
	s_waitcnt vmcnt(8)
	s_waitcnt lgkmcnt(0)
	s_barrier
	s_cbranch_vccnz .LBB0_1630
; #define PG8_STAGE(bufoff, gbase, voff) do { _Pragma("unroll") for (int _i = 0; _i < 2; ++_i) \
;         __builtin_amdgcn_global_load_lds((const unsigned*)((const char*)(gbase) + (voff)[_i]), (LAS unsigned*)(lds + (bufoff) + ldsw + _i * 8192), 16, 0, 0); } while (0)
; #define PG8_STAGE_A(bufoff, h, kp, nx) do { if constexpr (GATHER) { const unsigned _p = (nx) ? ng[h] : cg[h]; unsigned _v[2]; _v[0] = (_p & 0xffffu) * lda + CA2[0]; _v[1] = (_p >> 16) * lda + CA2[1]; PG8_STAGE(bufoff, kp, _v); } \
;         else { PG8_STAGE(bufoff, (kp) + (h) * hstepA, voffA); } } while (0)
; #define PG8_LDA(dst, b, h) do { _Pragma("unroll") for (int m = 0; m < 4; ++m) _Pragma("unroll") for (int k = 0; k < 2; ++k) dst[m][k] = *(const LAS bf16x8*)(lds + PG8_SA(b, h) + aoff + m * 2048 + k * 1024); } while (0)
; #define PG8_LDB(dst, b, h) do { _Pragma("unroll") for (int n = 0; n < 2; ++n) _Pragma("unroll") for (int k = 0; k < 2; ++k) dst[n][k] = *(const LAS bf16x8*)(lds + PG8_SB(b, h) + boff + n * 2048 + k * 1024); } while (0)
; #define PG8_MMA(ai, bj, At, Bt) do { __builtin_amdgcn_s_setprio(1); _Pragma("unroll") for (int m = 0; m < 4; ++m) _Pragma("unroll") for (int n = 0; n < 2; ++n) _Pragma("unroll") for (int k = 0; k < 2; ++k) \
;         acc[ai][bj][m][n] = __builtin_amdgcn_mfma_f32_16x16x32_bf16(Bt[n][k], At[m][k], acc[ai][bj][m][n], 0, 0, 0); __builtin_amdgcn_s_setprio(0); } while (0)
; #define PG8_WAIT_V(n) asm volatile("s_waitcnt vmcnt(" #n ")" ::: "memory")
; #define PG8_WAIT_L(n) asm volatile("s_waitcnt lgkmcnt(" #n ")" ::: "memory")
; #define PG8_BAR __builtin_amdgcn_s_barrier()
; #define PG8_SCHED __builtin_amdgcn_sched_barrier(0)
;     ...
;             PG8_WAIT_V(8); PG8_WAIT_L(0); PG8_BAR; if (cur.amask & 2) { PG8_MMA(1, 0, At, B0); PG8_MMA(1, 1, At, B1); } PG8_BAR; PG8_SCHED;
;             PG8_LDB(B0, 1, 0); PG8_LDB(B1, 1, 1); PG8_SCHED; PG8_LDA(At, 1, 0); PG8_STAGE_A(PG8_SA(0, 1), 1, a2, last);
;             PG8_WAIT_V(8); PG8_WAIT_L(0); PG8_BAR; if (cur.amask & 1) { PG8_MMA(0, 0, At, B0); PG8_MMA(0, 1, At, B1); } PG8_BAR; PG8_SCHED;
;             PG8_LDA(At, 1, 1); PG8_STAGE(PG8_SB(1, 0), b3, voffB); PG8_STAGE(PG8_SB(1, 1), b3 + hstepB, voffB); PG8_STAGE_A(PG8_SA(1, 0), 0, a3, last);
;             PG8_WAIT_V(8); PG8_WAIT_L(0); PG8_BAR; if (cur.amask & 2) { PG8_MMA(1, 0, At, B0); PG8_MMA(1, 1, At, B1); } PG8_BAR; PG8_SCHED;
	s_waitcnt lgkmcnt(0)
	v_mfma_f32_16x16x32_bf16 v[64:67], v[148:151], v[188:191], v[64:67]
	v_mfma_f32_16x16x32_bf16 v[60:63], v[156:159], v[188:191], v[60:63]
	v_mfma_f32_16x16x32_bf16 v[48:51], v[148:151], v[180:183], v[48:51]
	v_mfma_f32_16x16x32_bf16 v[44:47], v[156:159], v[180:183], v[44:47]
	v_mfma_f32_16x16x32_bf16 v[32:35], v[148:151], v[172:175], v[32:35]
	v_mfma_f32_16x16x32_bf16 v[28:31], v[156:159], v[172:175], v[28:31]
	v_mfma_f32_16x16x32_bf16 v[16:19], v[148:151], v[164:167], v[16:19]
	v_mfma_f32_16x16x32_bf16 v[12:15], v[156:159], v[164:167], v[12:15]
	v_mfma_f32_16x16x32_bf16 v[64:67], v[152:155], v[192:195], v[64:67]
	v_mfma_f32_16x16x32_bf16 v[60:63], v[160:163], v[192:195], v[60:63]
	v_mfma_f32_16x16x32_bf16 v[48:51], v[152:155], v[184:187], v[48:51]
	v_mfma_f32_16x16x32_bf16 v[44:47], v[160:163], v[184:187], v[44:47]
	v_mfma_f32_16x16x32_bf16 v[32:35], v[152:155], v[176:179], v[32:35]
	v_mfma_f32_16x16x32_bf16 v[28:31], v[160:163], v[176:179], v[28:31]
	v_mfma_f32_16x16x32_bf16 v[16:19], v[152:155], v[168:171], v[16:19]
	v_mfma_f32_16x16x32_bf16 v[12:15], v[160:163], v[168:171], v[12:15]
	v_mfma_f32_16x16x32_bf16 v[56:59], v[132:135], v[188:191], v[56:59]
	v_mfma_f32_16x16x32_bf16 v[52:55], v[140:143], v[188:191], v[52:55]
	v_mfma_f32_16x16x32_bf16 v[40:43], v[132:135], v[180:183], v[40:43]
	v_mfma_f32_16x16x32_bf16 v[36:39], v[140:143], v[180:183], v[36:39]
	v_mfma_f32_16x16x32_bf16 v[24:27], v[132:135], v[172:175], v[24:27]
	v_mfma_f32_16x16x32_bf16 v[20:23], v[140:143], v[172:175], v[20:23]
	v_mfma_f32_16x16x32_bf16 v[8:11], v[132:135], v[164:167], v[8:11]
	v_mfma_f32_16x16x32_bf16 v[4:7], v[140:143], v[164:167], v[4:7]
	v_mfma_f32_16x16x32_bf16 v[56:59], v[136:139], v[192:195], v[56:59]
	v_mfma_f32_16x16x32_bf16 v[52:55], v[144:147], v[192:195], v[52:55]
	v_mfma_f32_16x16x32_bf16 v[40:43], v[136:139], v[184:187], v[40:43]
	v_mfma_f32_16x16x32_bf16 v[36:39], v[144:147], v[184:187], v[36:39]
	v_mfma_f32_16x16x32_bf16 v[24:27], v[136:139], v[176:179], v[24:27]
	v_mfma_f32_16x16x32_bf16 v[20:23], v[144:147], v[176:179], v[20:23]
	v_mfma_f32_16x16x32_bf16 v[8:11], v[136:139], v[168:171], v[8:11]
	v_mfma_f32_16x16x32_bf16 v[4:7], v[144:147], v[168:171], v[4:7]
.LBB0_1630:
	s_barrier
	v_add_u32_e32 v0, 0x18000, v224
	ds_read_b128 v[148:151], v0
	ds_read_b128 v[152:155], v0 offset:1024
	ds_read_b128 v[156:159], v0 offset:2048
	ds_read_b128 v[160:163], v0 offset:3072
	v_add_u32_e32 v0, 0x1c000, v224
	ds_read_b128 v[132:135], v0
	ds_read_b128 v[136:139], v0 offset:1024
	ds_read_b128 v[140:143], v0 offset:2048
	ds_read_b128 v[144:147], v0 offset:3072
	s_add_u32 s64, s64, 0x20000
	s_addc_u32 s65, s65, 0
	s_mov_b32 m0, s21
	v_lshl_add_u64 v[226:227], s[64:65], 0, v[202:203]
	s_waitcnt lgkmcnt(0)
	ds_read_b128 v[188:191], v225 offset:32768
	ds_read_b128 v[192:195], v225 offset:33792
	ds_read_b128 v[180:183], v225 offset:34816
	ds_read_b128 v[184:187], v225 offset:35840
	ds_read_b128 v[172:175], v225 offset:36864
	ds_read_b128 v[176:179], v225 offset:37888
	ds_read_b128 v[164:167], v225 offset:38912
	ds_read_b128 v[168:171], v225 offset:39936
	global_load_lds_dwordx4 v[226:227], off
	v_lshl_add_u64 v[226:227], s[64:65], 0, v[198:199]
	s_mov_b32 m0, s22
	s_and_b64 vcc, exec, s[58:59]
	global_load_lds_dwordx4 v[226:227], off
	s_waitcnt vmcnt(8)
	s_waitcnt lgkmcnt(0)
	s_barrier
	s_cbranch_vccnz .LBB0_1632
	s_waitcnt lgkmcnt(0)
	v_mfma_f32_16x16x32_bf16 v[128:131], v[148:151], v[188:191], v[128:131]
	v_mfma_f32_16x16x32_bf16 v[124:127], v[156:159], v[188:191], v[124:127]
	v_mfma_f32_16x16x32_bf16 v[112:115], v[148:151], v[180:183], v[112:115]
	v_mfma_f32_16x16x32_bf16 v[108:111], v[156:159], v[180:183], v[108:111]
	v_mfma_f32_16x16x32_bf16 v[96:99], v[148:151], v[172:175], v[96:99]
	v_mfma_f32_16x16x32_bf16 v[92:95], v[156:159], v[172:175], v[92:95]
	v_mfma_f32_16x16x32_bf16 v[80:83], v[148:151], v[164:167], v[80:83]
	v_mfma_f32_16x16x32_bf16 v[76:79], v[156:159], v[164:167], v[76:79]
	v_mfma_f32_16x16x32_bf16 v[128:131], v[152:155], v[192:195], v[128:131]
	v_mfma_f32_16x16x32_bf16 v[124:127], v[160:163], v[192:195], v[124:127]
	v_mfma_f32_16x16x32_bf16 v[112:115], v[152:155], v[184:187], v[112:115]
	v_mfma_f32_16x16x32_bf16 v[108:111], v[160:163], v[184:187], v[108:111]
	v_mfma_f32_16x16x32_bf16 v[96:99], v[152:155], v[176:179], v[96:99]
	v_mfma_f32_16x16x32_bf16 v[92:95], v[160:163], v[176:179], v[92:95]
	v_mfma_f32_16x16x32_bf16 v[80:83], v[152:155], v[168:171], v[80:83]
	v_mfma_f32_16x16x32_bf16 v[76:79], v[160:163], v[168:171], v[76:79]
	v_mfma_f32_16x16x32_bf16 v[120:123], v[132:135], v[188:191], v[120:123]
	v_mfma_f32_16x16x32_bf16 v[116:119], v[140:143], v[188:191], v[116:119]
	v_mfma_f32_16x16x32_bf16 v[104:107], v[132:135], v[180:183], v[104:107]
	v_mfma_f32_16x16x32_bf16 v[100:103], v[140:143], v[180:183], v[100:103]
	v_mfma_f32_16x16x32_bf16 v[88:91], v[132:135], v[172:175], v[88:91]
	v_mfma_f32_16x16x32_bf16 v[84:87], v[140:143], v[172:175], v[84:87]
	v_mfma_f32_16x16x32_bf16 v[72:75], v[132:135], v[164:167], v[72:75]
	v_mfma_f32_16x16x32_bf16 v[68:71], v[140:143], v[164:167], v[68:71]
	v_mfma_f32_16x16x32_bf16 v[120:123], v[136:139], v[192:195], v[120:123]
	v_mfma_f32_16x16x32_bf16 v[116:119], v[144:147], v[192:195], v[116:119]
	v_mfma_f32_16x16x32_bf16 v[104:107], v[136:139], v[184:187], v[104:107]
	v_mfma_f32_16x16x32_bf16 v[100:103], v[144:147], v[184:187], v[100:103]
	v_mfma_f32_16x16x32_bf16 v[88:91], v[136:139], v[176:179], v[88:91]
	v_mfma_f32_16x16x32_bf16 v[84:87], v[144:147], v[176:179], v[84:87]
	v_mfma_f32_16x16x32_bf16 v[72:75], v[136:139], v[168:171], v[72:75]
	v_mfma_f32_16x16x32_bf16 v[68:71], v[144:147], v[168:171], v[68:71]
; #define PG8_STAGE(bufoff, gbase, voff) do { _Pragma("unroll") for (int _i = 0; _i < 2; ++_i) \
;         __builtin_amdgcn_global_load_lds((const unsigned*)((const char*)(gbase) + (voff)[_i]), (LAS unsigned*)(lds + (bufoff) + ldsw + _i * 8192), 16, 0, 0); } while (0)
; #define PG8_STAGE_A(bufoff, h, kp, nx) do { if constexpr (GATHER) { const unsigned _p = (nx) ? ng[h] : cg[h]; unsigned _v[2]; _v[0] = (_p & 0xffffu) * lda + CA2[0]; _v[1] = (_p >> 16) * lda + CA2[1]; PG8_STAGE(bufoff, kp, _v); } \
;         else { PG8_STAGE(bufoff, (kp) + (h) * hstepA, voffA); } } while (0)
; #define PG8_LDA(dst, b, h) do { _Pragma("unroll") for (int m = 0; m < 4; ++m) _Pragma("unroll") for (int k = 0; k < 2; ++k) dst[m][k] = *(const LAS bf16x8*)(lds + PG8_SA(b, h) + aoff + m * 2048 + k * 1024); } while (0)
; #define PG8_MMA(ai, bj, At, Bt) do { __builtin_amdgcn_s_setprio(1); _Pragma("unroll") for (int m = 0; m < 4; ++m) _Pragma("unroll") for (int n = 0; n < 2; ++n) _Pragma("unroll") for (int k = 0; k < 2; ++k) \
;         acc[ai][bj][m][n] = __builtin_amdgcn_mfma_f32_16x16x32_bf16(Bt[n][k], At[m][k], acc[ai][bj][m][n], 0, 0, 0); __builtin_amdgcn_s_setprio(0); } while (0)
; #define PG8_WAIT_V(n) asm volatile("s_waitcnt vmcnt(" #n ")" ::: "memory")
; #define PG8_WAIT_L(n) asm volatile("s_waitcnt lgkmcnt(" #n ")" ::: "memory")
; #define PG8_BAR __builtin_amdgcn_s_barrier()
; #define PG8_SCHED __builtin_amdgcn_sched_barrier(0)
;     ...
;             PG8_LDA(At, 1, 1); PG8_STAGE(PG8_SB(1, 0), b3, voffB); PG8_STAGE(PG8_SB(1, 1), b3 + hstepB, voffB); PG8_STAGE_A(PG8_SA(1, 0), 0, a3, last);
;             PG8_WAIT_V(8); PG8_WAIT_L(0); PG8_BAR; if (cur.amask & 2) { PG8_MMA(1, 0, At, B0); PG8_MMA(1, 1, At, B1); } PG8_BAR; PG8_SCHED;
;         }
.LBB0_1632:
	s_barrier
	s_mov_b32 m0, s26
	v_lshl_add_u64 v[2:3], v[2:3], 0, s[92:93]
	s_add_u32 s62, s62, 0x20080
	s_waitcnt lgkmcnt(0)
	ds_read_b128 v[188:191], v225 offset:49152
	ds_read_b128 v[192:195], v225 offset:50176
	ds_read_b128 v[180:183], v225 offset:51200
	ds_read_b128 v[184:187], v225 offset:52224
	ds_read_b128 v[172:175], v225 offset:53248
	ds_read_b128 v[176:179], v225 offset:54272
	ds_read_b128 v[164:167], v225 offset:55296
	ds_read_b128 v[168:171], v225 offset:56320
	global_load_lds_dwordx4 v[2:3], off
	v_lshl_add_u64 v[2:3], v[210:211], 0, s[92:93]
	s_mov_b32 m0, s27
	s_addc_u32 s63, s63, 0
	global_load_lds_dwordx4 v[2:3], off
	v_lshl_add_u64 v[2:3], s[62:63], 0, v[200:201]
	s_mov_b32 m0, s30
	s_and_b64 vcc, exec, s[56:57]
	global_load_lds_dwordx4 v[2:3], off
	v_lshl_add_u64 v[2:3], s[62:63], 0, v[196:197]
	s_mov_b32 m0, s31
	s_nop 0
	global_load_lds_dwordx4 v[2:3], off
	v_lshl_add_u64 v[2:3], v[212:213], 0, s[92:93]
	s_mov_b32 m0, s28
	s_nop 0
	global_load_lds_dwordx4 v[2:3], off
	v_lshl_add_u64 v[2:3], v[214:215], 0, s[92:93]
	s_mov_b32 m0, s29
	s_nop 0
	global_load_lds_dwordx4 v[2:3], off
	s_waitcnt vmcnt(8)
	s_waitcnt lgkmcnt(0)
	s_barrier
	s_cbranch_vccnz .LBB0_1625
	s_waitcnt lgkmcnt(0)
	v_mfma_f32_16x16x32_bf16 v[64:67], v[148:151], v[188:191], v[64:67]
	v_mfma_f32_16x16x32_bf16 v[60:63], v[156:159], v[188:191], v[60:63]
	v_mfma_f32_16x16x32_bf16 v[48:51], v[148:151], v[180:183], v[48:51]
	v_mfma_f32_16x16x32_bf16 v[44:47], v[156:159], v[180:183], v[44:47]
	v_mfma_f32_16x16x32_bf16 v[32:35], v[148:151], v[172:175], v[32:35]
	v_mfma_f32_16x16x32_bf16 v[28:31], v[156:159], v[172:175], v[28:31]
	v_mfma_f32_16x16x32_bf16 v[16:19], v[148:151], v[164:167], v[16:19]
	v_mfma_f32_16x16x32_bf16 v[12:15], v[156:159], v[164:167], v[12:15]
	v_mfma_f32_16x16x32_bf16 v[64:67], v[152:155], v[192:195], v[64:67]
	v_mfma_f32_16x16x32_bf16 v[60:63], v[160:163], v[192:195], v[60:63]
	v_mfma_f32_16x16x32_bf16 v[48:51], v[152:155], v[184:187], v[48:51]
	v_mfma_f32_16x16x32_bf16 v[44:47], v[160:163], v[184:187], v[44:47]
	v_mfma_f32_16x16x32_bf16 v[32:35], v[152:155], v[176:179], v[32:35]
	v_mfma_f32_16x16x32_bf16 v[28:31], v[160:163], v[176:179], v[28:31]
	v_mfma_f32_16x16x32_bf16 v[16:19], v[152:155], v[168:171], v[16:19]
	v_mfma_f32_16x16x32_bf16 v[12:15], v[160:163], v[168:171], v[12:15]
	v_mfma_f32_16x16x32_bf16 v[56:59], v[132:135], v[188:191], v[56:59]
	v_mfma_f32_16x16x32_bf16 v[52:55], v[140:143], v[188:191], v[52:55]
	v_mfma_f32_16x16x32_bf16 v[40:43], v[132:135], v[180:183], v[40:43]
	v_mfma_f32_16x16x32_bf16 v[36:39], v[140:143], v[180:183], v[36:39]
	v_mfma_f32_16x16x32_bf16 v[24:27], v[132:135], v[172:175], v[24:27]
	v_mfma_f32_16x16x32_bf16 v[20:23], v[140:143], v[172:175], v[20:23]
	v_mfma_f32_16x16x32_bf16 v[8:11], v[132:135], v[164:167], v[8:11]
	v_mfma_f32_16x16x32_bf16 v[2:5], v[140:143], v[164:167], v[4:7]
	v_mfma_f32_16x16x32_bf16 v[56:59], v[136:139], v[192:195], v[56:59]
	v_mfma_f32_16x16x32_bf16 v[52:55], v[144:147], v[192:195], v[52:55]
	v_mfma_f32_16x16x32_bf16 v[40:43], v[136:139], v[184:187], v[40:43]
	v_mfma_f32_16x16x32_bf16 v[36:39], v[144:147], v[184:187], v[36:39]
	v_mfma_f32_16x16x32_bf16 v[24:27], v[136:139], v[176:179], v[24:27]
	v_mfma_f32_16x16x32_bf16 v[20:23], v[144:147], v[176:179], v[20:23]
	v_mfma_f32_16x16x32_bf16 v[8:11], v[136:139], v[168:171], v[8:11]
	v_mfma_f32_16x16x32_bf16 v[4:7], v[144:147], v[168:171], v[2:5]
	s_branch .LBB0_1625
